# PEER u-sweep: workgroup barrier per column slice (keeps the CU's waves on one slice: L2 reuse) + loop-invariant gather offsets hoisted out of the slice loop
# speedup vs baseline: 1.0531x; 1.0266x over previous
; __device__ __forceinline__ float bflo(unsigned u) { return __uint_as_float(u << 16); }
; __device__ __forceinline__ float bfhi(unsigned u) { return __uint_as_float(u & 0xffff0000u); }
; __device__ __forceinline__ void peer_expert_phase(const Args& a, int layer, LAS unsigned char* lds, int G, int bid) {
;     ...
;         for (int i = 0; i < 4; ++i) { int tok = tb + i * NGW; const bool ok = tok < NTOK; tok = ok ? tok : tb; ea[i] = ok ? IDX[(size_t)tok * 128 + lane] : 0; eb[i] = ok ? IDX[(size_t)tok * 128 + 64 + lane] : 0;
; #pragma unroll
;             for (int c = 0; c < 16; ++c) pacc[i][c] = 0;
;             const u32x4* xr = (const u32x4*)(XN + (size_t)tok * DM) + lane; u32x4 xv[8]; float am = 0.f;
; #pragma unroll
;             for (int j = 0; j < 8; ++j) { xv[j] = xr[64 * j];
;                 am = fmaxf(am, fmaxf(fmaxf(fmaxf(fabsf(bflo(xv[j].x)), fabsf(bfhi(xv[j].x))), fmaxf(fabsf(bflo(xv[j].y)), fabsf(bfhi(xv[j].y)))), fmaxf(fmaxf(fabsf(bflo(xv[j].z)), fabsf(bfhi(xv[j].z))), fmaxf(fabsf(bflo(xv[j].w)), fabsf(bfhi(xv[j].w)))))); }
;             am = wave_max(am); const float qs = am > 0.f ? 127.0f / am : 0.f; xs[i] = am * (1.0f / 127.0f);
.LBB0_1205:
	v_lshl_add_u64 v[70:71], v[12:13], 0, s[62:63]
	global_load_dwordx4 v[32:35], v[70:71], off
	global_load_dwordx4 v[58:61], v[70:71], off offset:1024
	global_load_dwordx4 v[62:65], v[70:71], off offset:2048
	global_load_dwordx4 v[66:69], v[70:71], off offset:3072
	v_add_co_u32_e32 v82, vcc, s81, v70
	s_mov_b32 s50, 0
	s_nop 0
	v_addc_co_u32_e32 v83, vcc, 0, v71, vcc
	global_load_dwordx4 v[70:73], v[82:83], off
	global_load_dwordx4 v[74:77], v[82:83], off offset:1024
	global_load_dwordx4 v[78:81], v[82:83], off offset:2048
	s_nop 0
	global_load_dwordx4 v[82:85], v[82:83], off offset:3072
	v_mov_b32_e32 v120, 0
	s_waitcnt vmcnt(7)
	v_lshlrev_b32_e32 v9, 16, v32
	v_and_b32_e32 v25, 0xffff0000, v32
	v_lshlrev_b32_e32 v27, 16, v33
	v_and_b32_e32 v29, 0xffff0000, v33
	v_lshlrev_b32_e32 v57, 16, v35
	v_and_b32_e32 v35, 0xffff0000, v35
	s_waitcnt vmcnt(6)
	v_lshlrev_b32_e32 v89, 16, v61
	v_and_b32_e32 v61, 0xffff0000, v61
	v_lshlrev_b32_e32 v86, 16, v58
	v_and_b32_e32 v58, 0xffff0000, v58
	v_lshlrev_b32_e32 v87, 16, v59
	v_and_b32_e32 v59, 0xffff0000, v59
	v_max_f32_e64 v31, |v25|, |v25|
	v_max_f32_e64 v32, |v9|, |v9|
	v_max_f32_e64 v98, |v29|, |v29|
	v_max_f32_e64 v99, |v27|, |v27|
	v_max_f32_e64 v100, |v35|, |v35|
	v_max_f32_e64 v101, |v57|, |v57|
	v_max_f32_e64 v106, |v61|, |v61|
	v_max_f32_e64 v107, |v89|, |v89|
	v_lshlrev_b32_e32 v33, 16, v34
	v_and_b32_e32 v34, 0xffff0000, v34
	v_lshlrev_b32_e32 v88, 16, v60
	v_and_b32_e32 v60, 0xffff0000, v60
	v_max_f32_e64 v102, |v58|, |v58|
	v_max_f32_e64 v103, |v86|, |v86|
	v_max_f32_e64 v104, |v59|, |v59|
	v_max_f32_e64 v105, |v87|, |v87|
	v_max_f32_e32 v31, v32, v31
	v_max_f32_e32 v32, v99, v98
	v_max_f32_e32 v98, v101, v100
	v_max_f32_e32 v101, v107, v106
	s_waitcnt vmcnt(5)
	v_lshlrev_b32_e32 v93, 16, v65
	v_and_b32_e32 v65, 0xffff0000, v65
	s_waitcnt vmcnt(4)
	v_lshlrev_b32_e32 v97, 16, v69
	v_and_b32_e32 v69, 0xffff0000, v69
	v_max_f32_e32 v99, v103, v102
	v_max_f32_e32 v100, v105, v104
	v_max3_f32 v98, |v33|, |v34|, v98
	v_max3_f32 v101, |v88|, |v60|, v101
	v_lshlrev_b32_e32 v90, 16, v62
	v_and_b32_e32 v62, 0xffff0000, v62
	v_lshlrev_b32_e32 v91, 16, v63
	v_and_b32_e32 v63, 0xffff0000, v63
	v_lshlrev_b32_e32 v94, 16, v66
	v_and_b32_e32 v66, 0xffff0000, v66
	v_lshlrev_b32_e32 v95, 16, v67
	v_and_b32_e32 v67, 0xffff0000, v67
	v_max_f32_e64 v112, |v65|, |v65|
	v_max_f32_e64 v113, |v93|, |v93|
	v_max_f32_e64 v118, |v69|, |v69|
	v_max_f32_e64 v119, |v97|, |v97|
	v_max3_f32 v31, v31, v32, v98
	v_max3_f32 v32, v99, v100, v101
	v_lshlrev_b32_e32 v92, 16, v64
	v_and_b32_e32 v64, 0xffff0000, v64
	v_lshlrev_b32_e32 v96, 16, v68
	v_and_b32_e32 v68, 0xffff0000, v68
	v_max_f32_e64 v108, |v62|, |v62|
	v_max_f32_e64 v109, |v90|, |v90|
	v_max_f32_e64 v110, |v63|, |v63|
	v_max_f32_e64 v111, |v91|, |v91|
	v_max_f32_e64 v114, |v66|, |v66|
	v_max_f32_e64 v115, |v94|, |v94|
	v_max_f32_e64 v116, |v67|, |v67|
	v_max_f32_e64 v117, |v95|, |v95|
	v_max_f32_e32 v104, v113, v112
	v_max3_f32 v31, v31, 0, v32
	v_max_f32_e32 v32, v119, v118
	v_max_f32_e32 v102, v109, v108
	v_max_f32_e32 v103, v111, v110
	v_max_f32_e32 v105, v115, v114
	v_max_f32_e32 v106, v117, v116
	v_max3_f32 v104, |v92|, |v64|, v104
	v_max3_f32 v32, |v96|, |v68|, v32
	v_max3_f32 v98, v102, v103, v104
	v_max3_f32 v32, v105, v106, v32
	v_max3_f32 v31, v31, v98, v32
	s_waitcnt vmcnt(3)
	v_lshlrev_b32_e32 v98, 16, v70
	v_and_b32_e32 v70, 0xffff0000, v70
	v_max_f32_e64 v32, |v70|, |v70|
	v_max_f32_e64 v99, |v98|, |v98|
	v_max_f32_e32 v32, v99, v32
	v_lshlrev_b32_e32 v99, 16, v71
	v_and_b32_e32 v71, 0xffff0000, v71
	v_lshlrev_b32_e32 v102, 16, v73
	v_and_b32_e32 v73, 0xffff0000, v73
	v_max_f32_e64 v100, |v71|, |v71|
	v_max_f32_e64 v101, |v99|, |v99|
	v_max_f32_e64 v103, |v73|, |v73|
	v_max_f32_e64 v104, |v102|, |v102|
	v_max_f32_e32 v100, v101, v100
	v_lshlrev_b32_e32 v101, 16, v72
	v_and_b32_e32 v72, 0xffff0000, v72
	v_max_f32_e32 v103, v104, v103
	v_max3_f32 v103, |v101|, |v72|, v103
	v_max3_f32 v32, v32, v100, v103
	s_waitcnt vmcnt(2)
	v_lshlrev_b32_e32 v100, 16, v74
	v_and_b32_e32 v74, 0xffff0000, v74
	v_max_f32_e64 v103, |v74|, |v74|
	v_max_f32_e64 v104, |v100|, |v100|
	v_max_f32_e32 v103, v104, v103
	v_lshlrev_b32_e32 v104, 16, v75
	v_and_b32_e32 v75, 0xffff0000, v75
	v_lshlrev_b32_e32 v107, 16, v77
	v_and_b32_e32 v77, 0xffff0000, v77
	v_max_f32_e64 v105, |v75|, |v75|
	v_max_f32_e64 v106, |v104|, |v104|
	v_max_f32_e64 v108, |v77|, |v77|
	v_max_f32_e64 v109, |v107|, |v107|
	v_max_f32_e32 v105, v106, v105
	v_lshlrev_b32_e32 v106, 16, v76
	v_and_b32_e32 v76, 0xffff0000, v76
	v_max_f32_e32 v108, v109, v108
	v_max3_f32 v108, |v106|, |v76|, v108
	v_max3_f32 v103, v103, v105, v108
	v_max3_f32 v31, v31, v32, v103
	s_waitcnt vmcnt(1)
	v_lshlrev_b32_e32 v103, 16, v78
	v_and_b32_e32 v78, 0xffff0000, v78
	v_max_f32_e64 v32, |v78|, |v78|
	v_max_f32_e64 v105, |v103|, |v103|
	v_max_f32_e32 v32, v105, v32
	v_lshlrev_b32_e32 v105, 16, v79
	v_and_b32_e32 v79, 0xffff0000, v79
	v_lshlrev_b32_e32 v110, 16, v81
	v_and_b32_e32 v81, 0xffff0000, v81
	v_max_f32_e64 v108, |v79|, |v79|
	v_max_f32_e64 v109, |v105|, |v105|
	v_max_f32_e64 v111, |v81|, |v81|
	v_max_f32_e64 v112, |v110|, |v110|
	v_max_f32_e32 v108, v109, v108
	v_lshlrev_b32_e32 v109, 16, v80
	v_and_b32_e32 v80, 0xffff0000, v80
	v_max_f32_e32 v111, v112, v111
	v_max3_f32 v111, |v109|, |v80|, v111
	v_max3_f32 v32, v32, v108, v111
	s_waitcnt vmcnt(0)
; #define LAS __attribute__((address_space(3)))
; __device__ __forceinline__ float bflo(unsigned u) { return __uint_as_float(u << 16); }
; __device__ __forceinline__ float bfhi(unsigned u) { return __uint_as_float(u & 0xffff0000u); }
; __device__ __forceinline__ void peer_expert_phase(const Args& a, int layer, LAS unsigned char* lds, int G, int bid) {
;     ...
;             am = wave_max(am); const float qs = am > 0.f ? 127.0f / am : 0.f; xs[i] = am * (1.0f / 127.0f);
; #pragma unroll
;             for (int j = 0; j < 8; ++j) { u32x2 o; o.x = pk_i8(bflo(xv[j].x) * qs, bfhi(xv[j].x) * qs, bflo(xv[j].y) * qs, bfhi(xv[j].y) * qs); o.y = pk_i8(bflo(xv[j].z) * qs, bfhi(xv[j].z) * qs, bflo(xv[j].w) * qs, bfhi(xv[j].w) * qs);
;                 *(LAS u32x2*)(X8 + i * 4096 + 8 * (lane + 64 * j)) = o; } }
	v_lshlrev_b32_e32 v108, 16, v82
	v_and_b32_e32 v82, 0xffff0000, v82
	v_max_f32_e64 v111, |v82|, |v82|
	v_max_f32_e64 v112, |v108|, |v108|
	v_max_f32_e32 v111, v112, v111
	v_lshlrev_b32_e32 v112, 16, v83
	v_and_b32_e32 v83, 0xffff0000, v83
	v_lshlrev_b32_e32 v115, 16, v85
	v_and_b32_e32 v85, 0xffff0000, v85
	v_max_f32_e64 v113, |v83|, |v83|
	v_max_f32_e64 v114, |v112|, |v112|
	v_max_f32_e64 v116, |v85|, |v85|
	v_max_f32_e64 v117, |v115|, |v115|
	v_max_f32_e32 v113, v114, v113
	v_lshlrev_b32_e32 v114, 16, v84
	v_and_b32_e32 v84, 0xffff0000, v84
	v_max_f32_e32 v116, v117, v116
	v_max3_f32 v116, |v114|, |v84|, v116
	v_max3_f32 v111, v111, v113, v116
	v_max3_f32 v31, v31, v32, v111
	ds_bpermute_b32 v32, v36, v31
	v_mov_b32_e32 v118, 0
	v_mov_b32_e32 v119, 0
	s_waitcnt lgkmcnt(0)
	v_max_f32_e32 v32, v32, v32
	v_max_f32_e32 v31, v31, v32
	ds_bpermute_b32 v32, v37, v31
	s_waitcnt lgkmcnt(0)
	v_max_f32_e32 v32, v32, v32
	v_max_f32_e32 v31, v31, v32
	ds_bpermute_b32 v32, v38, v31
	s_waitcnt lgkmcnt(0)
	v_max_f32_e32 v32, v32, v32
	v_max_f32_e32 v31, v31, v32
	ds_bpermute_b32 v32, v39, v31
	s_waitcnt lgkmcnt(0)
	v_max_f32_e32 v32, v32, v32
	v_max_f32_e32 v31, v31, v32
	ds_bpermute_b32 v32, v40, v31
	s_waitcnt lgkmcnt(0)
	v_max_f32_e32 v32, v32, v32
	v_max_f32_e32 v31, v31, v32
	ds_bpermute_b32 v32, v41, v31
	s_waitcnt lgkmcnt(0)
	v_max_f32_e32 v32, v32, v32
	v_max_f32_e32 v31, v31, v32
	v_div_scale_f32 v32, s[34:35], v31, v31, s82
	v_rcp_f32_e32 v111, v32
	s_nop 0
	v_fma_f32 v113, -v32, v111, 1.0
	v_fmac_f32_e32 v111, v113, v111
	v_div_scale_f32 v113, vcc, s82, v31, s82
	v_mul_f32_e32 v116, v113, v111
	v_fma_f32 v117, -v32, v116, v113
	v_fmac_f32_e32 v116, v117, v111
	v_fma_f32 v32, -v32, v116, v113
	v_div_fmas_f32 v32, v32, v111, v116
	v_div_fixup_f32 v32, v32, v31, s82
	v_cmp_lt_f32_e32 vcc, 0, v31
	v_mov_b32_e32 v113, 0
	v_mov_b32_e32 v116, 0
	v_cndmask_b32_e32 v111, 0, v32, vcc
	v_fmaak_f32 v9, v111, v9, 0x4b400000
	v_fmaak_f32 v25, v111, v25, 0x4b400000
	v_fmaak_f32 v27, v111, v27, 0x4b400000
	v_fmaak_f32 v29, v111, v29, 0x4b400000
	v_perm_b32 v27, v29, v27, s83
	v_perm_b32 v9, v25, v9, s83
	v_perm_b32 v32, v27, v9, s84
	v_fmaak_f32 v9, v111, v33, 0x4b400000
	v_fmaak_f32 v25, v111, v34, 0x4b400000
	v_fmaak_f32 v27, v111, v57, 0x4b400000
	v_fmaak_f32 v29, v111, v35, 0x4b400000
	v_perm_b32 v27, v29, v27, s83
	v_perm_b32 v9, v25, v9, s83
	v_perm_b32 v33, v27, v9, s84
	v_fmaak_f32 v9, v111, v86, 0x4b400000
	v_fmaak_f32 v25, v111, v58, 0x4b400000
	v_fmaak_f32 v27, v111, v87, 0x4b400000
	v_fmaak_f32 v29, v111, v59, 0x4b400000
	v_perm_b32 v27, v29, v27, s83
	v_perm_b32 v9, v25, v9, s83
	v_perm_b32 v34, v27, v9, s84
	v_fmaak_f32 v9, v111, v88, 0x4b400000
	v_fmaak_f32 v25, v111, v60, 0x4b400000
	v_fmaak_f32 v27, v111, v89, 0x4b400000
	v_fmaak_f32 v29, v111, v61, 0x4b400000
	v_perm_b32 v27, v29, v27, s83
	v_perm_b32 v9, v25, v9, s83
	v_perm_b32 v35, v27, v9, s84
	v_fmaak_f32 v9, v111, v90, 0x4b400000
	v_fmaak_f32 v25, v111, v62, 0x4b400000
	v_fmaak_f32 v27, v111, v91, 0x4b400000
	v_fmaak_f32 v29, v111, v63, 0x4b400000
	v_perm_b32 v27, v29, v27, s83
	v_perm_b32 v9, v25, v9, s83
	ds_write2st64_b64 v55, v[32:33], v[34:35] offset0:24 offset1:25
	v_perm_b32 v32, v27, v9, s84
	v_fmaak_f32 v9, v111, v92, 0x4b400000
	v_fmaak_f32 v25, v111, v64, 0x4b400000
	v_fmaak_f32 v27, v111, v93, 0x4b400000
	v_fmaak_f32 v29, v111, v65, 0x4b400000
	v_perm_b32 v27, v29, v27, s83
	v_perm_b32 v9, v25, v9, s83
	v_perm_b32 v33, v27, v9, s84
	v_fmaak_f32 v9, v111, v94, 0x4b400000
	v_fmaak_f32 v25, v111, v66, 0x4b400000
	v_fmaak_f32 v27, v111, v95, 0x4b400000
	v_fmaak_f32 v29, v111, v67, 0x4b400000
	v_perm_b32 v27, v29, v27, s83
	v_perm_b32 v9, v25, v9, s83
	v_perm_b32 v34, v27, v9, s84
	v_fmaak_f32 v9, v111, v96, 0x4b400000
	v_fmaak_f32 v25, v111, v68, 0x4b400000
	v_fmaak_f32 v27, v111, v97, 0x4b400000
	v_fmaak_f32 v29, v111, v69, 0x4b400000
	v_perm_b32 v27, v29, v27, s83
	v_perm_b32 v9, v25, v9, s83
	v_perm_b32 v35, v27, v9, s84
	v_fmaak_f32 v9, v111, v98, 0x4b400000
	v_fmaak_f32 v25, v111, v70, 0x4b400000
	v_fmaak_f32 v27, v111, v99, 0x4b400000
	v_fmaak_f32 v29, v111, v71, 0x4b400000
	v_perm_b32 v27, v29, v27, s83
	v_perm_b32 v9, v25, v9, s83
	ds_write2st64_b64 v55, v[32:33], v[34:35] offset0:26 offset1:27
	v_perm_b32 v32, v27, v9, s84
	v_fmaak_f32 v9, v111, v101, 0x4b400000
	v_fmaak_f32 v25, v111, v72, 0x4b400000
	v_fmaak_f32 v27, v111, v102, 0x4b400000
	v_fmaak_f32 v29, v111, v73, 0x4b400000
	v_perm_b32 v27, v29, v27, s83
	v_perm_b32 v9, v25, v9, s83
	v_perm_b32 v33, v27, v9, s84
	v_fmaak_f32 v9, v111, v100, 0x4b400000
	v_fmaak_f32 v25, v111, v74, 0x4b400000
	v_fmaak_f32 v27, v111, v104, 0x4b400000
	v_fmaak_f32 v29, v111, v75, 0x4b400000
	v_perm_b32 v27, v29, v27, s83
	v_perm_b32 v9, v25, v9, s83
	v_perm_b32 v34, v27, v9, s84
	v_fmaak_f32 v9, v111, v106, 0x4b400000
	v_fmaak_f32 v25, v111, v76, 0x4b400000
	v_fmaak_f32 v27, v111, v107, 0x4b400000
	v_fmaak_f32 v29, v111, v77, 0x4b400000
	v_perm_b32 v27, v29, v27, s83
	v_perm_b32 v9, v25, v9, s83
	v_perm_b32 v35, v27, v9, s84
	v_fmaak_f32 v9, v111, v103, 0x4b400000
	v_fmaak_f32 v25, v111, v78, 0x4b400000
	v_fmaak_f32 v27, v111, v105, 0x4b400000
	v_fmaak_f32 v29, v111, v79, 0x4b400000
	v_perm_b32 v27, v29, v27, s83
	v_perm_b32 v9, v25, v9, s83
	ds_write2st64_b64 v55, v[32:33], v[34:35] offset0:28 offset1:29
	v_perm_b32 v32, v27, v9, s84
	v_fmaak_f32 v9, v111, v109, 0x4b400000
	v_fmaak_f32 v25, v111, v80, 0x4b400000
	v_fmaak_f32 v27, v111, v110, 0x4b400000
	v_fmaak_f32 v29, v111, v81, 0x4b400000
	v_perm_b32 v27, v29, v27, s83
	v_perm_b32 v9, v25, v9, s83
	v_perm_b32 v33, v27, v9, s84
	v_fmaak_f32 v9, v111, v108, 0x4b400000
; #define LAS __attribute__((address_space(3)))
; __device__ __forceinline__ void peer_expert_phase(const Args& a, int layer, LAS unsigned char* lds, int G, int bid) {
;     ...
;             for (int c = 0; c < 16; ++c) pacc[i][c] = 0;
;     ...
;         for (int i = 0; i < 4; ++i) { eoa[i] = (unsigned)ea[i] << 12; eob[i] = (unsigned)eb[i] << 12; }
;         const unsigned lo16 = 16u * (unsigned)l7;
; #pragma unroll 1
;         for (int sidx = 0; sidx < 32; ++sidx) { const int s = (sidx + srot) & 31; const unsigned char* pus = PU + s * 128;
; #pragma unroll
;             for (int i = 0; i < 4; ++i) {
;                 int tok = tb + i * NGW; tok = tok < NTOK ? tok : tb;
;                 const u32x4 xq = *(const LAS u32x4*)(X8 + i * 4096 + s * 128 + 16 * l7);
;                 u32x4 r[16];
; #pragma unroll
;                 for (int c = 0; c < 16; ++c) { const unsigned eo = (unsigned)__shfl((int)(c < 8 ? eoa[i] : eob[i]), (8 * c + g8) & 63); r[c] = *(const u32x4*)(pus + (eo + lo16)); }
	v_fmaak_f32 v25, v111, v82, 0x4b400000
	v_fmaak_f32 v27, v111, v112, 0x4b400000
	v_fmaak_f32 v29, v111, v83, 0x4b400000
	v_perm_b32 v27, v29, v27, s83
	v_perm_b32 v9, v25, v9, s83
	v_perm_b32 v34, v27, v9, s84
	v_fmaak_f32 v9, v111, v114, 0x4b400000
	v_fmaak_f32 v25, v111, v84, 0x4b400000
	v_fmaak_f32 v27, v111, v115, 0x4b400000
	v_fmaak_f32 v29, v111, v85, 0x4b400000
	v_perm_b32 v27, v29, v27, s83
	v_perm_b32 v9, v25, v9, s83
	v_perm_b32 v35, v27, v9, s84
	ds_write2st64_b64 v55, v[32:33], v[34:35] offset0:30 offset1:31
	v_lshlrev_b32_e32 v57, 12, v24
	v_lshlrev_b32_e32 v58, 12, v4
	v_lshlrev_b32_e32 v59, 12, v8
	v_lshlrev_b32_e32 v60, 12, v2
	v_lshlrev_b32_e32 v61, 12, v28
	v_lshlrev_b32_e32 v62, 12, v26
	v_lshlrev_b32_e32 v63, 12, v6
	v_lshlrev_b32_e32 v64, 12, v30
	v_mov_b32_e32 v93, 0
	v_mov_b32_e32 v96, 0
	v_mov_b32_e32 v97, 0
	v_mov_b32_e32 v98, 0
	v_mov_b32_e32 v99, 0
	v_mov_b32_e32 v100, 0
	v_mov_b32_e32 v101, 0
	v_mov_b32_e32 v102, 0
	v_mov_b32_e32 v103, 0
	v_mov_b32_e32 v104, 0
	v_mov_b32_e32 v105, 0
	v_mov_b32_e32 v106, 0
	v_mov_b32_e32 v107, 0
	v_mov_b32_e32 v108, 0
	v_mov_b32_e32 v109, 0
	v_mov_b32_e32 v110, 0
	v_mov_b32_e32 v111, 0
	v_mov_b32_e32 v32, 0
	v_mov_b32_e32 v112, 0
	v_mov_b32_e32 v114, 0
	v_mov_b32_e32 v115, 0
	v_mov_b32_e32 v117, 0
	v_mov_b32_e32 v33, 0
	v_mov_b32_e32 v95, 0
	v_mov_b32_e32 v94, 0
	v_mov_b32_e32 v92, 0
	v_mov_b32_e32 v91, 0
	v_mov_b32_e32 v90, 0
	v_mov_b32_e32 v89, 0
	v_mov_b32_e32 v88, 0
	v_mov_b32_e32 v87, 0
	v_mov_b32_e32 v86, 0
	v_mov_b32_e32 v85, 0
	v_mov_b32_e32 v84, 0
	v_mov_b32_e32 v83, 0
	v_mov_b32_e32 v82, 0
	v_mov_b32_e32 v81, 0
	v_mov_b32_e32 v80, 0
	v_mov_b32_e32 v79, 0
	v_mov_b32_e32 v78, 0
	v_mov_b32_e32 v77, 0
	v_mov_b32_e32 v76, 0
	v_mov_b32_e32 v75, 0
	v_mov_b32_e32 v74, 0
	v_mov_b32_e32 v73, 0
	v_mov_b32_e32 v72, 0
	v_mov_b32_e32 v71, 0
	v_mov_b32_e32 v70, 0
	v_mov_b32_e32 v69, 0
	v_mov_b32_e32 v68, 0
	v_mov_b32_e32 v67, 0
	v_mov_b32_e32 v66, 0
	v_mov_b32_e32 v65, 0
	v_mov_b32_e32 v35, 0
	v_mov_b32_e32 v34, 0
	v_mov_b32_e32 v25, 0
	v_mov_b32_e32 v29, 0
	v_mov_b32_e32 v27, 0
	v_mov_b32_e32 v9, 0
	ds_bpermute_b32 v190, v10, v57
	ds_bpermute_b32 v191, v45, v57
	ds_bpermute_b32 v192, v46, v57
	ds_bpermute_b32 v193, v47, v57
	ds_bpermute_b32 v194, v48, v57
	ds_bpermute_b32 v195, v49, v57
	ds_bpermute_b32 v196, v50, v57
	ds_bpermute_b32 v197, v51, v57
	s_waitcnt lgkmcnt(7)
	v_add_u32_e32 v190, v190, v42
	s_waitcnt lgkmcnt(6)
	v_add_u32_e32 v191, v191, v42
	s_waitcnt lgkmcnt(5)
	v_add_u32_e32 v192, v192, v42
	s_waitcnt lgkmcnt(4)
	v_add_u32_e32 v193, v193, v42
	s_waitcnt lgkmcnt(3)
	v_add_u32_e32 v194, v194, v42
	s_waitcnt lgkmcnt(2)
	v_add_u32_e32 v195, v195, v42
	s_waitcnt lgkmcnt(1)
	v_add_u32_e32 v196, v196, v42
	s_waitcnt lgkmcnt(0)
	v_add_u32_e32 v197, v197, v42
	ds_bpermute_b32 v198, v10, v58
	ds_bpermute_b32 v199, v46, v58
	ds_bpermute_b32 v200, v48, v58
	ds_bpermute_b32 v201, v45, v58
	ds_bpermute_b32 v202, v50, v58
	ds_bpermute_b32 v203, v47, v58
	ds_bpermute_b32 v204, v49, v58
	ds_bpermute_b32 v205, v51, v58
	s_waitcnt lgkmcnt(7)
	v_add_u32_e32 v198, v198, v42
	s_waitcnt lgkmcnt(6)
	v_add_u32_e32 v199, v199, v42
	s_waitcnt lgkmcnt(5)
	v_add_u32_e32 v200, v200, v42
	s_waitcnt lgkmcnt(4)
	v_add_u32_e32 v201, v201, v42
	s_waitcnt lgkmcnt(3)
	v_add_u32_e32 v202, v202, v42
	s_waitcnt lgkmcnt(2)
	v_add_u32_e32 v203, v203, v42
	s_waitcnt lgkmcnt(1)
	v_add_u32_e32 v204, v204, v42
	s_waitcnt lgkmcnt(0)
	v_add_u32_e32 v205, v205, v42
	ds_bpermute_b32 v206, v10, v59
	ds_bpermute_b32 v207, v45, v59
	ds_bpermute_b32 v208, v46, v59
	ds_bpermute_b32 v209, v47, v59
	ds_bpermute_b32 v210, v48, v59
	ds_bpermute_b32 v211, v49, v59
	ds_bpermute_b32 v212, v50, v59
	ds_bpermute_b32 v213, v51, v59
	s_waitcnt lgkmcnt(7)
	v_add_u32_e32 v206, v206, v42
	s_waitcnt lgkmcnt(6)
	v_add_u32_e32 v207, v207, v42
	s_waitcnt lgkmcnt(5)
	v_add_u32_e32 v208, v208, v42
	s_waitcnt lgkmcnt(4)
	v_add_u32_e32 v209, v209, v42
	s_waitcnt lgkmcnt(3)
	v_add_u32_e32 v210, v210, v42
	s_waitcnt lgkmcnt(2)
	v_add_u32_e32 v211, v211, v42
	s_waitcnt lgkmcnt(1)
	v_add_u32_e32 v212, v212, v42
	s_waitcnt lgkmcnt(0)
	v_add_u32_e32 v213, v213, v42
	ds_bpermute_b32 v214, v10, v60
	ds_bpermute_b32 v215, v45, v60
	ds_bpermute_b32 v216, v46, v60
	ds_bpermute_b32 v217, v47, v60
	ds_bpermute_b32 v218, v48, v60
	ds_bpermute_b32 v219, v49, v60
	ds_bpermute_b32 v220, v50, v60
	ds_bpermute_b32 v221, v51, v60
	s_waitcnt lgkmcnt(7)
	v_add_u32_e32 v214, v214, v42
	s_waitcnt lgkmcnt(6)
	v_add_u32_e32 v215, v215, v42
	s_waitcnt lgkmcnt(5)
	v_add_u32_e32 v216, v216, v42
	s_waitcnt lgkmcnt(4)
	v_add_u32_e32 v217, v217, v42
	s_waitcnt lgkmcnt(3)
	v_add_u32_e32 v218, v218, v42
	s_waitcnt lgkmcnt(2)
	v_add_u32_e32 v219, v219, v42
	s_waitcnt lgkmcnt(1)
	v_add_u32_e32 v220, v220, v42
	s_waitcnt lgkmcnt(0)
	v_add_u32_e32 v221, v221, v42
	ds_bpermute_b32 v222, v10, v61
	ds_bpermute_b32 v223, v45, v61
	ds_bpermute_b32 v224, v46, v61
	ds_bpermute_b32 v225, v47, v61
	ds_bpermute_b32 v226, v48, v61
	ds_bpermute_b32 v227, v49, v61
	ds_bpermute_b32 v229, v50, v61
	ds_bpermute_b32 v230, v51, v61
	s_waitcnt lgkmcnt(7)
	v_add_u32_e32 v222, v222, v42
	s_waitcnt lgkmcnt(6)
	v_add_u32_e32 v223, v223, v42
	s_waitcnt lgkmcnt(5)
	v_add_u32_e32 v224, v224, v42
	s_waitcnt lgkmcnt(4)
	v_add_u32_e32 v225, v225, v42
	s_waitcnt lgkmcnt(3)
	v_add_u32_e32 v226, v226, v42
	s_waitcnt lgkmcnt(2)
	v_add_u32_e32 v227, v227, v42
	s_waitcnt lgkmcnt(1)
	v_add_u32_e32 v229, v229, v42
	s_waitcnt lgkmcnt(0)
	v_add_u32_e32 v230, v230, v42
	ds_bpermute_b32 v231, v10, v62
	ds_bpermute_b32 v232, v45, v62
	ds_bpermute_b32 v233, v46, v62
	ds_bpermute_b32 v234, v47, v62
	ds_bpermute_b32 v235, v48, v62
	ds_bpermute_b32 v236, v49, v62
	ds_bpermute_b32 v237, v50, v62
	ds_bpermute_b32 v238, v51, v62
	s_waitcnt lgkmcnt(7)
; #define LAS __attribute__((address_space(3)))
; __device__ __forceinline__ void peer_expert_phase(const Args& a, int layer, LAS unsigned char* lds, int G, int bid) {
;     ...
;         for (int sidx = 0; sidx < 32; ++sidx) { const int s = (sidx + srot) & 31; const unsigned char* pus = PU + s * 128;
; #pragma unroll
;             for (int i = 0; i < 4; ++i) {
;                 int tok = tb + i * NGW; tok = tok < NTOK ? tok : tb;
;                 const u32x4 xq = *(const LAS u32x4*)(X8 + i * 4096 + s * 128 + 16 * l7);
;                 u32x4 r[16];
; #pragma unroll
;                 for (int c = 0; c < 16; ++c) { const unsigned eo = (unsigned)__shfl((int)(c < 8 ? eoa[i] : eob[i]), (8 * c + g8) & 63); r[c] = *(const u32x4*)(pus + (eo + lo16)); }
; #pragma unroll
;                 for (int c = 0; c < 16; ++c) { int d = pacc[i][c];
; #pragma unroll
;                     for (int q = 0; q < 4; ++q) d = __builtin_amdgcn_sdot4((int)r[c][q], (int)xq[q], d, false);
;                     pacc[i][c] = d; }
	v_add_u32_e32 v231, v231, v42
	s_waitcnt lgkmcnt(6)
	v_add_u32_e32 v232, v232, v42
	s_waitcnt lgkmcnt(5)
	v_add_u32_e32 v233, v233, v42
	s_waitcnt lgkmcnt(4)
	v_add_u32_e32 v234, v234, v42
	s_waitcnt lgkmcnt(3)
	v_add_u32_e32 v235, v235, v42
	s_waitcnt lgkmcnt(2)
	v_add_u32_e32 v236, v236, v42
	s_waitcnt lgkmcnt(1)
	v_add_u32_e32 v237, v237, v42
	s_waitcnt lgkmcnt(0)
	v_add_u32_e32 v238, v238, v42
	ds_bpermute_b32 v239, v10, v63
	ds_bpermute_b32 v240, v45, v63
	ds_bpermute_b32 v241, v46, v63
	ds_bpermute_b32 v242, v47, v63
	ds_bpermute_b32 v243, v48, v63
	ds_bpermute_b32 v244, v49, v63
	ds_bpermute_b32 v245, v50, v63
	ds_bpermute_b32 v246, v51, v63
	s_waitcnt lgkmcnt(7)
	v_add_u32_e32 v239, v239, v42
	s_waitcnt lgkmcnt(6)
	v_add_u32_e32 v240, v240, v42
	s_waitcnt lgkmcnt(5)
	v_add_u32_e32 v241, v241, v42
	s_waitcnt lgkmcnt(4)
	v_add_u32_e32 v242, v242, v42
	s_waitcnt lgkmcnt(3)
	v_add_u32_e32 v243, v243, v42
	s_waitcnt lgkmcnt(2)
	v_add_u32_e32 v244, v244, v42
	s_waitcnt lgkmcnt(1)
	v_add_u32_e32 v245, v245, v42
	s_waitcnt lgkmcnt(0)
	v_add_u32_e32 v246, v246, v42
	ds_bpermute_b32 v247, v10, v64
	ds_bpermute_b32 v248, v45, v64
	ds_bpermute_b32 v249, v46, v64
	ds_bpermute_b32 v250, v47, v64
	ds_bpermute_b32 v251, v48, v64
	ds_bpermute_b32 v252, v49, v64
	ds_bpermute_b32 v253, v50, v64
	ds_bpermute_b32 v254, v51, v64
	s_waitcnt lgkmcnt(7)
	v_add_u32_e32 v247, v247, v42
	s_waitcnt lgkmcnt(6)
	v_add_u32_e32 v248, v248, v42
	s_waitcnt lgkmcnt(5)
	v_add_u32_e32 v249, v249, v42
	s_waitcnt lgkmcnt(4)
	v_add_u32_e32 v250, v250, v42
	s_waitcnt lgkmcnt(3)
	v_add_u32_e32 v251, v251, v42
	s_waitcnt lgkmcnt(2)
	v_add_u32_e32 v252, v252, v42
	s_waitcnt lgkmcnt(1)
	v_add_u32_e32 v253, v253, v42
	s_waitcnt lgkmcnt(0)
	v_add_u32_e32 v254, v254, v42
.LBB0_1206:
	s_barrier
	s_add_i32 s34, s80, s50
	s_and_b32 s34, s34, 0xf80
	s_add_u32 s70, s33, s34
	s_addc_u32 s71, s72, 0
	v_add_u32_e32 v121, s34, v43
	global_load_dwordx4 v[122:125], v190, s[70:71]
	global_load_dwordx4 v[126:129], v191, s[70:71]
	global_load_dwordx4 v[130:133], v192, s[70:71]
	global_load_dwordx4 v[134:137], v193, s[70:71]
	global_load_dwordx4 v[138:141], v194, s[70:71]
	global_load_dwordx4 v[142:145], v195, s[70:71]
	global_load_dwordx4 v[146:149], v196, s[70:71]
	global_load_dwordx4 v[150:153], v197, s[70:71]
	global_load_dwordx4 v[154:157], v198, s[70:71]
	global_load_dwordx4 v[162:165], v199, s[70:71]
	global_load_dwordx4 v[170:173], v200, s[70:71]
	global_load_dwordx4 v[158:161], v201, s[70:71]
	global_load_dwordx4 v[178:181], v202, s[70:71]
	global_load_dwordx4 v[166:169], v203, s[70:71]
	global_load_dwordx4 v[174:177], v204, s[70:71]
	global_load_dwordx4 v[182:185], v205, s[70:71]
	ds_read_b128 v[186:189], v121
	s_waitcnt lgkmcnt(0)
	s_waitcnt vmcnt(15)
	v_dot4c_i32_i8_e32 v120, v122, v186
	s_waitcnt vmcnt(14)
	v_dot4c_i32_i8_e32 v119, v126, v186
	v_dot4c_i32_i8_e32 v120, v123, v187
	s_waitcnt vmcnt(13)
	v_dot4c_i32_i8_e32 v33, v130, v186
	s_waitcnt vmcnt(12)
	v_dot4c_i32_i8_e32 v118, v134, v186
	v_dot4c_i32_i8_e32 v119, v127, v187
	v_dot4c_i32_i8_e32 v33, v131, v187
	v_dot4c_i32_i8_e32 v118, v135, v187
	s_waitcnt vmcnt(11)
	v_dot4c_i32_i8_e32 v117, v138, v186
	s_waitcnt vmcnt(10)
	v_dot4c_i32_i8_e32 v116, v142, v186
	v_dot4c_i32_i8_e32 v117, v139, v187
	v_dot4c_i32_i8_e32 v116, v143, v187
	v_dot4c_i32_i8_e32 v120, v124, v188
	s_waitcnt vmcnt(9)
	v_dot4c_i32_i8_e32 v115, v146, v186
	s_waitcnt vmcnt(8)
	v_dot4c_i32_i8_e32 v114, v150, v186
	v_dot4c_i32_i8_e32 v115, v147, v187
	v_dot4c_i32_i8_e32 v114, v151, v187
	s_waitcnt vmcnt(7)
	v_dot4c_i32_i8_e32 v113, v154, v186
	v_dot4c_i32_i8_e32 v113, v155, v187
	s_waitcnt vmcnt(6)
	v_dot4c_i32_i8_e32 v32, v162, v186
	v_dot4c_i32_i8_e32 v32, v163, v187
	v_dot4c_i32_i8_e32 v119, v128, v188
	v_dot4c_i32_i8_e32 v33, v132, v188
	v_dot4c_i32_i8_e32 v118, v136, v188
	s_waitcnt vmcnt(5)
	v_dot4c_i32_i8_e32 v110, v170, v186
	v_dot4c_i32_i8_e32 v110, v171, v187
	s_waitcnt vmcnt(4)
	v_dot4c_i32_i8_e32 v112, v158, v186
	v_dot4c_i32_i8_e32 v112, v159, v187
	v_dot4c_i32_i8_e32 v117, v140, v188
	s_waitcnt vmcnt(3)
	v_dot4c_i32_i8_e32 v108, v178, v186
	v_dot4c_i32_i8_e32 v108, v179, v187
	v_dot4c_i32_i8_e32 v116, v144, v188
	v_dot4c_i32_i8_e32 v115, v148, v188
	s_waitcnt vmcnt(2)
	v_dot4c_i32_i8_e32 v111, v166, v186
	v_dot4c_i32_i8_e32 v111, v167, v187
	v_dot4c_i32_i8_e32 v114, v152, v188
	v_dot4c_i32_i8_e32 v113, v156, v188
	v_dot4c_i32_i8_e32 v112, v160, v188
	v_dot4c_i32_i8_e32 v32, v164, v188
	v_dot4c_i32_i8_e32 v111, v168, v188
	s_waitcnt vmcnt(1)
	v_dot4c_i32_i8_e32 v109, v174, v186
	v_dot4c_i32_i8_e32 v109, v175, v187
	v_dot4c_i32_i8_e32 v110, v172, v188
	v_dot4c_i32_i8_e32 v109, v176, v188
	v_dot4c_i32_i8_e32 v108, v180, v188
	v_dot4c_i32_i8_e32 v120, v125, v189
	v_dot4c_i32_i8_e32 v119, v129, v189
	s_waitcnt vmcnt(0)
	v_dot4c_i32_i8_e32 v107, v182, v186
	v_dot4c_i32_i8_e32 v107, v183, v187
	v_dot4c_i32_i8_e32 v107, v184, v188
	v_dot4c_i32_i8_e32 v33, v133, v189
	v_dot4c_i32_i8_e32 v118, v137, v189
	v_dot4c_i32_i8_e32 v117, v141, v189
	v_dot4c_i32_i8_e32 v116, v145, v189
	v_dot4c_i32_i8_e32 v115, v149, v189
	v_dot4c_i32_i8_e32 v114, v153, v189
	v_dot4c_i32_i8_e32 v113, v157, v189
	v_dot4c_i32_i8_e32 v112, v161, v189
	v_dot4c_i32_i8_e32 v32, v165, v189
	v_dot4c_i32_i8_e32 v111, v169, v189
	v_dot4c_i32_i8_e32 v110, v173, v189
	v_dot4c_i32_i8_e32 v109, v177, v189
	v_dot4c_i32_i8_e32 v108, v181, v189
	v_dot4c_i32_i8_e32 v107, v185, v189
	global_load_dwordx4 v[122:125], v206, s[70:71]
	global_load_dwordx4 v[126:129], v207, s[70:71]
	global_load_dwordx4 v[130:133], v208, s[70:71]
	global_load_dwordx4 v[134:137], v209, s[70:71]
	global_load_dwordx4 v[138:141], v210, s[70:71]
	global_load_dwordx4 v[142:145], v211, s[70:71]
	global_load_dwordx4 v[146:149], v212, s[70:71]
	global_load_dwordx4 v[150:153], v213, s[70:71]
	global_load_dwordx4 v[154:157], v214, s[70:71]
	global_load_dwordx4 v[158:161], v215, s[70:71]
	global_load_dwordx4 v[162:165], v216, s[70:71]
	global_load_dwordx4 v[166:169], v217, s[70:71]
	global_load_dwordx4 v[170:173], v218, s[70:71]
	global_load_dwordx4 v[174:177], v219, s[70:71]
	global_load_dwordx4 v[178:181], v220, s[70:71]
	global_load_dwordx4 v[182:185], v221, s[70:71]
	ds_read_b128 v[186:189], v121 offset:4096
	s_waitcnt lgkmcnt(0)
; #define LAS __attribute__((address_space(3)))
; __device__ __forceinline__ void peer_expert_phase(const Args& a, int layer, LAS unsigned char* lds, int G, int bid) {
;     ...
;             for (int i = 0; i < 4; ++i) {
;                 int tok = tb + i * NGW; tok = tok < NTOK ? tok : tb;
;                 const u32x4 xq = *(const LAS u32x4*)(X8 + i * 4096 + s * 128 + 16 * l7);
;                 u32x4 r[16];
; #pragma unroll
;                 for (int c = 0; c < 16; ++c) { const unsigned eo = (unsigned)__shfl((int)(c < 8 ? eoa[i] : eob[i]), (8 * c + g8) & 63); r[c] = *(const u32x4*)(pus + (eo + lo16)); }
; #pragma unroll
;                 for (int c = 0; c < 16; ++c) { int d = pacc[i][c];
; #pragma unroll
;                     for (int q = 0; q < 4; ++q) d = __builtin_amdgcn_sdot4((int)r[c][q], (int)xq[q], d, false);
;                     pacc[i][c] = d; }
	s_waitcnt vmcnt(15)
	v_dot4c_i32_i8_e32 v106, v122, v186
	s_waitcnt vmcnt(14)
	v_dot4c_i32_i8_e32 v105, v126, v186
	s_waitcnt vmcnt(13)
	v_dot4c_i32_i8_e32 v104, v130, v186
	s_waitcnt vmcnt(12)
	v_dot4c_i32_i8_e32 v103, v134, v186
	s_waitcnt vmcnt(11)
	v_dot4c_i32_i8_e32 v102, v138, v186
	s_waitcnt vmcnt(10)
	v_dot4c_i32_i8_e32 v101, v142, v186
	s_waitcnt vmcnt(9)
	v_dot4c_i32_i8_e32 v100, v146, v186
	s_waitcnt vmcnt(8)
	v_dot4c_i32_i8_e32 v99, v150, v186
	s_waitcnt vmcnt(7)
	v_dot4c_i32_i8_e32 v98, v154, v186
	s_waitcnt vmcnt(6)
	v_dot4c_i32_i8_e32 v97, v158, v186
	s_waitcnt vmcnt(5)
	v_dot4c_i32_i8_e32 v96, v162, v186
	v_dot4c_i32_i8_e32 v106, v123, v187
	v_dot4c_i32_i8_e32 v105, v127, v187
	v_dot4c_i32_i8_e32 v104, v131, v187
	v_dot4c_i32_i8_e32 v103, v135, v187
	v_dot4c_i32_i8_e32 v102, v139, v187
	v_dot4c_i32_i8_e32 v101, v143, v187
	v_dot4c_i32_i8_e32 v100, v147, v187
	v_dot4c_i32_i8_e32 v99, v151, v187
	v_dot4c_i32_i8_e32 v98, v155, v187
	v_dot4c_i32_i8_e32 v97, v159, v187
	v_dot4c_i32_i8_e32 v96, v163, v187
	v_dot4c_i32_i8_e32 v106, v124, v188
	v_dot4c_i32_i8_e32 v105, v128, v188
	v_dot4c_i32_i8_e32 v104, v132, v188
	v_dot4c_i32_i8_e32 v103, v136, v188
	v_dot4c_i32_i8_e32 v102, v140, v188
	v_dot4c_i32_i8_e32 v101, v144, v188
	v_dot4c_i32_i8_e32 v100, v148, v188
	v_dot4c_i32_i8_e32 v99, v152, v188
	v_dot4c_i32_i8_e32 v98, v156, v188
	v_dot4c_i32_i8_e32 v97, v160, v188
	v_dot4c_i32_i8_e32 v96, v164, v188
	v_dot4c_i32_i8_e32 v106, v125, v189
	v_dot4c_i32_i8_e32 v105, v129, v189
	v_dot4c_i32_i8_e32 v104, v133, v189
	v_dot4c_i32_i8_e32 v103, v137, v189
	v_dot4c_i32_i8_e32 v102, v141, v189
	v_dot4c_i32_i8_e32 v101, v145, v189
	v_dot4c_i32_i8_e32 v100, v149, v189
	v_dot4c_i32_i8_e32 v99, v153, v189
	v_dot4c_i32_i8_e32 v98, v157, v189
	v_dot4c_i32_i8_e32 v97, v161, v189
	v_dot4c_i32_i8_e32 v96, v165, v189
	s_waitcnt vmcnt(4)
	v_dot4c_i32_i8_e32 v93, v166, v186
	v_dot4c_i32_i8_e32 v93, v167, v187
	s_waitcnt vmcnt(3)
	v_dot4c_i32_i8_e32 v95, v170, v186
	v_dot4c_i32_i8_e32 v95, v171, v187
	s_waitcnt vmcnt(2)
	v_dot4c_i32_i8_e32 v94, v174, v186
	v_dot4c_i32_i8_e32 v94, v175, v187
	s_waitcnt vmcnt(1)
	v_dot4c_i32_i8_e32 v92, v178, v186
	v_dot4c_i32_i8_e32 v92, v179, v187
	s_waitcnt vmcnt(0)
	v_dot4c_i32_i8_e32 v91, v182, v186
	v_dot4c_i32_i8_e32 v91, v183, v187
	v_dot4c_i32_i8_e32 v93, v168, v188
	v_dot4c_i32_i8_e32 v95, v172, v188
	v_dot4c_i32_i8_e32 v94, v176, v188
	v_dot4c_i32_i8_e32 v92, v180, v188
	v_dot4c_i32_i8_e32 v91, v184, v188
	v_dot4c_i32_i8_e32 v93, v169, v189
	v_dot4c_i32_i8_e32 v95, v173, v189
	v_dot4c_i32_i8_e32 v94, v177, v189
	v_dot4c_i32_i8_e32 v92, v181, v189
	v_dot4c_i32_i8_e32 v91, v185, v189
	global_load_dwordx4 v[122:125], v222, s[70:71]
	global_load_dwordx4 v[126:129], v223, s[70:71]
	global_load_dwordx4 v[130:133], v224, s[70:71]
	global_load_dwordx4 v[134:137], v225, s[70:71]
	global_load_dwordx4 v[138:141], v226, s[70:71]
	global_load_dwordx4 v[142:145], v227, s[70:71]
	global_load_dwordx4 v[146:149], v229, s[70:71]
	global_load_dwordx4 v[150:153], v230, s[70:71]
	global_load_dwordx4 v[154:157], v231, s[70:71]
	global_load_dwordx4 v[158:161], v232, s[70:71]
	global_load_dwordx4 v[162:165], v233, s[70:71]
	global_load_dwordx4 v[166:169], v234, s[70:71]
	global_load_dwordx4 v[170:173], v235, s[70:71]
	global_load_dwordx4 v[174:177], v236, s[70:71]
	global_load_dwordx4 v[178:181], v237, s[70:71]
	global_load_dwordx4 v[182:185], v238, s[70:71]
	ds_read_b128 v[186:189], v121 offset:8192
	s_waitcnt lgkmcnt(0)
	s_waitcnt vmcnt(15)
	v_dot4c_i32_i8_e32 v90, v122, v186
	s_waitcnt vmcnt(14)
	v_dot4c_i32_i8_e32 v89, v126, v186
	s_waitcnt vmcnt(13)
	v_dot4c_i32_i8_e32 v88, v130, v186
	s_waitcnt vmcnt(12)
	v_dot4c_i32_i8_e32 v87, v134, v186
	s_waitcnt vmcnt(11)
	v_dot4c_i32_i8_e32 v86, v138, v186
	s_waitcnt vmcnt(10)
	v_dot4c_i32_i8_e32 v85, v142, v186
	s_waitcnt vmcnt(9)
	v_dot4c_i32_i8_e32 v84, v146, v186
	s_waitcnt vmcnt(8)
	v_dot4c_i32_i8_e32 v83, v150, v186
	s_waitcnt vmcnt(7)
	v_dot4c_i32_i8_e32 v82, v154, v186
	s_waitcnt vmcnt(6)
	v_dot4c_i32_i8_e32 v81, v158, v186
	s_waitcnt vmcnt(5)
	v_dot4c_i32_i8_e32 v80, v162, v186
	v_dot4c_i32_i8_e32 v90, v123, v187
	v_dot4c_i32_i8_e32 v89, v127, v187
	v_dot4c_i32_i8_e32 v88, v131, v187
	v_dot4c_i32_i8_e32 v87, v135, v187
	v_dot4c_i32_i8_e32 v86, v139, v187
	v_dot4c_i32_i8_e32 v85, v143, v187
	v_dot4c_i32_i8_e32 v84, v147, v187
	v_dot4c_i32_i8_e32 v83, v151, v187
	v_dot4c_i32_i8_e32 v82, v155, v187
	v_dot4c_i32_i8_e32 v81, v159, v187
	v_dot4c_i32_i8_e32 v80, v163, v187
	v_dot4c_i32_i8_e32 v90, v124, v188
	v_dot4c_i32_i8_e32 v89, v128, v188
	v_dot4c_i32_i8_e32 v88, v132, v188
	v_dot4c_i32_i8_e32 v87, v136, v188
	v_dot4c_i32_i8_e32 v86, v140, v188
	v_dot4c_i32_i8_e32 v85, v144, v188
	v_dot4c_i32_i8_e32 v84, v148, v188
	v_dot4c_i32_i8_e32 v83, v152, v188
	v_dot4c_i32_i8_e32 v82, v156, v188
	v_dot4c_i32_i8_e32 v81, v160, v188
	v_dot4c_i32_i8_e32 v80, v164, v188
	v_dot4c_i32_i8_e32 v90, v125, v189
	v_dot4c_i32_i8_e32 v89, v129, v189
	v_dot4c_i32_i8_e32 v88, v133, v189
	v_dot4c_i32_i8_e32 v87, v137, v189
	v_dot4c_i32_i8_e32 v86, v141, v189
	v_dot4c_i32_i8_e32 v85, v145, v189
	v_dot4c_i32_i8_e32 v84, v149, v189
	v_dot4c_i32_i8_e32 v83, v153, v189
	v_dot4c_i32_i8_e32 v82, v157, v189
	v_dot4c_i32_i8_e32 v81, v161, v189
	v_dot4c_i32_i8_e32 v80, v165, v189
	s_waitcnt vmcnt(4)
	v_dot4c_i32_i8_e32 v79, v166, v186
	v_dot4c_i32_i8_e32 v79, v167, v187
	s_waitcnt vmcnt(3)
	v_dot4c_i32_i8_e32 v78, v170, v186
	v_dot4c_i32_i8_e32 v78, v171, v187
	s_waitcnt vmcnt(2)
	v_dot4c_i32_i8_e32 v77, v174, v186
	v_dot4c_i32_i8_e32 v77, v175, v187
	s_waitcnt vmcnt(1)
; #define LAS __attribute__((address_space(3)))
; __device__ __forceinline__ void peer_expert_phase(const Args& a, int layer, LAS unsigned char* lds, int G, int bid) {
;     ...
;             for (int i = 0; i < 4; ++i) {
;                 int tok = tb + i * NGW; tok = tok < NTOK ? tok : tb;
;                 const u32x4 xq = *(const LAS u32x4*)(X8 + i * 4096 + s * 128 + 16 * l7);
;                 u32x4 r[16];
; #pragma unroll
;                 for (int c = 0; c < 16; ++c) { const unsigned eo = (unsigned)__shfl((int)(c < 8 ? eoa[i] : eob[i]), (8 * c + g8) & 63); r[c] = *(const u32x4*)(pus + (eo + lo16)); }
; #pragma unroll
;                 for (int c = 0; c < 16; ++c) { int d = pacc[i][c];
; #pragma unroll
;                     for (int q = 0; q < 4; ++q) d = __builtin_amdgcn_sdot4((int)r[c][q], (int)xq[q], d, false);
;                     pacc[i][c] = d; }
;                 __builtin_amdgcn_sched_barrier(0);
;             }
;         }
;         float pa[4], pb[4];
; #pragma unroll
;         for (int i = 0; i < 4; ++i) { pa[i] = 0.f; pb[i] = 0.f;
; #pragma unroll
;             for (int c = 0; c < 16; ++c) { float v = (float)pacc[i][c]; v += __shfl_xor(v, 1); v += __shfl_xor(v, 2); v += __shfl_xor(v, 4);
;                 const float t = __shfl(v, 8 * (lane & 7));
;                 if (c < 8) pa[i] = (g8 == c) ? t : pa[i]; else pb[i] = (g8 == c - 8) ? t : pb[i]; } }
	v_dot4c_i32_i8_e32 v76, v178, v186
	v_dot4c_i32_i8_e32 v76, v179, v187
	s_waitcnt vmcnt(0)
	v_dot4c_i32_i8_e32 v75, v182, v186
	v_dot4c_i32_i8_e32 v75, v183, v187
	v_dot4c_i32_i8_e32 v79, v168, v188
	v_dot4c_i32_i8_e32 v78, v172, v188
	v_dot4c_i32_i8_e32 v77, v176, v188
	v_dot4c_i32_i8_e32 v76, v180, v188
	v_dot4c_i32_i8_e32 v75, v184, v188
	v_dot4c_i32_i8_e32 v79, v169, v189
	v_dot4c_i32_i8_e32 v78, v173, v189
	v_dot4c_i32_i8_e32 v77, v177, v189
	v_dot4c_i32_i8_e32 v76, v181, v189
	v_dot4c_i32_i8_e32 v75, v185, v189
	global_load_dwordx4 v[122:125], v239, s[70:71]
	global_load_dwordx4 v[126:129], v240, s[70:71]
	global_load_dwordx4 v[130:133], v241, s[70:71]
	global_load_dwordx4 v[134:137], v242, s[70:71]
	global_load_dwordx4 v[138:141], v243, s[70:71]
	global_load_dwordx4 v[142:145], v244, s[70:71]
	global_load_dwordx4 v[146:149], v245, s[70:71]
	global_load_dwordx4 v[150:153], v246, s[70:71]
	global_load_dwordx4 v[154:157], v247, s[70:71]
	global_load_dwordx4 v[158:161], v248, s[70:71]
	global_load_dwordx4 v[162:165], v249, s[70:71]
	global_load_dwordx4 v[166:169], v250, s[70:71]
	global_load_dwordx4 v[170:173], v251, s[70:71]
	global_load_dwordx4 v[174:177], v252, s[70:71]
	global_load_dwordx4 v[178:181], v253, s[70:71]
	global_load_dwordx4 v[182:185], v254, s[70:71]
	ds_read_b128 v[186:189], v121 offset:12288
	s_waitcnt lgkmcnt(0)
	s_waitcnt vmcnt(15)
	v_dot4c_i32_i8_e32 v74, v122, v186
	s_waitcnt vmcnt(14)
	v_dot4c_i32_i8_e32 v73, v126, v186
	s_waitcnt vmcnt(13)
	v_dot4c_i32_i8_e32 v72, v130, v186
	s_waitcnt vmcnt(12)
	v_dot4c_i32_i8_e32 v71, v134, v186
	s_waitcnt vmcnt(11)
	v_dot4c_i32_i8_e32 v70, v138, v186
	s_waitcnt vmcnt(10)
	v_dot4c_i32_i8_e32 v69, v142, v186
	s_waitcnt vmcnt(9)
	v_dot4c_i32_i8_e32 v68, v146, v186
	s_waitcnt vmcnt(8)
	v_dot4c_i32_i8_e32 v67, v150, v186
	s_waitcnt vmcnt(7)
	v_dot4c_i32_i8_e32 v66, v154, v186
	s_waitcnt vmcnt(6)
	v_dot4c_i32_i8_e32 v65, v158, v186
	s_waitcnt vmcnt(5)
	v_dot4c_i32_i8_e32 v35, v162, v186
	v_dot4c_i32_i8_e32 v74, v123, v187
	v_dot4c_i32_i8_e32 v73, v127, v187
	v_dot4c_i32_i8_e32 v72, v131, v187
	v_dot4c_i32_i8_e32 v71, v135, v187
	v_dot4c_i32_i8_e32 v70, v139, v187
	v_dot4c_i32_i8_e32 v69, v143, v187
	v_dot4c_i32_i8_e32 v68, v147, v187
	v_dot4c_i32_i8_e32 v67, v151, v187
	v_dot4c_i32_i8_e32 v66, v155, v187
	v_dot4c_i32_i8_e32 v65, v159, v187
	v_dot4c_i32_i8_e32 v35, v163, v187
	v_dot4c_i32_i8_e32 v74, v124, v188
	v_dot4c_i32_i8_e32 v73, v128, v188
	v_dot4c_i32_i8_e32 v72, v132, v188
	v_dot4c_i32_i8_e32 v71, v136, v188
	v_dot4c_i32_i8_e32 v70, v140, v188
	v_dot4c_i32_i8_e32 v69, v144, v188
	v_dot4c_i32_i8_e32 v68, v148, v188
	v_dot4c_i32_i8_e32 v67, v152, v188
	v_dot4c_i32_i8_e32 v66, v156, v188
	v_dot4c_i32_i8_e32 v65, v160, v188
	v_dot4c_i32_i8_e32 v35, v164, v188
	v_dot4c_i32_i8_e32 v74, v125, v189
	v_dot4c_i32_i8_e32 v73, v129, v189
	v_dot4c_i32_i8_e32 v72, v133, v189
	v_dot4c_i32_i8_e32 v71, v137, v189
	v_dot4c_i32_i8_e32 v70, v141, v189
	v_dot4c_i32_i8_e32 v69, v145, v189
	v_dot4c_i32_i8_e32 v68, v149, v189
	v_dot4c_i32_i8_e32 v67, v153, v189
	v_dot4c_i32_i8_e32 v66, v157, v189
	v_dot4c_i32_i8_e32 v65, v161, v189
	v_dot4c_i32_i8_e32 v35, v165, v189
	s_waitcnt vmcnt(4)
	v_dot4c_i32_i8_e32 v34, v166, v186
	v_dot4c_i32_i8_e32 v34, v167, v187
	s_waitcnt vmcnt(3)
	v_dot4c_i32_i8_e32 v25, v170, v186
	v_dot4c_i32_i8_e32 v25, v171, v187
	s_waitcnt vmcnt(2)
	v_dot4c_i32_i8_e32 v29, v174, v186
	v_dot4c_i32_i8_e32 v29, v175, v187
	s_waitcnt vmcnt(1)
	v_dot4c_i32_i8_e32 v27, v178, v186
	v_dot4c_i32_i8_e32 v27, v179, v187
	s_waitcnt vmcnt(0)
	v_dot4c_i32_i8_e32 v9, v182, v186
	v_dot4c_i32_i8_e32 v9, v183, v187
	v_dot4c_i32_i8_e32 v34, v168, v188
	v_dot4c_i32_i8_e32 v25, v172, v188
	v_dot4c_i32_i8_e32 v29, v176, v188
	v_dot4c_i32_i8_e32 v27, v180, v188
	v_dot4c_i32_i8_e32 v9, v184, v188
	v_dot4c_i32_i8_e32 v34, v169, v189
	v_dot4c_i32_i8_e32 v25, v173, v189
	v_dot4c_i32_i8_e32 v29, v177, v189
	v_dot4c_i32_i8_e32 v27, v181, v189
	v_dot4c_i32_i8_e32 v9, v185, v189
	s_addk_i32 s50, 0x80
	s_cmpk_eq_i32 s50, 0x1000
	s_cbranch_scc0 .LBB0_1206
	v_cvt_f32_i32_e32 v120, v120
	v_cvt_f32_i32_e32 v119, v119
	v_cvt_f32_i32_e32 v123, v33
	v_mul_f32_e32 v33, 0x3c010204, v5
	ds_bpermute_b32 v121, v41, v120
	ds_bpermute_b32 v122, v41, v119
	v_cvt_f32_i32_e32 v5, v118
	ds_bpermute_b32 v118, v41, v123
	v_cvt_f32_i32_e32 v116, v116
	s_waitcnt lgkmcnt(2)
	v_add_f32_e32 v120, v120, v121
	s_waitcnt lgkmcnt(1)
	v_add_f32_e32 v119, v119, v122
	ds_bpermute_b32 v121, v40, v120
	ds_bpermute_b32 v122, v40, v119
	ds_bpermute_b32 v124, v41, v5
	s_waitcnt lgkmcnt(3)
	v_add_f32_e32 v118, v123, v118
	ds_bpermute_b32 v123, v40, v118
	s_waitcnt lgkmcnt(3)
	v_add_f32_e32 v120, v120, v121
	s_waitcnt lgkmcnt(2)
	v_add_f32_e32 v119, v119, v122
	ds_bpermute_b32 v121, v39, v120
	ds_bpermute_b32 v122, v39, v119
	s_waitcnt lgkmcnt(3)
	v_add_f32_e32 v5, v5, v124
	s_waitcnt lgkmcnt(2)
	v_add_f32_e32 v118, v118, v123
	v_cvt_f32_i32_e32 v117, v117
	s_waitcnt lgkmcnt(1)
	v_add_f32_e32 v120, v120, v121
	s_waitcnt lgkmcnt(0)
	v_add_f32_e32 v119, v119, v122
	ds_bpermute_b32 v120, v44, v120
	ds_bpermute_b32 v122, v40, v5
	ds_bpermute_b32 v119, v44, v119
	ds_bpermute_b32 v121, v39, v118
	ds_bpermute_b32 v123, v41, v117
	s_waitcnt lgkmcnt(4)
	v_cndmask_b32_e64 v120, 0, v120, s[10:11]
	s_waitcnt lgkmcnt(3)
	v_add_f32_e32 v5, v5, v122
	s_waitcnt lgkmcnt(2)
	v_cndmask_b32_e64 v119, v120, v119, s[12:13]
	ds_bpermute_b32 v120, v39, v5
	s_waitcnt lgkmcnt(2)
	v_add_f32_e32 v118, v118, v121
	ds_bpermute_b32 v118, v44, v118
	s_waitcnt lgkmcnt(2)
	v_add_f32_e32 v117, v117, v123
	ds_bpermute_b32 v121, v40, v117
	s_waitcnt lgkmcnt(2)
; __device__ __forceinline__ void peer_expert_phase(const Args& a, int layer, LAS unsigned char* lds, int G, int bid) {
;     ...
;         float pa[4], pb[4];
; #pragma unroll
;         for (int i = 0; i < 4; ++i) { pa[i] = 0.f; pb[i] = 0.f;
; #pragma unroll
;             for (int c = 0; c < 16; ++c) { float v = (float)pacc[i][c]; v += __shfl_xor(v, 1); v += __shfl_xor(v, 2); v += __shfl_xor(v, 4);
;                 const float t = __shfl(v, 8 * (lane & 7));
;                 if (c < 8) pa[i] = (g8 == c) ? t : pa[i]; else pb[i] = (g8 == c - 8) ? t : pb[i]; } }
	v_add_f32_e32 v5, v5, v120
	ds_bpermute_b32 v120, v41, v116
	ds_bpermute_b32 v5, v44, v5
	s_waitcnt lgkmcnt(3)
	v_cndmask_b32_e64 v118, v119, v118, s[14:15]
	v_cvt_f32_i32_e32 v114, v114
	s_waitcnt lgkmcnt(2)
	v_add_f32_e32 v117, v117, v121
	s_waitcnt lgkmcnt(1)
	v_add_f32_e32 v116, v116, v120
	ds_bpermute_b32 v120, v40, v116
	s_waitcnt lgkmcnt(1)
	v_cndmask_b32_e64 v5, v118, v5, s[16:17]
	v_cvt_f32_i32_e32 v115, v115
	ds_bpermute_b32 v121, v39, v117
	v_cvt_f32_i32_e32 v113, v113
	s_waitcnt lgkmcnt(1)
	v_add_f32_e32 v116, v116, v120
	ds_bpermute_b32 v118, v39, v116
	ds_bpermute_b32 v119, v41, v115
	s_waitcnt lgkmcnt(2)
	v_add_f32_e32 v117, v117, v121
	ds_bpermute_b32 v117, v44, v117
	v_cvt_f32_i32_e32 v112, v112
	s_waitcnt lgkmcnt(2)
	v_add_f32_e32 v116, v116, v118
	ds_bpermute_b32 v118, v41, v114
	ds_bpermute_b32 v116, v44, v116
	s_waitcnt lgkmcnt(3)
	v_add_f32_e32 v115, v115, v119
	ds_bpermute_b32 v119, v40, v115
	s_waitcnt lgkmcnt(3)
	v_cndmask_b32_e64 v5, v5, v117, s[18:19]
	s_waitcnt lgkmcnt(2)
	v_add_f32_e32 v114, v114, v118
	ds_bpermute_b32 v118, v40, v114
	ds_bpermute_b32 v117, v41, v113
	s_waitcnt lgkmcnt(3)
	v_cndmask_b32_e64 v5, v5, v116, s[20:21]
	s_waitcnt lgkmcnt(2)
	v_add_f32_e32 v115, v115, v119
	ds_bpermute_b32 v119, v39, v115
	s_waitcnt lgkmcnt(2)
	v_add_f32_e32 v114, v114, v118
	ds_bpermute_b32 v116, v39, v114
	s_waitcnt lgkmcnt(2)
	v_add_f32_e32 v113, v113, v117
	ds_bpermute_b32 v117, v40, v113
	s_waitcnt lgkmcnt(2)
	v_add_f32_e32 v115, v115, v119
	ds_bpermute_b32 v115, v44, v115
	s_waitcnt lgkmcnt(2)
	v_add_f32_e32 v114, v114, v116
	ds_bpermute_b32 v116, v41, v112
	v_cvt_f32_i32_e32 v118, v32
	s_waitcnt lgkmcnt(2)
	v_add_f32_e32 v113, v113, v117
	ds_bpermute_b32 v114, v44, v114
	ds_bpermute_b32 v117, v39, v113
	s_waitcnt lgkmcnt(2)
	v_add_f32_e32 v112, v112, v116
	ds_bpermute_b32 v116, v40, v112
	v_cndmask_b32_e64 v5, v5, v115, s[22:23]
	ds_bpermute_b32 v115, v41, v118
	s_waitcnt lgkmcnt(3)
	v_cndmask_b32_e64 v32, v5, v114, s[24:25]
	s_waitcnt lgkmcnt(2)
	v_add_f32_e32 v5, v113, v117
	s_waitcnt lgkmcnt(1)
	v_add_f32_e32 v112, v112, v116
	ds_bpermute_b32 v113, v39, v112
	s_waitcnt lgkmcnt(1)
	v_add_f32_e32 v114, v118, v115
	ds_bpermute_b32 v115, v40, v114
	v_cvt_f32_i32_e32 v116, v111
	ds_bpermute_b32 v111, v44, v5
	s_waitcnt lgkmcnt(2)
	v_add_f32_e32 v5, v112, v113
	v_cvt_f32_i32_e32 v112, v110
	ds_bpermute_b32 v113, v41, v116
	s_waitcnt lgkmcnt(2)
	v_add_f32_e32 v114, v114, v115
	ds_bpermute_b32 v115, v39, v114
	ds_bpermute_b32 v117, v41, v112
	ds_bpermute_b32 v110, v44, v5
	s_waitcnt lgkmcnt(3)
	v_add_f32_e32 v5, v116, v113
	ds_bpermute_b32 v113, v40, v5
	s_waitcnt lgkmcnt(3)
	v_add_f32_e32 v114, v114, v115
	s_waitcnt lgkmcnt(2)
	v_add_f32_e32 v115, v112, v117
	ds_bpermute_b32 v116, v40, v115
	v_cvt_f32_i32_e32 v109, v109
	s_waitcnt lgkmcnt(1)
	v_add_f32_e32 v5, v5, v113
	ds_bpermute_b32 v112, v44, v114
	ds_bpermute_b32 v113, v39, v5
	s_waitcnt lgkmcnt(2)
	v_add_f32_e32 v114, v115, v116
	ds_bpermute_b32 v117, v41, v109
	ds_bpermute_b32 v116, v39, v114
	v_cvt_f32_i32_e32 v108, v108
	s_waitcnt lgkmcnt(2)
	v_add_f32_e32 v5, v5, v113
	ds_bpermute_b32 v115, v44, v5
	s_waitcnt lgkmcnt(2)
	v_add_f32_e32 v109, v109, v117
	ds_bpermute_b32 v113, v41, v108
	s_waitcnt lgkmcnt(2)
	v_add_f32_e32 v5, v114, v116
	ds_bpermute_b32 v114, v40, v109
	v_cvt_f32_i32_e32 v107, v107
	ds_bpermute_b32 v119, v44, v5
	s_waitcnt lgkmcnt(2)
	v_add_f32_e32 v108, v108, v113
	ds_bpermute_b32 v113, v40, v108
	s_waitcnt lgkmcnt(2)
	v_add_f32_e32 v5, v109, v114
	ds_bpermute_b32 v109, v41, v107
	ds_bpermute_b32 v114, v39, v5
	v_cvt_f32_i32_e32 v106, v106
	s_waitcnt lgkmcnt(2)
	v_add_f32_e32 v108, v108, v113
	ds_bpermute_b32 v113, v39, v108
	s_waitcnt lgkmcnt(2)
	v_add_f32_e32 v107, v107, v109
	ds_bpermute_b32 v109, v40, v107
	s_waitcnt lgkmcnt(2)
	v_add_f32_e32 v5, v5, v114
	ds_bpermute_b32 v114, v41, v106
	ds_bpermute_b32 v120, v44, v5
	s_waitcnt lgkmcnt(3)
	v_add_f32_e32 v5, v108, v113
	s_waitcnt lgkmcnt(2)
	v_add_f32_e32 v107, v107, v109
	ds_bpermute_b32 v108, v39, v107
	s_waitcnt lgkmcnt(2)
	v_add_f32_e32 v106, v106, v114
	v_cvt_f32_i32_e32 v105, v105
	ds_bpermute_b32 v109, v40, v106
	v_cvt_f32_i32_e32 v104, v104
	ds_bpermute_b32 v121, v44, v5
	s_waitcnt lgkmcnt(2)
	v_add_f32_e32 v5, v107, v108
	ds_bpermute_b32 v107, v41, v105
	s_waitcnt lgkmcnt(2)
	v_add_f32_e32 v106, v106, v109
	ds_bpermute_b32 v109, v41, v104
	ds_bpermute_b32 v108, v39, v106
	ds_bpermute_b32 v122, v44, v5
	s_waitcnt lgkmcnt(3)
	v_add_f32_e32 v5, v105, v107
	ds_bpermute_b32 v105, v40, v5
	s_waitcnt lgkmcnt(3)
	v_add_f32_e32 v107, v104, v109
	s_waitcnt lgkmcnt(2)
	v_add_f32_e32 v106, v106, v108
	ds_bpermute_b32 v108, v40, v107
	v_cvt_f32_i32_e32 v103, v103
	s_waitcnt lgkmcnt(1)
	v_add_f32_e32 v5, v5, v105
	ds_bpermute_b32 v105, v39, v5
	ds_bpermute_b32 v104, v44, v106
	s_waitcnt lgkmcnt(2)
	v_add_f32_e32 v106, v107, v108
	v_cvt_f32_i32_e32 v107, v102
	ds_bpermute_b32 v109, v41, v103
	ds_bpermute_b32 v108, v39, v106
	s_waitcnt lgkmcnt(3)
	v_add_f32_e32 v5, v5, v105
	ds_bpermute_b32 v105, v41, v107
	ds_bpermute_b32 v102, v44, v5
	s_waitcnt lgkmcnt(3)
	v_add_f32_e32 v103, v103, v109
	s_waitcnt lgkmcnt(2)
	v_add_f32_e32 v5, v106, v108
	ds_bpermute_b32 v106, v40, v103
	s_waitcnt lgkmcnt(2)
	v_add_f32_e32 v105, v107, v105
	v_cvt_f32_i32_e32 v107, v101
	ds_bpermute_b32 v101, v44, v5
	ds_bpermute_b32 v108, v40, v105
	s_waitcnt lgkmcnt(2)
	v_add_f32_e32 v5, v103, v106
	ds_bpermute_b32 v103, v41, v107
	ds_bpermute_b32 v106, v39, v5
	v_cvt_f32_i32_e32 v109, v100
	s_waitcnt lgkmcnt(2)
	v_add_f32_e32 v105, v105, v108
	ds_bpermute_b32 v108, v39, v105
	s_waitcnt lgkmcnt(2)
; __device__ __forceinline__ void peer_expert_phase(const Args& a, int layer, LAS unsigned char* lds, int G, int bid) {
;     ...
;         float pa[4], pb[4];
; #pragma unroll
;         for (int i = 0; i < 4; ++i) { pa[i] = 0.f; pb[i] = 0.f;
; #pragma unroll
;             for (int c = 0; c < 16; ++c) { float v = (float)pacc[i][c]; v += __shfl_xor(v, 1); v += __shfl_xor(v, 2); v += __shfl_xor(v, 4);
;                 const float t = __shfl(v, 8 * (lane & 7));
;                 if (c < 8) pa[i] = (g8 == c) ? t : pa[i]; else pb[i] = (g8 == c - 8) ? t : pb[i]; } }
	v_add_f32_e32 v103, v107, v103
	ds_bpermute_b32 v107, v40, v103
	s_waitcnt lgkmcnt(2)
	v_add_f32_e32 v5, v5, v106
	ds_bpermute_b32 v106, v41, v109
	ds_bpermute_b32 v100, v44, v5
	s_waitcnt lgkmcnt(3)
	v_add_f32_e32 v5, v105, v108
	s_waitcnt lgkmcnt(2)
	v_add_f32_e32 v103, v103, v107
	ds_bpermute_b32 v105, v39, v103
	v_cvt_f32_i32_e32 v108, v99
	s_waitcnt lgkmcnt(2)
	v_add_f32_e32 v106, v109, v106
	ds_bpermute_b32 v107, v40, v106
	ds_bpermute_b32 v99, v44, v5
	s_waitcnt lgkmcnt(2)
	v_add_f32_e32 v5, v103, v105
	v_cvt_f32_i32_e32 v98, v98
	ds_bpermute_b32 v103, v41, v108
	s_waitcnt lgkmcnt(2)
	v_add_f32_e32 v105, v106, v107
	ds_bpermute_b32 v106, v39, v105
	ds_bpermute_b32 v109, v41, v98
	ds_bpermute_b32 v107, v44, v5
	s_waitcnt lgkmcnt(3)
	v_add_f32_e32 v5, v108, v103
	ds_bpermute_b32 v103, v40, v5
	s_waitcnt lgkmcnt(3)
	v_add_f32_e32 v105, v105, v106
	s_waitcnt lgkmcnt(2)
	v_add_f32_e32 v98, v98, v109
	ds_bpermute_b32 v106, v40, v98
	v_cvt_f32_i32_e32 v97, v97
	s_waitcnt lgkmcnt(1)
	v_add_f32_e32 v5, v5, v103
	ds_bpermute_b32 v103, v39, v5
	v_cvt_f32_i32_e32 v96, v96
	s_waitcnt lgkmcnt(1)
	v_add_f32_e32 v98, v98, v106
	ds_bpermute_b32 v106, v41, v97
	ds_bpermute_b32 v109, v44, v105
	ds_bpermute_b32 v105, v39, v98
	s_waitcnt lgkmcnt(3)
	v_add_f32_e32 v5, v5, v103
	ds_bpermute_b32 v103, v41, v96
	s_waitcnt lgkmcnt(3)
	v_add_f32_e32 v97, v97, v106
	ds_bpermute_b32 v113, v44, v5
	s_waitcnt lgkmcnt(2)
	v_add_f32_e32 v5, v98, v105
	ds_bpermute_b32 v98, v40, v97
	s_waitcnt lgkmcnt(2)
	v_add_f32_e32 v96, v96, v103
	v_cvt_f32_i32_e32 v103, v93
	ds_bpermute_b32 v105, v40, v96
	ds_bpermute_b32 v93, v44, v5
	s_waitcnt lgkmcnt(2)
	v_add_f32_e32 v5, v97, v98
	ds_bpermute_b32 v97, v41, v103
	ds_bpermute_b32 v98, v39, v5
	s_waitcnt lgkmcnt(3)
	v_add_f32_e32 v96, v96, v105
	v_cvt_f32_i32_e32 v106, v95
	ds_bpermute_b32 v105, v39, v96
	s_waitcnt lgkmcnt(2)
	v_add_f32_e32 v97, v103, v97
	ds_bpermute_b32 v103, v40, v97
	s_waitcnt lgkmcnt(2)
	v_add_f32_e32 v5, v5, v98
	ds_bpermute_b32 v98, v41, v106
	ds_bpermute_b32 v95, v44, v5
	s_waitcnt lgkmcnt(3)
	v_add_f32_e32 v5, v96, v105
	s_waitcnt lgkmcnt(2)
	v_add_f32_e32 v96, v97, v103
	ds_bpermute_b32 v97, v39, v96
	s_waitcnt lgkmcnt(2)
	v_add_f32_e32 v98, v106, v98
	ds_bpermute_b32 v103, v40, v98
	v_cvt_f32_i32_e32 v105, v94
	ds_bpermute_b32 v94, v44, v5
	s_waitcnt lgkmcnt(2)
	v_add_f32_e32 v5, v96, v97
	v_cvt_f32_i32_e32 v96, v92
	ds_bpermute_b32 v97, v41, v105
	s_waitcnt lgkmcnt(2)
	v_add_f32_e32 v98, v98, v103
	ds_bpermute_b32 v103, v39, v98
	ds_bpermute_b32 v106, v41, v96
	ds_bpermute_b32 v92, v44, v5
	s_waitcnt lgkmcnt(3)
	v_add_f32_e32 v5, v105, v97
	ds_bpermute_b32 v97, v40, v5
	s_waitcnt lgkmcnt(3)
	v_add_f32_e32 v98, v98, v103
	s_waitcnt lgkmcnt(2)
	v_add_f32_e32 v103, v96, v106
	ds_bpermute_b32 v105, v40, v103
	v_cvt_f32_i32_e32 v91, v91
	s_waitcnt lgkmcnt(1)
	v_add_f32_e32 v5, v5, v97
	ds_bpermute_b32 v96, v44, v98
	ds_bpermute_b32 v97, v39, v5
	s_waitcnt lgkmcnt(2)
	v_add_f32_e32 v98, v103, v105
	ds_bpermute_b32 v105, v41, v91
	ds_bpermute_b32 v103, v39, v98
	v_cvt_f32_i32_e32 v90, v90
	s_waitcnt lgkmcnt(2)
	v_add_f32_e32 v5, v5, v97
	ds_bpermute_b32 v108, v44, v5
	s_waitcnt lgkmcnt(2)
	v_add_f32_e32 v91, v91, v105
	ds_bpermute_b32 v97, v41, v90
	s_waitcnt lgkmcnt(2)
	v_add_f32_e32 v5, v98, v103
	ds_bpermute_b32 v98, v40, v91
	v_cvt_f32_i32_e32 v89, v89
	ds_bpermute_b32 v114, v44, v5
	s_waitcnt lgkmcnt(2)
	v_add_f32_e32 v90, v90, v97
	ds_bpermute_b32 v97, v40, v90
	s_waitcnt lgkmcnt(2)
	v_add_f32_e32 v5, v91, v98
	ds_bpermute_b32 v91, v41, v89
	ds_bpermute_b32 v98, v39, v5
	v_cvt_f32_i32_e32 v88, v88
	s_waitcnt lgkmcnt(2)
	v_add_f32_e32 v90, v90, v97
	ds_bpermute_b32 v97, v39, v90
	s_waitcnt lgkmcnt(2)
	v_add_f32_e32 v89, v89, v91
	ds_bpermute_b32 v91, v40, v89
	s_waitcnt lgkmcnt(2)
	v_add_f32_e32 v5, v5, v98
	ds_bpermute_b32 v98, v41, v88
	ds_bpermute_b32 v116, v44, v5
	s_waitcnt lgkmcnt(3)
	v_add_f32_e32 v5, v90, v97
	s_waitcnt lgkmcnt(2)
	v_add_f32_e32 v89, v89, v91
	ds_bpermute_b32 v90, v39, v89
	s_waitcnt lgkmcnt(2)
	v_add_f32_e32 v88, v88, v98
	v_cvt_f32_i32_e32 v97, v87
	ds_bpermute_b32 v91, v40, v88
	ds_bpermute_b32 v87, v44, v5
	s_waitcnt lgkmcnt(2)
	v_add_f32_e32 v5, v89, v90
	v_cvt_f32_i32_e32 v89, v86
	ds_bpermute_b32 v90, v41, v97
	s_waitcnt lgkmcnt(2)
	v_add_f32_e32 v88, v88, v91
	ds_bpermute_b32 v91, v39, v88
	ds_bpermute_b32 v98, v41, v89
	ds_bpermute_b32 v86, v44, v5
	s_waitcnt lgkmcnt(3)
	v_add_f32_e32 v5, v97, v90
	ds_bpermute_b32 v90, v40, v5
	s_waitcnt lgkmcnt(3)
	v_add_f32_e32 v88, v88, v91
	s_waitcnt lgkmcnt(2)
	v_add_f32_e32 v89, v89, v98
	ds_bpermute_b32 v91, v40, v89
	v_cvt_f32_i32_e32 v85, v85
	s_waitcnt lgkmcnt(1)
	v_add_f32_e32 v5, v5, v90
	ds_bpermute_b32 v90, v39, v5
	v_cvt_f32_i32_e32 v80, v80
	s_waitcnt lgkmcnt(1)
	v_add_f32_e32 v89, v89, v91
	v_cvt_f32_i32_e32 v91, v84
	ds_bpermute_b32 v98, v41, v85
	ds_bpermute_b32 v97, v39, v89
	s_waitcnt lgkmcnt(2)
	v_add_f32_e32 v5, v5, v90
	ds_bpermute_b32 v90, v41, v91
	ds_bpermute_b32 v84, v44, v5
	s_waitcnt lgkmcnt(3)
	v_add_f32_e32 v85, v85, v98
	s_waitcnt lgkmcnt(2)
	v_add_f32_e32 v5, v89, v97
	ds_bpermute_b32 v89, v40, v85
	s_waitcnt lgkmcnt(2)
	v_add_f32_e32 v90, v91, v90
	v_cvt_f32_i32_e32 v91, v83
	ds_bpermute_b32 v97, v40, v90
	ds_bpermute_b32 v83, v44, v5
	s_waitcnt lgkmcnt(2)
	v_add_f32_e32 v5, v85, v89
	ds_bpermute_b32 v85, v41, v91
	ds_bpermute_b32 v89, v39, v5
	v_cvt_f32_i32_e32 v98, v82
	s_waitcnt lgkmcnt(3)
	v_add_f32_e32 v90, v90, v97
	ds_bpermute_b32 v97, v39, v90
	s_waitcnt lgkmcnt(2)
	v_add_f32_e32 v85, v91, v85
	ds_bpermute_b32 v91, v40, v85
	s_waitcnt lgkmcnt(2)
; __device__ __forceinline__ void peer_expert_phase(const Args& a, int layer, LAS unsigned char* lds, int G, int bid) {
;     ...
;         float pa[4], pb[4];
; #pragma unroll
;         for (int i = 0; i < 4; ++i) { pa[i] = 0.f; pb[i] = 0.f;
; #pragma unroll
;             for (int c = 0; c < 16; ++c) { float v = (float)pacc[i][c]; v += __shfl_xor(v, 1); v += __shfl_xor(v, 2); v += __shfl_xor(v, 4);
;                 const float t = __shfl(v, 8 * (lane & 7));
;                 if (c < 8) pa[i] = (g8 == c) ? t : pa[i]; else pb[i] = (g8 == c - 8) ? t : pb[i]; } }
;         float wa[4], wb[4], ssq[4], hgm[4] = {0.f, 0.f, 0.f, 0.f};
; #pragma unroll
;         for (int i = 0; i < 4; ++i) { int tok = tb + i * NGW; tok = tok < NTOK ? tok : tb;
;             const float rstd_t = 1.0f / sqrtf(wave_sum(((const float*)(ws + WS_SSP))[((size_t)layer * NTOK + tok) * 64 + lane]) * (1.0f / DM) + EPS);
	v_add_f32_e32 v5, v5, v89
	ds_bpermute_b32 v89, v41, v98
	ds_bpermute_b32 v82, v44, v5
	s_waitcnt lgkmcnt(3)
	v_add_f32_e32 v5, v90, v97
	s_waitcnt lgkmcnt(2)
	v_add_f32_e32 v90, v85, v91
	ds_bpermute_b32 v91, v39, v90
	s_waitcnt lgkmcnt(2)
	v_add_f32_e32 v89, v98, v89
	ds_bpermute_b32 v97, v40, v89
	v_cvt_f32_i32_e32 v98, v81
	ds_bpermute_b32 v85, v44, v5
	s_waitcnt lgkmcnt(2)
	v_add_f32_e32 v5, v90, v91
	ds_bpermute_b32 v81, v44, v5
	ds_bpermute_b32 v90, v41, v98
	s_waitcnt lgkmcnt(3)
	v_add_f32_e32 v89, v89, v97
	ds_bpermute_b32 v91, v39, v89
	ds_bpermute_b32 v97, v41, v80
	v_cvt_f32_i32_e32 v79, v79
	s_waitcnt lgkmcnt(2)
	v_add_f32_e32 v5, v98, v90
	ds_bpermute_b32 v90, v40, v5
	s_waitcnt lgkmcnt(2)
	v_add_f32_e32 v89, v89, v91
	s_waitcnt lgkmcnt(1)
	v_add_f32_e32 v91, v80, v97
	ds_bpermute_b32 v97, v40, v91
	ds_bpermute_b32 v80, v44, v89
	s_waitcnt lgkmcnt(2)
	v_add_f32_e32 v5, v5, v90
	ds_bpermute_b32 v89, v39, v5
	ds_bpermute_b32 v98, v41, v79
	s_waitcnt lgkmcnt(3)
	v_add_f32_e32 v90, v91, v97
	v_cvt_f32_i32_e32 v91, v78
	ds_bpermute_b32 v97, v39, v90
	s_waitcnt lgkmcnt(2)
	v_add_f32_e32 v5, v5, v89
	s_waitcnt lgkmcnt(1)
	v_add_f32_e32 v79, v79, v98
	ds_bpermute_b32 v89, v41, v91
	ds_bpermute_b32 v78, v44, v5
	s_waitcnt lgkmcnt(2)
	v_add_f32_e32 v5, v90, v97
	ds_bpermute_b32 v90, v40, v79
	v_cvt_f32_i32_e32 v98, v76
	s_waitcnt lgkmcnt(2)
	v_add_f32_e32 v89, v91, v89
	v_cvt_f32_i32_e32 v91, v77
	ds_bpermute_b32 v77, v44, v5
	s_waitcnt lgkmcnt(1)
	v_add_f32_e32 v5, v79, v90
	ds_bpermute_b32 v97, v40, v89
	ds_bpermute_b32 v79, v41, v91
	ds_bpermute_b32 v90, v39, v5
	v_cvt_f32_i32_e32 v73, v73
	v_cvt_f32_i32_e32 v72, v72
	s_waitcnt lgkmcnt(2)
	v_add_f32_e32 v89, v89, v97
	s_waitcnt lgkmcnt(1)
	v_add_f32_e32 v79, v91, v79
	ds_bpermute_b32 v91, v40, v79
	ds_bpermute_b32 v97, v39, v89
	s_waitcnt lgkmcnt(2)
	v_add_f32_e32 v5, v5, v90
	ds_bpermute_b32 v90, v41, v98
	ds_bpermute_b32 v76, v44, v5
	s_waitcnt lgkmcnt(3)
	v_add_f32_e32 v79, v79, v91
	s_waitcnt lgkmcnt(2)
	v_add_f32_e32 v5, v89, v97
	ds_bpermute_b32 v89, v39, v79
	v_cvt_f32_i32_e32 v97, v75
	s_waitcnt lgkmcnt(2)
	v_add_f32_e32 v90, v98, v90
	ds_bpermute_b32 v75, v44, v5
	ds_bpermute_b32 v91, v40, v90
	s_waitcnt lgkmcnt(2)
	v_add_f32_e32 v5, v79, v89
	ds_bpermute_b32 v89, v41, v97
	v_cvt_f32_i32_e32 v79, v74
	ds_bpermute_b32 v74, v44, v5
	s_waitcnt lgkmcnt(2)
	v_add_f32_e32 v90, v90, v91
	ds_bpermute_b32 v91, v39, v90
	s_waitcnt lgkmcnt(2)
	v_add_f32_e32 v5, v97, v89
	ds_bpermute_b32 v89, v40, v5
	ds_bpermute_b32 v98, v41, v79
	s_lshl_b64 s[34:35], s[38:39], 8
	s_waitcnt lgkmcnt(2)
	v_add_f32_e32 v90, v90, v91
	v_cvt_f32_i32_e32 v105, v70
	s_waitcnt lgkmcnt(1)
	v_add_f32_e32 v5, v5, v89
	s_waitcnt lgkmcnt(0)
	v_add_f32_e32 v91, v79, v98
	ds_bpermute_b32 v89, v39, v5
	ds_bpermute_b32 v97, v40, v91
	ds_bpermute_b32 v79, v44, v90
	ds_bpermute_b32 v98, v41, v73
	v_cvt_f32_i32_e32 v68, v68
	s_waitcnt lgkmcnt(3)
	v_add_f32_e32 v5, v5, v89
	s_waitcnt lgkmcnt(2)
	v_add_f32_e32 v91, v91, v97
	ds_bpermute_b32 v90, v44, v5
	ds_bpermute_b32 v5, v41, v72
	ds_bpermute_b32 v97, v39, v91
	s_waitcnt lgkmcnt(3)
	v_add_f32_e32 v73, v73, v98
	v_cvt_f32_i32_e32 v67, v67
	v_cvt_f32_i32_e32 v66, v66
	s_waitcnt lgkmcnt(1)
	v_add_f32_e32 v5, v72, v5
	s_waitcnt lgkmcnt(0)
	v_add_f32_e32 v89, v91, v97
	ds_bpermute_b32 v91, v40, v73
	ds_bpermute_b32 v72, v40, v5
	v_cvt_f32_i32_e32 v97, v71
	ds_bpermute_b32 v71, v44, v89
	v_cvt_f32_i32_e32 v65, v65
	s_waitcnt lgkmcnt(2)
	v_add_f32_e32 v91, v73, v91
	s_waitcnt lgkmcnt(1)
	v_add_f32_e32 v5, v5, v72
	v_lshl_add_u64 v[72:73], v[16:17], 0, s[34:35]
	global_load_dword v106, v[72:73], off
	ds_bpermute_b32 v89, v41, v97
	ds_bpermute_b32 v72, v41, v105
	ds_bpermute_b32 v98, v39, v91
	ds_bpermute_b32 v103, v39, v5
	v_cvt_f32_i32_e32 v35, v35
	s_waitcnt lgkmcnt(3)
	v_add_f32_e32 v89, v97, v89
	ds_bpermute_b32 v97, v40, v89
	s_waitcnt lgkmcnt(3)
	v_add_f32_e32 v72, v105, v72
	s_waitcnt lgkmcnt(2)
	v_add_f32_e32 v70, v91, v98
	ds_bpermute_b32 v91, v40, v72
	s_waitcnt lgkmcnt(2)
	v_add_f32_e32 v5, v5, v103
	s_waitcnt lgkmcnt(1)
	v_add_f32_e32 v73, v89, v97
	ds_bpermute_b32 v89, v39, v73
	v_cvt_f32_i32_e32 v97, v69
	ds_bpermute_b32 v69, v44, v5
	s_waitcnt lgkmcnt(2)
	v_add_f32_e32 v72, v72, v91
	ds_bpermute_b32 v98, v41, v68
	s_waitcnt lgkmcnt(2)
	v_add_f32_e32 v5, v73, v89
	ds_bpermute_b32 v73, v41, v97
	ds_bpermute_b32 v91, v39, v72
	ds_bpermute_b32 v89, v44, v5
	s_waitcnt lgkmcnt(3)
	v_add_f32_e32 v68, v68, v98
	ds_bpermute_b32 v98, v41, v67
	s_waitcnt lgkmcnt(3)
	v_add_f32_e32 v5, v97, v73
	ds_bpermute_b32 v97, v40, v5
	s_waitcnt lgkmcnt(3)
	v_add_f32_e32 v72, v72, v91
	ds_bpermute_b32 v91, v40, v68
	ds_bpermute_b32 v73, v44, v72
	s_waitcnt lgkmcnt(3)
	v_add_f32_e32 v67, v67, v98
	s_waitcnt lgkmcnt(2)
	v_add_f32_e32 v5, v5, v97
	ds_bpermute_b32 v72, v39, v5
	s_waitcnt lgkmcnt(2)
	v_add_f32_e32 v68, v68, v91
	ds_bpermute_b32 v91, v39, v68
	v_cvt_f32_i32_e32 v34, v34
	v_lshl_add_u64 v[124:125], v[18:19], 0, s[28:29]
	s_waitcnt lgkmcnt(1)
	v_add_f32_e32 v5, v5, v72
	ds_bpermute_b32 v72, v41, v66
	ds_bpermute_b32 v97, v44, v5
	s_waitcnt lgkmcnt(2)
; __device__ __forceinline__ float gelu_tanh(float x) { const float u = 0.7978845608028654f * (x + 0.044715f * x * x * x); return 0.5f * x * (1.0f + tanhf(u)); }
; __device__ __forceinline__ void peer_expert_phase(const Args& a, int layer, LAS unsigned char* lds, int G, int bid) {
;     ...
;         for (int i = 0; i < 4; ++i) { int tok = tb + i * NGW; tok = tok < NTOK ? tok : tb;
;             const float rstd_t = 1.0f / sqrtf(wave_sum(((const float*)(ws + WS_SSP))[((size_t)layer * NTOK + tok) * 64 + lane]) * (1.0f / DM) + EPS);
;             const float ga = GATE[(size_t)tok * 128 + lane], gb = GATE[(size_t)tok * 128 + 64 + lane];
;             const float rx = rstd_t * xs[i];
;             wa[i] = ga * gelu_tanh(pa[i] * SCU[ea[i]] * rx) * SCV[ea[i]]; wb[i] = gb * gelu_tanh(pb[i] * SCU[eb[i]] * rx) * SCV[eb[i]]; ssq[i] = 0.f; }
	v_add_f32_e32 v5, v68, v91
	ds_bpermute_b32 v68, v40, v67
	ds_bpermute_b32 v103, v44, v5
	s_waitcnt lgkmcnt(3)
	v_add_f32_e32 v66, v66, v72
	ds_bpermute_b32 v72, v40, v66
	v_cvt_f32_i32_e32 v29, v29
	s_waitcnt lgkmcnt(2)
	v_add_f32_e32 v5, v67, v68
	ds_bpermute_b32 v67, v41, v65
	ds_bpermute_b32 v68, v39, v5
	s_waitcnt lgkmcnt(2)
	v_add_f32_e32 v66, v66, v72
	ds_bpermute_b32 v72, v39, v66
	v_cvt_f32_i32_e32 v27, v27
	s_waitcnt lgkmcnt(2)
	v_add_f32_e32 v65, v65, v67
	ds_bpermute_b32 v67, v40, v65
	s_waitcnt lgkmcnt(2)
	v_add_f32_e32 v5, v5, v68
	ds_bpermute_b32 v68, v41, v35
	ds_bpermute_b32 v98, v44, v5
	s_waitcnt lgkmcnt(3)
	v_add_f32_e32 v5, v66, v72
	s_waitcnt lgkmcnt(2)
	v_add_f32_e32 v66, v65, v67
	ds_bpermute_b32 v67, v39, v66
	s_waitcnt lgkmcnt(2)
	v_add_f32_e32 v35, v35, v68
	ds_bpermute_b32 v68, v40, v35
	ds_bpermute_b32 v65, v44, v5
	v_cvt_f32_i32_e32 v9, v9
	s_waitcnt lgkmcnt(2)
	v_add_f32_e32 v5, v66, v67
	ds_bpermute_b32 v67, v41, v34
	ds_bpermute_b32 v66, v44, v5
	s_waitcnt lgkmcnt(3)
	v_add_f32_e32 v5, v35, v68
	v_cvt_f32_i32_e32 v68, v25
	v_ashrrev_i32_e32 v25, 31, v24
	s_waitcnt lgkmcnt(1)
	v_add_f32_e32 v67, v34, v67
	v_lshl_add_u64 v[126:127], v[24:25], 2, s[42:43]
	global_load_dword v34, v[124:125], off
	global_load_dword v35, v[124:125], off offset:256
	s_nop 0
	global_load_dword v124, v[126:127], off
	ds_bpermute_b32 v105, v41, v68
	ds_bpermute_b32 v91, v40, v67
	ds_bpermute_b32 v72, v39, v5
	ds_bpermute_b32 v88, v44, v88
	ds_bpermute_b32 v70, v44, v70
	s_waitcnt lgkmcnt(4)
	v_add_f32_e32 v68, v68, v105
	ds_bpermute_b32 v105, v40, v68
	s_waitcnt lgkmcnt(4)
	v_add_f32_e32 v67, v67, v91
	s_waitcnt vmcnt(3)
	ds_bpermute_b32 v117, v36, v106
	ds_bpermute_b32 v91, v39, v67
	s_waitcnt lgkmcnt(5)
	v_add_f32_e32 v5, v5, v72
	s_waitcnt lgkmcnt(2)
	v_add_f32_e32 v68, v68, v105
	ds_bpermute_b32 v72, v44, v5
	s_waitcnt lgkmcnt(2)
	v_add_f32_e32 v105, v106, v117
	ds_bpermute_b32 v106, v37, v105
	s_waitcnt lgkmcnt(2)
	v_add_f32_e32 v5, v67, v91
	ds_bpermute_b32 v67, v41, v29
	ds_bpermute_b32 v91, v44, v5
	ds_bpermute_b32 v117, v39, v68
	s_waitcnt lgkmcnt(3)
	v_add_f32_e32 v5, v105, v106
	ds_bpermute_b32 v105, v38, v5
	s_waitcnt lgkmcnt(3)
	v_add_f32_e32 v29, v29, v67
	ds_bpermute_b32 v67, v40, v29
	s_waitcnt lgkmcnt(2)
	v_add_f32_e32 v68, v68, v117
	s_waitcnt lgkmcnt(1)
	v_add_f32_e32 v5, v5, v105
	ds_bpermute_b32 v106, v39, v5
	s_waitcnt lgkmcnt(1)
	v_add_f32_e32 v29, v29, v67
	ds_bpermute_b32 v67, v39, v29
	ds_bpermute_b32 v105, v44, v68
	ds_bpermute_b32 v68, v41, v27
	s_waitcnt lgkmcnt(3)
	v_add_f32_e32 v5, v5, v106
	s_waitcnt lgkmcnt(2)
	v_add_f32_e32 v29, v29, v67
	ds_bpermute_b32 v67, v40, v5
	s_waitcnt lgkmcnt(1)
	v_add_f32_e32 v27, v27, v68
	ds_bpermute_b32 v68, v40, v27
	ds_bpermute_b32 v106, v44, v29
	ds_bpermute_b32 v29, v41, v9
	s_waitcnt lgkmcnt(3)
	v_add_f32_e32 v5, v5, v67
	ds_bpermute_b32 v67, v41, v5
	s_waitcnt lgkmcnt(3)
	v_add_f32_e32 v27, v27, v68
	ds_bpermute_b32 v68, v39, v27
	s_waitcnt lgkmcnt(2)
	v_add_f32_e32 v9, v9, v29
	ds_bpermute_b32 v29, v40, v9
	s_waitcnt lgkmcnt(2)
	v_add_f32_e32 v5, v5, v67
	v_fmamk_f32 v5, v5, 0x39800000, v52
	v_mul_f32_e32 v67, 0x4f800000, v5
	v_cmp_gt_f32_e32 vcc, s85, v5
	s_waitcnt lgkmcnt(1)
	v_add_f32_e32 v27, v27, v68
	s_waitcnt lgkmcnt(0)
	v_add_f32_e32 v9, v9, v29
	v_cndmask_b32_e32 v5, v5, v67, vcc
	v_sqrt_f32_e32 v67, v5
	ds_bpermute_b32 v29, v39, v9
	v_add_u32_e32 v68, -1, v67
	v_fma_f32 v117, -v68, v67, v5
	v_cmp_ge_f32_e64 s[28:29], 0, v117
	v_add_u32_e32 v117, 1, v67
	s_waitcnt lgkmcnt(0)
	v_add_f32_e32 v9, v9, v29
	v_cndmask_b32_e64 v68, v67, v68, s[28:29]
	v_fma_f32 v67, -v117, v67, v5
	v_cmp_lt_f32_e64 s[28:29], 0, v67
	ds_bpermute_b32 v118, v44, v9
	s_nop 0
	v_cndmask_b32_e64 v67, v68, v117, s[28:29]
	v_mul_f32_e32 v68, 0x37800000, v67
	v_cndmask_b32_e32 v67, v67, v68, vcc
	v_cmp_class_f32_e32 vcc, v5, v53
	ds_bpermute_b32 v117, v44, v27
	s_nop 0
	v_cndmask_b32_e32 v5, v67, v5, vcc
	v_div_scale_f32 v67, s[28:29], v5, v5, 1.0
	v_rcp_f32_e32 v68, v67
	s_nop 0
	v_fma_f32 v9, -v67, v68, 1.0
	v_fmac_f32_e32 v68, v9, v68
	v_div_scale_f32 v9, vcc, 1.0, v5, 1.0
	v_mul_f32_e32 v27, v9, v68
	v_fma_f32 v29, -v67, v27, v9
	v_fmac_f32_e32 v27, v29, v68
	v_fma_f32 v9, -v67, v27, v9
	v_div_fmas_f32 v9, v9, v68, v27
	v_div_fixup_f32 v125, v9, v5, 1.0
	s_waitcnt vmcnt(0)
	v_pk_mul_f32 v[32:33], v[32:33], v[124:125]
	s_nop 0
	v_mul_f32_e32 v32, v32, v33
	v_mul_f32_e32 v5, 0x3d372713, v32
	v_mul_f32_e32 v5, v32, v5
	v_fma_f32 v5, v32, v5, v32
	v_mul_f32_e32 v67, 0x3f4c422a, v5
	v_cmp_nlt_f32_e64 s[28:29], |v67|, s86
	s_and_saveexec_b64 s[34:35], s[28:29]
	s_xor_b64 s[28:29], exec, s[34:35]
	s_cbranch_execz .LBB0_1209
	v_add_f32_e64 v5, |v67|, |v67|
	v_mul_f32_e32 v9, 0x3fb8aa3b, v5
	v_rndne_f32_e32 v27, v9
	v_sub_f32_e32 v29, v9, v27
	v_fma_f32 v9, v5, s87, -v9
	v_fmac_f32_e32 v9, 0x32a5705f, v5
	v_add_f32_e32 v9, v29, v9
	v_cvt_i32_f32_e32 v27, v27
	v_exp_f32_e32 v9, v9
	v_cmp_ngt_f32_e32 vcc, s88, v5
	v_ldexp_f32 v9, v9, v27
	s_nop 0
	v_cndmask_b32_e32 v9, 0, v9, vcc
	v_cmp_nlt_f32_e32 vcc, s89, v5
	s_nop 1
	v_cndmask_b32_e32 v5, v56, v9, vcc
	v_add_f32_e32 v5, 1.0, v5
	v_rcp_f32_e32 v5, v5
	s_nop 0
	v_fma_f32 v68, v5, -2.0, 1.0

; __device__ __forceinline__ float bflo(unsigned u) { return __uint_as_float(u << 16); }
; __device__ __forceinline__ float bfhi(unsigned u) { return __uint_as_float(u & 0xffff0000u); }
; __device__ __forceinline__ void peer_expert_phase(const Args& a, int layer, LAS unsigned char* lds, int G, int bid) {
;     ...
;         for (int i = 0; i < 4; ++i) { int tok = tb + i * NGW; const bool ok = tok < NTOK; tok = ok ? tok : tb; ea[i] = ok ? IDX[(size_t)tok * 128 + lane] : 0; eb[i] = ok ? IDX[(size_t)tok * 128 + 64 + lane] : 0;
; #pragma unroll
;             for (int c = 0; c < 16; ++c) pacc[i][c] = 0;
;             const u32x4* xr = (const u32x4*)(XN + (size_t)tok * DM) + lane; u32x4 xv[8]; float am = 0.f;
; #pragma unroll
;             for (int j = 0; j < 8; ++j) { xv[j] = xr[64 * j];
;                 am = fmaxf(am, fmaxf(fmaxf(fmaxf(fabsf(bflo(xv[j].x)), fabsf(bfhi(xv[j].x))), fmaxf(fabsf(bflo(xv[j].y)), fabsf(bfhi(xv[j].y)))), fmaxf(fmaxf(fabsf(bflo(xv[j].z)), fabsf(bfhi(xv[j].z))), fmaxf(fabsf(bflo(xv[j].w)), fabsf(bfhi(xv[j].w)))))); }
;             am = wave_max(am); const float qs = am > 0.f ? 127.0f / am : 0.f; xs[i] = am * (1.0f / 127.0f);
.LBB0_2266:
	v_lshl_add_u64 v[26:27], v[8:9], 0, s[52:53]
	global_load_dwordx4 v[52:55], v[26:27], off
	global_load_dwordx4 v[56:59], v[26:27], off offset:1024
	global_load_dwordx4 v[60:63], v[26:27], off offset:2048
	global_load_dwordx4 v[64:67], v[26:27], off offset:3072
	v_add_co_u32_e32 v26, vcc, s68, v26
	s_mov_b32 s40, 0
	s_nop 0
	v_addc_co_u32_e32 v27, vcc, 0, v27, vcc
	global_load_dwordx4 v[68:71], v[26:27], off
	global_load_dwordx4 v[72:75], v[26:27], off offset:1024
	global_load_dwordx4 v[76:79], v[26:27], off offset:2048
	global_load_dwordx4 v[80:83], v[26:27], off offset:3072
	v_mov_b32_e32 v116, 0
	s_waitcnt vmcnt(7)
	v_lshlrev_b32_e32 v7, 16, v52
	v_and_b32_e32 v19, 0xffff0000, v52
	v_lshlrev_b32_e32 v21, 16, v53
	v_and_b32_e32 v23, 0xffff0000, v53
	v_lshlrev_b32_e32 v52, 16, v55
	v_and_b32_e32 v53, 0xffff0000, v55
	s_waitcnt vmcnt(6)
	v_lshlrev_b32_e32 v85, 16, v59
	v_and_b32_e32 v59, 0xffff0000, v59
	v_lshlrev_b32_e32 v27, 16, v54
	v_and_b32_e32 v51, 0xffff0000, v54
	v_lshlrev_b32_e32 v54, 16, v56
	v_and_b32_e32 v55, 0xffff0000, v56
	v_lshlrev_b32_e32 v56, 16, v57
	v_and_b32_e32 v57, 0xffff0000, v57
	v_max_f32_e64 v25, |v19|, |v19|
	v_max_f32_e64 v26, |v7|, |v7|
	v_max_f32_e64 v94, |v23|, |v23|
	v_max_f32_e64 v95, |v21|, |v21|
	v_max_f32_e64 v96, |v53|, |v53|
	v_max_f32_e64 v97, |v52|, |v52|
	v_max_f32_e64 v102, |v59|, |v59|
	v_max_f32_e64 v103, |v85|, |v85|
	v_lshlrev_b32_e32 v84, 16, v58
	v_and_b32_e32 v58, 0xffff0000, v58
	v_max_f32_e64 v98, |v55|, |v55|
	v_max_f32_e64 v99, |v54|, |v54|
	v_max_f32_e64 v100, |v57|, |v57|
	v_max_f32_e64 v101, |v56|, |v56|
	v_max_f32_e32 v25, v26, v25
	v_max_f32_e32 v26, v95, v94
	v_max_f32_e32 v94, v97, v96
	v_max_f32_e32 v97, v103, v102
	s_waitcnt vmcnt(5)
	v_lshlrev_b32_e32 v89, 16, v63
	v_and_b32_e32 v63, 0xffff0000, v63
	s_waitcnt vmcnt(4)
	v_lshlrev_b32_e32 v93, 16, v67
	v_and_b32_e32 v67, 0xffff0000, v67
	v_max_f32_e32 v95, v99, v98
	v_max_f32_e32 v96, v101, v100
	v_max3_f32 v94, |v27|, |v51|, v94
	v_max3_f32 v97, |v84|, |v58|, v97
	v_lshlrev_b32_e32 v86, 16, v60
	v_and_b32_e32 v60, 0xffff0000, v60
	v_lshlrev_b32_e32 v87, 16, v61
	v_and_b32_e32 v61, 0xffff0000, v61
	v_lshlrev_b32_e32 v90, 16, v64
	v_and_b32_e32 v64, 0xffff0000, v64
	v_lshlrev_b32_e32 v91, 16, v65
	v_and_b32_e32 v65, 0xffff0000, v65
	v_max_f32_e64 v108, |v63|, |v63|
	v_max_f32_e64 v109, |v89|, |v89|
	v_max_f32_e64 v114, |v67|, |v67|
	v_max_f32_e64 v115, |v93|, |v93|
	v_max3_f32 v25, v25, v26, v94
	v_max3_f32 v26, v95, v96, v97
	v_lshlrev_b32_e32 v88, 16, v62
	v_and_b32_e32 v62, 0xffff0000, v62
	v_lshlrev_b32_e32 v92, 16, v66
	v_and_b32_e32 v66, 0xffff0000, v66
	v_max_f32_e64 v104, |v60|, |v60|
	v_max_f32_e64 v105, |v86|, |v86|
	v_max_f32_e64 v106, |v61|, |v61|
	v_max_f32_e64 v107, |v87|, |v87|
	v_max_f32_e64 v110, |v64|, |v64|
	v_max_f32_e64 v111, |v90|, |v90|
	v_max_f32_e64 v112, |v65|, |v65|
	v_max_f32_e64 v113, |v91|, |v91|
	v_max_f32_e32 v100, v109, v108
	v_max3_f32 v25, v25, 0, v26
	v_max_f32_e32 v26, v115, v114
	v_max_f32_e32 v98, v105, v104
	v_max_f32_e32 v99, v107, v106
	v_max_f32_e32 v101, v111, v110
	v_max_f32_e32 v102, v113, v112
	v_max3_f32 v100, |v88|, |v62|, v100
	v_max3_f32 v26, |v92|, |v66|, v26
	v_max3_f32 v94, v98, v99, v100
	v_max3_f32 v26, v101, v102, v26
	v_max3_f32 v25, v25, v94, v26
	s_waitcnt vmcnt(3)
	v_lshlrev_b32_e32 v94, 16, v68
	v_and_b32_e32 v68, 0xffff0000, v68
	v_max_f32_e64 v26, |v68|, |v68|
	v_max_f32_e64 v95, |v94|, |v94|
	v_max_f32_e32 v26, v95, v26
	v_lshlrev_b32_e32 v95, 16, v69
	v_and_b32_e32 v69, 0xffff0000, v69
	v_lshlrev_b32_e32 v98, 16, v71
	v_and_b32_e32 v71, 0xffff0000, v71
	v_max_f32_e64 v96, |v69|, |v69|
	v_max_f32_e64 v97, |v95|, |v95|
	v_max_f32_e64 v99, |v71|, |v71|
	v_max_f32_e64 v100, |v98|, |v98|
	v_max_f32_e32 v96, v97, v96
	v_lshlrev_b32_e32 v97, 16, v70
	v_and_b32_e32 v70, 0xffff0000, v70
	v_max_f32_e32 v99, v100, v99
	v_max3_f32 v99, |v97|, |v70|, v99
	v_max3_f32 v26, v26, v96, v99
	s_waitcnt vmcnt(2)
	v_lshlrev_b32_e32 v96, 16, v72
	v_and_b32_e32 v72, 0xffff0000, v72
	v_max_f32_e64 v99, |v72|, |v72|
	v_max_f32_e64 v100, |v96|, |v96|
	v_max_f32_e32 v99, v100, v99
	v_lshlrev_b32_e32 v100, 16, v73
	v_and_b32_e32 v73, 0xffff0000, v73
	v_lshlrev_b32_e32 v103, 16, v75
	v_and_b32_e32 v75, 0xffff0000, v75
	v_max_f32_e64 v101, |v73|, |v73|
	v_max_f32_e64 v102, |v100|, |v100|
	v_max_f32_e64 v104, |v75|, |v75|
	v_max_f32_e64 v105, |v103|, |v103|
	v_max_f32_e32 v101, v102, v101
	v_lshlrev_b32_e32 v102, 16, v74
	v_and_b32_e32 v74, 0xffff0000, v74
	v_max_f32_e32 v104, v105, v104
	v_max3_f32 v104, |v102|, |v74|, v104
	v_max3_f32 v99, v99, v101, v104
	v_max3_f32 v25, v25, v26, v99
	s_waitcnt vmcnt(1)
	v_lshlrev_b32_e32 v99, 16, v76
	v_and_b32_e32 v76, 0xffff0000, v76
	v_max_f32_e64 v26, |v76|, |v76|
	v_max_f32_e64 v101, |v99|, |v99|
	v_max_f32_e32 v26, v101, v26
	v_lshlrev_b32_e32 v101, 16, v77
	v_and_b32_e32 v77, 0xffff0000, v77
	v_lshlrev_b32_e32 v106, 16, v79
	v_and_b32_e32 v79, 0xffff0000, v79
	v_max_f32_e64 v104, |v77|, |v77|
	v_max_f32_e64 v105, |v101|, |v101|
	v_max_f32_e64 v107, |v79|, |v79|
	v_max_f32_e64 v108, |v106|, |v106|
	v_max_f32_e32 v104, v105, v104
	v_lshlrev_b32_e32 v105, 16, v78
	v_and_b32_e32 v78, 0xffff0000, v78
	v_max_f32_e32 v107, v108, v107
	v_max3_f32 v107, |v105|, |v78|, v107
	v_max3_f32 v26, v26, v104, v107
	s_waitcnt vmcnt(0)
; #define LAS __attribute__((address_space(3)))
; __device__ __forceinline__ float bflo(unsigned u) { return __uint_as_float(u << 16); }
; __device__ __forceinline__ float bfhi(unsigned u) { return __uint_as_float(u & 0xffff0000u); }
; __device__ __forceinline__ void peer_expert_phase(const Args& a, int layer, LAS unsigned char* lds, int G, int bid) {
;     ...
;             am = wave_max(am); const float qs = am > 0.f ? 127.0f / am : 0.f; xs[i] = am * (1.0f / 127.0f);
; #pragma unroll
;             for (int j = 0; j < 8; ++j) { u32x2 o; o.x = pk_i8(bflo(xv[j].x) * qs, bfhi(xv[j].x) * qs, bflo(xv[j].y) * qs, bfhi(xv[j].y) * qs); o.y = pk_i8(bflo(xv[j].z) * qs, bfhi(xv[j].z) * qs, bflo(xv[j].w) * qs, bfhi(xv[j].w) * qs);
;                 *(LAS u32x2*)(X8 + i * 4096 + 8 * (lane + 64 * j)) = o; } }
	v_lshlrev_b32_e32 v104, 16, v80
	v_and_b32_e32 v80, 0xffff0000, v80
	v_max_f32_e64 v107, |v80|, |v80|
	v_max_f32_e64 v108, |v104|, |v104|
	v_max_f32_e32 v107, v108, v107
	v_lshlrev_b32_e32 v108, 16, v81
	v_and_b32_e32 v81, 0xffff0000, v81
	v_lshlrev_b32_e32 v111, 16, v83
	v_and_b32_e32 v83, 0xffff0000, v83
	v_max_f32_e64 v109, |v81|, |v81|
	v_max_f32_e64 v110, |v108|, |v108|
	v_max_f32_e64 v112, |v83|, |v83|
	v_max_f32_e64 v113, |v111|, |v111|
	v_max_f32_e32 v109, v110, v109
	v_lshlrev_b32_e32 v110, 16, v82
	v_and_b32_e32 v82, 0xffff0000, v82
	v_max_f32_e32 v112, v113, v112
	v_max3_f32 v112, |v110|, |v82|, v112
	v_max3_f32 v107, v107, v109, v112
	v_max3_f32 v25, v25, v26, v107
	ds_bpermute_b32 v26, v29, v25
	v_mov_b32_e32 v114, 0
	v_mov_b32_e32 v115, 0
	s_waitcnt lgkmcnt(0)
	v_max_f32_e32 v26, v26, v26
	v_max_f32_e32 v25, v25, v26
	ds_bpermute_b32 v26, v30, v25
	s_waitcnt lgkmcnt(0)
	v_max_f32_e32 v26, v26, v26
	v_max_f32_e32 v25, v25, v26
	ds_bpermute_b32 v26, v31, v25
	s_waitcnt lgkmcnt(0)
	v_max_f32_e32 v26, v26, v26
	v_max_f32_e32 v25, v25, v26
	ds_bpermute_b32 v26, v32, v25
	s_waitcnt lgkmcnt(0)
	v_max_f32_e32 v26, v26, v26
	v_max_f32_e32 v25, v25, v26
	ds_bpermute_b32 v26, v33, v25
	s_waitcnt lgkmcnt(0)
	v_max_f32_e32 v26, v26, v26
	v_max_f32_e32 v25, v25, v26
	ds_bpermute_b32 v26, v34, v25
	s_waitcnt lgkmcnt(0)
	v_max_f32_e32 v26, v26, v26
	v_max_f32_e32 v25, v25, v26
	v_div_scale_f32 v26, s[60:61], v25, v25, s69
	v_rcp_f32_e32 v107, v26
	s_nop 0
	v_fma_f32 v109, -v26, v107, 1.0
	v_fmac_f32_e32 v107, v109, v107
	v_div_scale_f32 v109, vcc, s69, v25, s69
	v_mul_f32_e32 v112, v109, v107
	v_fma_f32 v113, -v26, v112, v109
	v_fmac_f32_e32 v112, v113, v107
	v_fma_f32 v26, -v26, v112, v109
	v_div_fmas_f32 v26, v26, v107, v112
	v_div_fixup_f32 v26, v26, v25, s69
	v_cmp_lt_f32_e32 vcc, 0, v25
	v_mov_b32_e32 v109, 0
	v_mov_b32_e32 v112, 0
	v_cndmask_b32_e32 v107, 0, v26, vcc
	v_fmaak_f32 v7, v107, v7, 0x4b400000
	v_fmaak_f32 v19, v107, v19, 0x4b400000
	v_fmaak_f32 v21, v107, v21, 0x4b400000
	v_fmaak_f32 v23, v107, v23, 0x4b400000
	v_perm_b32 v21, v23, v21, s70
	v_perm_b32 v7, v19, v7, s70
	v_perm_b32 v26, v21, v7, s71
	v_fmaak_f32 v7, v107, v27, 0x4b400000
	v_fmaak_f32 v19, v107, v51, 0x4b400000
	v_fmaak_f32 v21, v107, v52, 0x4b400000
	v_fmaak_f32 v23, v107, v53, 0x4b400000
	v_perm_b32 v21, v23, v21, s70
	v_perm_b32 v7, v19, v7, s70
	v_perm_b32 v27, v21, v7, s71
	v_fmaak_f32 v7, v107, v54, 0x4b400000
	v_fmaak_f32 v19, v107, v55, 0x4b400000
	v_fmaak_f32 v21, v107, v56, 0x4b400000
	v_fmaak_f32 v23, v107, v57, 0x4b400000
	v_perm_b32 v21, v23, v21, s70
	v_perm_b32 v7, v19, v7, s70
	v_perm_b32 v52, v21, v7, s71
	v_fmaak_f32 v7, v107, v84, 0x4b400000
	v_fmaak_f32 v19, v107, v58, 0x4b400000
	v_fmaak_f32 v21, v107, v85, 0x4b400000
	v_fmaak_f32 v23, v107, v59, 0x4b400000
	v_perm_b32 v21, v23, v21, s70
	v_perm_b32 v7, v19, v7, s70
	v_perm_b32 v53, v21, v7, s71
	v_fmaak_f32 v7, v107, v86, 0x4b400000
	v_fmaak_f32 v19, v107, v60, 0x4b400000
	v_fmaak_f32 v21, v107, v87, 0x4b400000
	v_fmaak_f32 v23, v107, v61, 0x4b400000
	v_perm_b32 v21, v23, v21, s70
	v_perm_b32 v7, v19, v7, s70
	ds_write2st64_b64 v46, v[26:27], v[52:53] offset0:24 offset1:25
	v_perm_b32 v26, v21, v7, s71
	v_fmaak_f32 v7, v107, v88, 0x4b400000
	v_fmaak_f32 v19, v107, v62, 0x4b400000
	v_fmaak_f32 v21, v107, v89, 0x4b400000
	v_fmaak_f32 v23, v107, v63, 0x4b400000
	v_perm_b32 v21, v23, v21, s70
	v_perm_b32 v7, v19, v7, s70
	v_perm_b32 v27, v21, v7, s71
	v_fmaak_f32 v7, v107, v90, 0x4b400000
	v_fmaak_f32 v19, v107, v64, 0x4b400000
	v_fmaak_f32 v21, v107, v91, 0x4b400000
	v_fmaak_f32 v23, v107, v65, 0x4b400000
	v_perm_b32 v21, v23, v21, s70
	v_perm_b32 v7, v19, v7, s70
	v_perm_b32 v52, v21, v7, s71
	v_fmaak_f32 v7, v107, v92, 0x4b400000
	v_fmaak_f32 v19, v107, v66, 0x4b400000
	v_fmaak_f32 v21, v107, v93, 0x4b400000
	v_fmaak_f32 v23, v107, v67, 0x4b400000
	v_perm_b32 v21, v23, v21, s70
	v_perm_b32 v7, v19, v7, s70
	v_perm_b32 v53, v21, v7, s71
	v_fmaak_f32 v7, v107, v94, 0x4b400000
	v_fmaak_f32 v19, v107, v68, 0x4b400000
	v_fmaak_f32 v21, v107, v95, 0x4b400000
	v_fmaak_f32 v23, v107, v69, 0x4b400000
	v_perm_b32 v21, v23, v21, s70
	v_perm_b32 v7, v19, v7, s70
	ds_write2st64_b64 v46, v[26:27], v[52:53] offset0:26 offset1:27
	v_perm_b32 v26, v21, v7, s71
	v_fmaak_f32 v7, v107, v97, 0x4b400000
	v_fmaak_f32 v19, v107, v70, 0x4b400000
	v_fmaak_f32 v21, v107, v98, 0x4b400000
	v_fmaak_f32 v23, v107, v71, 0x4b400000
	v_perm_b32 v21, v23, v21, s70
	v_perm_b32 v7, v19, v7, s70
	v_perm_b32 v27, v21, v7, s71
	v_fmaak_f32 v7, v107, v96, 0x4b400000
	v_fmaak_f32 v19, v107, v72, 0x4b400000
	v_fmaak_f32 v21, v107, v100, 0x4b400000
	v_fmaak_f32 v23, v107, v73, 0x4b400000
	v_perm_b32 v21, v23, v21, s70
	v_perm_b32 v7, v19, v7, s70
	v_perm_b32 v52, v21, v7, s71
	v_fmaak_f32 v7, v107, v102, 0x4b400000
	v_fmaak_f32 v19, v107, v74, 0x4b400000
	v_fmaak_f32 v21, v107, v103, 0x4b400000
	v_fmaak_f32 v23, v107, v75, 0x4b400000
	v_perm_b32 v21, v23, v21, s70
	v_perm_b32 v7, v19, v7, s70
	v_perm_b32 v53, v21, v7, s71
	v_fmaak_f32 v7, v107, v99, 0x4b400000
	v_fmaak_f32 v19, v107, v76, 0x4b400000
	v_fmaak_f32 v21, v107, v101, 0x4b400000
	v_fmaak_f32 v23, v107, v77, 0x4b400000
	v_perm_b32 v21, v23, v21, s70
	v_perm_b32 v7, v19, v7, s70
	ds_write2st64_b64 v46, v[26:27], v[52:53] offset0:28 offset1:29
	v_perm_b32 v26, v21, v7, s71
	v_fmaak_f32 v7, v107, v105, 0x4b400000
	v_fmaak_f32 v19, v107, v78, 0x4b400000
	v_fmaak_f32 v21, v107, v106, 0x4b400000
	v_fmaak_f32 v23, v107, v79, 0x4b400000
	v_perm_b32 v21, v23, v21, s70
	v_perm_b32 v7, v19, v7, s70
	v_perm_b32 v27, v21, v7, s71
	v_fmaak_f32 v7, v107, v104, 0x4b400000
; #define LAS __attribute__((address_space(3)))
; __device__ __forceinline__ void peer_expert_phase(const Args& a, int layer, LAS unsigned char* lds, int G, int bid) {
;     ...
;             for (int c = 0; c < 16; ++c) pacc[i][c] = 0;
;     ...
;         for (int i = 0; i < 4; ++i) { eoa[i] = (unsigned)ea[i] << 12; eob[i] = (unsigned)eb[i] << 12; }
;         const unsigned lo16 = 16u * (unsigned)l7;
; #pragma unroll 1
;         for (int sidx = 0; sidx < 32; ++sidx) { const int s = (sidx + srot) & 31; const unsigned char* pus = PU + s * 128;
; #pragma unroll
;             for (int i = 0; i < 4; ++i) {
;                 int tok = tb + i * NGW; tok = tok < NTOK ? tok : tb;
;                 const u32x4 xq = *(const LAS u32x4*)(X8 + i * 4096 + s * 128 + 16 * l7);
;                 u32x4 r[16];
; #pragma unroll
;                 for (int c = 0; c < 16; ++c) { const unsigned eo = (unsigned)__shfl((int)(c < 8 ? eoa[i] : eob[i]), (8 * c + g8) & 63); r[c] = *(const u32x4*)(pus + (eo + lo16)); }
	v_fmaak_f32 v19, v107, v80, 0x4b400000
	v_fmaak_f32 v21, v107, v108, 0x4b400000
	v_fmaak_f32 v23, v107, v81, 0x4b400000
	v_perm_b32 v21, v23, v21, s70
	v_perm_b32 v7, v19, v7, s70
	v_perm_b32 v52, v21, v7, s71
	v_fmaak_f32 v7, v107, v110, 0x4b400000
	v_fmaak_f32 v19, v107, v82, 0x4b400000
	v_fmaak_f32 v21, v107, v111, 0x4b400000
	v_fmaak_f32 v23, v107, v83, 0x4b400000
	v_perm_b32 v21, v23, v21, s70
	v_perm_b32 v7, v19, v7, s70
	v_perm_b32 v53, v21, v7, s71
	ds_write2st64_b64 v46, v[26:27], v[52:53] offset0:30 offset1:31
	v_lshlrev_b32_e32 v51, 12, v18
	v_lshlrev_b32_e32 v52, 12, v2
	v_lshlrev_b32_e32 v53, 12, v6
	v_lshlrev_b32_e32 v54, 12, v0
	v_lshlrev_b32_e32 v55, 12, v22
	v_lshlrev_b32_e32 v56, 12, v20
	v_lshlrev_b32_e32 v57, 12, v4
	v_lshlrev_b32_e32 v58, 12, v24
	v_mov_b32_e32 v89, 0
	v_mov_b32_e32 v92, 0
	v_mov_b32_e32 v93, 0
	v_mov_b32_e32 v94, 0
	v_mov_b32_e32 v95, 0
	v_mov_b32_e32 v96, 0
	v_mov_b32_e32 v97, 0
	v_mov_b32_e32 v98, 0
	v_mov_b32_e32 v99, 0
	v_mov_b32_e32 v100, 0
	v_mov_b32_e32 v101, 0
	v_mov_b32_e32 v102, 0
	v_mov_b32_e32 v103, 0
	v_mov_b32_e32 v104, 0
	v_mov_b32_e32 v105, 0
	v_mov_b32_e32 v106, 0
	v_mov_b32_e32 v107, 0
	v_mov_b32_e32 v26, 0
	v_mov_b32_e32 v108, 0
	v_mov_b32_e32 v110, 0
	v_mov_b32_e32 v111, 0
	v_mov_b32_e32 v113, 0
	v_mov_b32_e32 v27, 0
	v_mov_b32_e32 v91, 0
	v_mov_b32_e32 v90, 0
	v_mov_b32_e32 v88, 0
	v_mov_b32_e32 v87, 0
	v_mov_b32_e32 v86, 0
	v_mov_b32_e32 v85, 0
	v_mov_b32_e32 v84, 0
	v_mov_b32_e32 v83, 0
	v_mov_b32_e32 v82, 0
	v_mov_b32_e32 v81, 0
	v_mov_b32_e32 v80, 0
	v_mov_b32_e32 v79, 0
	v_mov_b32_e32 v78, 0
	v_mov_b32_e32 v77, 0
	v_mov_b32_e32 v76, 0
	v_mov_b32_e32 v75, 0
	v_mov_b32_e32 v74, 0
	v_mov_b32_e32 v73, 0
	v_mov_b32_e32 v72, 0
	v_mov_b32_e32 v71, 0
	v_mov_b32_e32 v70, 0
	v_mov_b32_e32 v69, 0
	v_mov_b32_e32 v68, 0
	v_mov_b32_e32 v67, 0
	v_mov_b32_e32 v66, 0
	v_mov_b32_e32 v65, 0
	v_mov_b32_e32 v64, 0
	v_mov_b32_e32 v63, 0
	v_mov_b32_e32 v62, 0
	v_mov_b32_e32 v61, 0
	v_mov_b32_e32 v60, 0
	v_mov_b32_e32 v59, 0
	v_mov_b32_e32 v19, 0
	v_mov_b32_e32 v23, 0
	v_mov_b32_e32 v21, 0
	v_mov_b32_e32 v7, 0
	ds_bpermute_b32 v186, v38, v51
	ds_bpermute_b32 v187, v39, v51
	ds_bpermute_b32 v188, v40, v51
	ds_bpermute_b32 v189, v41, v51
	ds_bpermute_b32 v190, v42, v51
	ds_bpermute_b32 v191, v43, v51
	ds_bpermute_b32 v192, v44, v51
	ds_bpermute_b32 v193, v45, v51
	s_waitcnt lgkmcnt(7)
	v_add_u32_e32 v186, v186, v35
	s_waitcnt lgkmcnt(6)
	v_add_u32_e32 v187, v187, v35
	s_waitcnt lgkmcnt(5)
	v_add_u32_e32 v188, v188, v35
	s_waitcnt lgkmcnt(4)
	v_add_u32_e32 v189, v189, v35
	s_waitcnt lgkmcnt(3)
	v_add_u32_e32 v190, v190, v35
	s_waitcnt lgkmcnt(2)
	v_add_u32_e32 v191, v191, v35
	s_waitcnt lgkmcnt(1)
	v_add_u32_e32 v192, v192, v35
	s_waitcnt lgkmcnt(0)
	v_add_u32_e32 v193, v193, v35
	ds_bpermute_b32 v194, v38, v52
	ds_bpermute_b32 v195, v40, v52
	ds_bpermute_b32 v196, v42, v52
	ds_bpermute_b32 v197, v39, v52
	ds_bpermute_b32 v198, v44, v52
	ds_bpermute_b32 v199, v41, v52
	ds_bpermute_b32 v200, v43, v52
	ds_bpermute_b32 v201, v45, v52
	s_waitcnt lgkmcnt(7)
	v_add_u32_e32 v194, v194, v35
	s_waitcnt lgkmcnt(6)
	v_add_u32_e32 v195, v195, v35
	s_waitcnt lgkmcnt(5)
	v_add_u32_e32 v196, v196, v35
	s_waitcnt lgkmcnt(4)
	v_add_u32_e32 v197, v197, v35
	s_waitcnt lgkmcnt(3)
	v_add_u32_e32 v198, v198, v35
	s_waitcnt lgkmcnt(2)
	v_add_u32_e32 v199, v199, v35
	s_waitcnt lgkmcnt(1)
	v_add_u32_e32 v200, v200, v35
	s_waitcnt lgkmcnt(0)
	v_add_u32_e32 v201, v201, v35
	ds_bpermute_b32 v202, v38, v53
	ds_bpermute_b32 v203, v39, v53
	ds_bpermute_b32 v204, v40, v53
	ds_bpermute_b32 v205, v41, v53
	ds_bpermute_b32 v206, v42, v53
	ds_bpermute_b32 v207, v43, v53
	ds_bpermute_b32 v208, v44, v53
	ds_bpermute_b32 v209, v45, v53
	s_waitcnt lgkmcnt(7)
	v_add_u32_e32 v202, v202, v35
	s_waitcnt lgkmcnt(6)
	v_add_u32_e32 v203, v203, v35
	s_waitcnt lgkmcnt(5)
	v_add_u32_e32 v204, v204, v35
	s_waitcnt lgkmcnt(4)
	v_add_u32_e32 v205, v205, v35
	s_waitcnt lgkmcnt(3)
	v_add_u32_e32 v206, v206, v35
	s_waitcnt lgkmcnt(2)
	v_add_u32_e32 v207, v207, v35
	s_waitcnt lgkmcnt(1)
	v_add_u32_e32 v208, v208, v35
	s_waitcnt lgkmcnt(0)
	v_add_u32_e32 v209, v209, v35
	ds_bpermute_b32 v210, v38, v54
	ds_bpermute_b32 v211, v39, v54
	ds_bpermute_b32 v212, v40, v54
	ds_bpermute_b32 v213, v41, v54
	ds_bpermute_b32 v214, v42, v54
	ds_bpermute_b32 v215, v43, v54
	ds_bpermute_b32 v216, v44, v54
	ds_bpermute_b32 v217, v45, v54
	s_waitcnt lgkmcnt(7)
	v_add_u32_e32 v210, v210, v35
	s_waitcnt lgkmcnt(6)
	v_add_u32_e32 v211, v211, v35
	s_waitcnt lgkmcnt(5)
	v_add_u32_e32 v212, v212, v35
	s_waitcnt lgkmcnt(4)
	v_add_u32_e32 v213, v213, v35
	s_waitcnt lgkmcnt(3)
	v_add_u32_e32 v214, v214, v35
	s_waitcnt lgkmcnt(2)
	v_add_u32_e32 v215, v215, v35
	s_waitcnt lgkmcnt(1)
	v_add_u32_e32 v216, v216, v35
	s_waitcnt lgkmcnt(0)
	v_add_u32_e32 v217, v217, v35
	ds_bpermute_b32 v218, v38, v55
	ds_bpermute_b32 v219, v39, v55
	ds_bpermute_b32 v220, v40, v55
	ds_bpermute_b32 v221, v41, v55
	ds_bpermute_b32 v222, v42, v55
	ds_bpermute_b32 v223, v43, v55
	ds_bpermute_b32 v224, v44, v55
	ds_bpermute_b32 v225, v45, v55
	s_waitcnt lgkmcnt(7)
	v_add_u32_e32 v218, v218, v35
	s_waitcnt lgkmcnt(6)
	v_add_u32_e32 v219, v219, v35
	s_waitcnt lgkmcnt(5)
	v_add_u32_e32 v220, v220, v35
	s_waitcnt lgkmcnt(4)
	v_add_u32_e32 v221, v221, v35
	s_waitcnt lgkmcnt(3)
	v_add_u32_e32 v222, v222, v35
	s_waitcnt lgkmcnt(2)
	v_add_u32_e32 v223, v223, v35
	s_waitcnt lgkmcnt(1)
	v_add_u32_e32 v224, v224, v35
	s_waitcnt lgkmcnt(0)
	v_add_u32_e32 v225, v225, v35
	ds_bpermute_b32 v226, v38, v56
	ds_bpermute_b32 v227, v39, v56
	ds_bpermute_b32 v229, v40, v56
	ds_bpermute_b32 v230, v41, v56
	ds_bpermute_b32 v231, v42, v56
	ds_bpermute_b32 v232, v43, v56
	ds_bpermute_b32 v233, v44, v56
	ds_bpermute_b32 v234, v45, v56
	s_waitcnt lgkmcnt(7)
; #define LAS __attribute__((address_space(3)))
; __device__ __forceinline__ void peer_expert_phase(const Args& a, int layer, LAS unsigned char* lds, int G, int bid) {
;     ...
;         for (int sidx = 0; sidx < 32; ++sidx) { const int s = (sidx + srot) & 31; const unsigned char* pus = PU + s * 128;
; #pragma unroll
;             for (int i = 0; i < 4; ++i) {
;                 int tok = tb + i * NGW; tok = tok < NTOK ? tok : tb;
;                 const u32x4 xq = *(const LAS u32x4*)(X8 + i * 4096 + s * 128 + 16 * l7);
;                 u32x4 r[16];
; #pragma unroll
;                 for (int c = 0; c < 16; ++c) { const unsigned eo = (unsigned)__shfl((int)(c < 8 ? eoa[i] : eob[i]), (8 * c + g8) & 63); r[c] = *(const u32x4*)(pus + (eo + lo16)); }
; #pragma unroll
;                 for (int c = 0; c < 16; ++c) { int d = pacc[i][c];
; #pragma unroll
;                     for (int q = 0; q < 4; ++q) d = __builtin_amdgcn_sdot4((int)r[c][q], (int)xq[q], d, false);
;                     pacc[i][c] = d; }
	v_add_u32_e32 v226, v226, v35
	s_waitcnt lgkmcnt(6)
	v_add_u32_e32 v227, v227, v35
	s_waitcnt lgkmcnt(5)
	v_add_u32_e32 v229, v229, v35
	s_waitcnt lgkmcnt(4)
	v_add_u32_e32 v230, v230, v35
	s_waitcnt lgkmcnt(3)
	v_add_u32_e32 v231, v231, v35
	s_waitcnt lgkmcnt(2)
	v_add_u32_e32 v232, v232, v35
	s_waitcnt lgkmcnt(1)
	v_add_u32_e32 v233, v233, v35
	s_waitcnt lgkmcnt(0)
	v_add_u32_e32 v234, v234, v35
	ds_bpermute_b32 v235, v38, v57
	ds_bpermute_b32 v236, v39, v57
	ds_bpermute_b32 v237, v40, v57
	ds_bpermute_b32 v238, v41, v57
	ds_bpermute_b32 v239, v42, v57
	ds_bpermute_b32 v240, v43, v57
	ds_bpermute_b32 v241, v44, v57
	ds_bpermute_b32 v242, v45, v57
	s_waitcnt lgkmcnt(7)
	v_add_u32_e32 v235, v235, v35
	s_waitcnt lgkmcnt(6)
	v_add_u32_e32 v236, v236, v35
	s_waitcnt lgkmcnt(5)
	v_add_u32_e32 v237, v237, v35
	s_waitcnt lgkmcnt(4)
	v_add_u32_e32 v238, v238, v35
	s_waitcnt lgkmcnt(3)
	v_add_u32_e32 v239, v239, v35
	s_waitcnt lgkmcnt(2)
	v_add_u32_e32 v240, v240, v35
	s_waitcnt lgkmcnt(1)
	v_add_u32_e32 v241, v241, v35
	s_waitcnt lgkmcnt(0)
	v_add_u32_e32 v242, v242, v35
	ds_bpermute_b32 v243, v38, v58
	ds_bpermute_b32 v244, v39, v58
	ds_bpermute_b32 v245, v40, v58
	ds_bpermute_b32 v246, v41, v58
	ds_bpermute_b32 v247, v42, v58
	ds_bpermute_b32 v248, v43, v58
	ds_bpermute_b32 v249, v44, v58
	ds_bpermute_b32 v250, v45, v58
	s_waitcnt lgkmcnt(7)
	v_add_u32_e32 v243, v243, v35
	s_waitcnt lgkmcnt(6)
	v_add_u32_e32 v244, v244, v35
	s_waitcnt lgkmcnt(5)
	v_add_u32_e32 v245, v245, v35
	s_waitcnt lgkmcnt(4)
	v_add_u32_e32 v246, v246, v35
	s_waitcnt lgkmcnt(3)
	v_add_u32_e32 v247, v247, v35
	s_waitcnt lgkmcnt(2)
	v_add_u32_e32 v248, v248, v35
	s_waitcnt lgkmcnt(1)
	v_add_u32_e32 v249, v249, v35
	s_waitcnt lgkmcnt(0)
	v_add_u32_e32 v250, v250, v35
.LBB0_2267:
	s_barrier
	s_add_i32 s60, s67, s40
	s_and_b32 s81, s60, 0xf80
	s_add_u32 s60, s62, s81
	s_addc_u32 s61, s63, 0
	v_add_u32_e32 v117, s81, v36
	global_load_dwordx4 v[118:121], v186, s[60:61]
	global_load_dwordx4 v[122:125], v187, s[60:61]
	global_load_dwordx4 v[126:129], v188, s[60:61]
	global_load_dwordx4 v[130:133], v189, s[60:61]
	global_load_dwordx4 v[134:137], v190, s[60:61]
	global_load_dwordx4 v[138:141], v191, s[60:61]
	global_load_dwordx4 v[142:145], v192, s[60:61]
	global_load_dwordx4 v[146:149], v193, s[60:61]
	global_load_dwordx4 v[150:153], v194, s[60:61]
	global_load_dwordx4 v[158:161], v195, s[60:61]
	global_load_dwordx4 v[166:169], v196, s[60:61]
	global_load_dwordx4 v[154:157], v197, s[60:61]
	global_load_dwordx4 v[174:177], v198, s[60:61]
	global_load_dwordx4 v[162:165], v199, s[60:61]
	global_load_dwordx4 v[170:173], v200, s[60:61]
	global_load_dwordx4 v[178:181], v201, s[60:61]
	ds_read_b128 v[182:185], v117
	s_waitcnt lgkmcnt(0)
	s_waitcnt vmcnt(15)
	v_dot4c_i32_i8_e32 v116, v118, v182
	s_waitcnt vmcnt(14)
	v_dot4c_i32_i8_e32 v115, v122, v182
	v_dot4c_i32_i8_e32 v116, v119, v183
	s_waitcnt vmcnt(13)
	v_dot4c_i32_i8_e32 v27, v126, v182
	s_waitcnt vmcnt(12)
	v_dot4c_i32_i8_e32 v114, v130, v182
	v_dot4c_i32_i8_e32 v115, v123, v183
	v_dot4c_i32_i8_e32 v27, v127, v183
	v_dot4c_i32_i8_e32 v114, v131, v183
	s_waitcnt vmcnt(11)
	v_dot4c_i32_i8_e32 v113, v134, v182
	s_waitcnt vmcnt(10)
	v_dot4c_i32_i8_e32 v112, v138, v182
	v_dot4c_i32_i8_e32 v113, v135, v183
	v_dot4c_i32_i8_e32 v112, v139, v183
	v_dot4c_i32_i8_e32 v116, v120, v184
	s_waitcnt vmcnt(9)
	v_dot4c_i32_i8_e32 v111, v142, v182
	s_waitcnt vmcnt(8)
	v_dot4c_i32_i8_e32 v110, v146, v182
	v_dot4c_i32_i8_e32 v111, v143, v183
	v_dot4c_i32_i8_e32 v110, v147, v183
	s_waitcnt vmcnt(7)
	v_dot4c_i32_i8_e32 v109, v150, v182
	v_dot4c_i32_i8_e32 v109, v151, v183
	s_waitcnt vmcnt(6)
	v_dot4c_i32_i8_e32 v26, v158, v182
	v_dot4c_i32_i8_e32 v26, v159, v183
	v_dot4c_i32_i8_e32 v115, v124, v184
	v_dot4c_i32_i8_e32 v27, v128, v184
	v_dot4c_i32_i8_e32 v114, v132, v184
	s_waitcnt vmcnt(5)
	v_dot4c_i32_i8_e32 v106, v166, v182
	v_dot4c_i32_i8_e32 v106, v167, v183
	s_waitcnt vmcnt(4)
	v_dot4c_i32_i8_e32 v108, v154, v182
	v_dot4c_i32_i8_e32 v108, v155, v183
	v_dot4c_i32_i8_e32 v113, v136, v184
	s_waitcnt vmcnt(3)
	v_dot4c_i32_i8_e32 v104, v174, v182
	v_dot4c_i32_i8_e32 v104, v175, v183
	v_dot4c_i32_i8_e32 v112, v140, v184
	v_dot4c_i32_i8_e32 v111, v144, v184
	s_waitcnt vmcnt(2)
	v_dot4c_i32_i8_e32 v107, v162, v182
	v_dot4c_i32_i8_e32 v107, v163, v183
	v_dot4c_i32_i8_e32 v110, v148, v184
	v_dot4c_i32_i8_e32 v109, v152, v184
	v_dot4c_i32_i8_e32 v108, v156, v184
	v_dot4c_i32_i8_e32 v26, v160, v184
	v_dot4c_i32_i8_e32 v107, v164, v184
	s_waitcnt vmcnt(1)
	v_dot4c_i32_i8_e32 v105, v170, v182
	v_dot4c_i32_i8_e32 v105, v171, v183
	v_dot4c_i32_i8_e32 v106, v168, v184
	v_dot4c_i32_i8_e32 v105, v172, v184
	v_dot4c_i32_i8_e32 v104, v176, v184
	v_dot4c_i32_i8_e32 v116, v121, v185
	v_dot4c_i32_i8_e32 v115, v125, v185
	s_waitcnt vmcnt(0)
	v_dot4c_i32_i8_e32 v103, v178, v182
	v_dot4c_i32_i8_e32 v103, v179, v183
	v_dot4c_i32_i8_e32 v103, v180, v184
	v_dot4c_i32_i8_e32 v27, v129, v185
	v_dot4c_i32_i8_e32 v114, v133, v185
	v_dot4c_i32_i8_e32 v113, v137, v185
	v_dot4c_i32_i8_e32 v112, v141, v185
	v_dot4c_i32_i8_e32 v111, v145, v185
	v_dot4c_i32_i8_e32 v110, v149, v185
	v_dot4c_i32_i8_e32 v109, v153, v185
	v_dot4c_i32_i8_e32 v108, v157, v185
	v_dot4c_i32_i8_e32 v26, v161, v185
	v_dot4c_i32_i8_e32 v107, v165, v185
	v_dot4c_i32_i8_e32 v106, v169, v185
	v_dot4c_i32_i8_e32 v105, v173, v185
	v_dot4c_i32_i8_e32 v104, v177, v185
	v_dot4c_i32_i8_e32 v103, v181, v185
	global_load_dwordx4 v[118:121], v202, s[60:61]
	global_load_dwordx4 v[122:125], v203, s[60:61]
	global_load_dwordx4 v[126:129], v204, s[60:61]
	global_load_dwordx4 v[130:133], v205, s[60:61]
	global_load_dwordx4 v[134:137], v206, s[60:61]
	global_load_dwordx4 v[138:141], v207, s[60:61]
	global_load_dwordx4 v[142:145], v208, s[60:61]
	global_load_dwordx4 v[146:149], v209, s[60:61]
	global_load_dwordx4 v[150:153], v210, s[60:61]
	global_load_dwordx4 v[154:157], v211, s[60:61]
	global_load_dwordx4 v[158:161], v212, s[60:61]
	global_load_dwordx4 v[162:165], v213, s[60:61]
	global_load_dwordx4 v[166:169], v214, s[60:61]
	global_load_dwordx4 v[170:173], v215, s[60:61]
	global_load_dwordx4 v[174:177], v216, s[60:61]
	global_load_dwordx4 v[178:181], v217, s[60:61]
	ds_read_b128 v[182:185], v117 offset:4096
	s_waitcnt lgkmcnt(0)
; #define LAS __attribute__((address_space(3)))
; __device__ __forceinline__ void peer_expert_phase(const Args& a, int layer, LAS unsigned char* lds, int G, int bid) {
;     ...
;             for (int i = 0; i < 4; ++i) {
;                 int tok = tb + i * NGW; tok = tok < NTOK ? tok : tb;
;                 const u32x4 xq = *(const LAS u32x4*)(X8 + i * 4096 + s * 128 + 16 * l7);
;                 u32x4 r[16];
; #pragma unroll
;                 for (int c = 0; c < 16; ++c) { const unsigned eo = (unsigned)__shfl((int)(c < 8 ? eoa[i] : eob[i]), (8 * c + g8) & 63); r[c] = *(const u32x4*)(pus + (eo + lo16)); }
; #pragma unroll
;                 for (int c = 0; c < 16; ++c) { int d = pacc[i][c];
; #pragma unroll
;                     for (int q = 0; q < 4; ++q) d = __builtin_amdgcn_sdot4((int)r[c][q], (int)xq[q], d, false);
;                     pacc[i][c] = d; }
	s_waitcnt vmcnt(15)
	v_dot4c_i32_i8_e32 v102, v118, v182
	s_waitcnt vmcnt(14)
	v_dot4c_i32_i8_e32 v101, v122, v182
	s_waitcnt vmcnt(13)
	v_dot4c_i32_i8_e32 v100, v126, v182
	s_waitcnt vmcnt(12)
	v_dot4c_i32_i8_e32 v99, v130, v182
	s_waitcnt vmcnt(11)
	v_dot4c_i32_i8_e32 v98, v134, v182
	s_waitcnt vmcnt(10)
	v_dot4c_i32_i8_e32 v97, v138, v182
	s_waitcnt vmcnt(9)
	v_dot4c_i32_i8_e32 v96, v142, v182
	s_waitcnt vmcnt(8)
	v_dot4c_i32_i8_e32 v95, v146, v182
	s_waitcnt vmcnt(7)
	v_dot4c_i32_i8_e32 v94, v150, v182
	s_waitcnt vmcnt(6)
	v_dot4c_i32_i8_e32 v93, v154, v182
	s_waitcnt vmcnt(5)
	v_dot4c_i32_i8_e32 v92, v158, v182
	v_dot4c_i32_i8_e32 v102, v119, v183
	v_dot4c_i32_i8_e32 v101, v123, v183
	v_dot4c_i32_i8_e32 v100, v127, v183
	v_dot4c_i32_i8_e32 v99, v131, v183
	v_dot4c_i32_i8_e32 v98, v135, v183
	v_dot4c_i32_i8_e32 v97, v139, v183
	v_dot4c_i32_i8_e32 v96, v143, v183
	v_dot4c_i32_i8_e32 v95, v147, v183
	v_dot4c_i32_i8_e32 v94, v151, v183
	v_dot4c_i32_i8_e32 v93, v155, v183
	v_dot4c_i32_i8_e32 v92, v159, v183
	v_dot4c_i32_i8_e32 v102, v120, v184
	v_dot4c_i32_i8_e32 v101, v124, v184
	v_dot4c_i32_i8_e32 v100, v128, v184
	v_dot4c_i32_i8_e32 v99, v132, v184
	v_dot4c_i32_i8_e32 v98, v136, v184
	v_dot4c_i32_i8_e32 v97, v140, v184
	v_dot4c_i32_i8_e32 v96, v144, v184
	v_dot4c_i32_i8_e32 v95, v148, v184
	v_dot4c_i32_i8_e32 v94, v152, v184
	v_dot4c_i32_i8_e32 v93, v156, v184
	v_dot4c_i32_i8_e32 v92, v160, v184
	v_dot4c_i32_i8_e32 v102, v121, v185
	v_dot4c_i32_i8_e32 v101, v125, v185
	v_dot4c_i32_i8_e32 v100, v129, v185
	v_dot4c_i32_i8_e32 v99, v133, v185
	v_dot4c_i32_i8_e32 v98, v137, v185
	v_dot4c_i32_i8_e32 v97, v141, v185
	v_dot4c_i32_i8_e32 v96, v145, v185
	v_dot4c_i32_i8_e32 v95, v149, v185
	v_dot4c_i32_i8_e32 v94, v153, v185
	v_dot4c_i32_i8_e32 v93, v157, v185
	v_dot4c_i32_i8_e32 v92, v161, v185
	s_waitcnt vmcnt(4)
	v_dot4c_i32_i8_e32 v89, v162, v182
	v_dot4c_i32_i8_e32 v89, v163, v183
	s_waitcnt vmcnt(3)
	v_dot4c_i32_i8_e32 v91, v166, v182
	v_dot4c_i32_i8_e32 v91, v167, v183
	s_waitcnt vmcnt(2)
	v_dot4c_i32_i8_e32 v90, v170, v182
	v_dot4c_i32_i8_e32 v90, v171, v183
	s_waitcnt vmcnt(1)
	v_dot4c_i32_i8_e32 v88, v174, v182
	v_dot4c_i32_i8_e32 v88, v175, v183
	s_waitcnt vmcnt(0)
	v_dot4c_i32_i8_e32 v87, v178, v182
	v_dot4c_i32_i8_e32 v87, v179, v183
	v_dot4c_i32_i8_e32 v89, v164, v184
	v_dot4c_i32_i8_e32 v91, v168, v184
	v_dot4c_i32_i8_e32 v90, v172, v184
	v_dot4c_i32_i8_e32 v88, v176, v184
	v_dot4c_i32_i8_e32 v87, v180, v184
	v_dot4c_i32_i8_e32 v89, v165, v185
	v_dot4c_i32_i8_e32 v91, v169, v185
	v_dot4c_i32_i8_e32 v90, v173, v185
	v_dot4c_i32_i8_e32 v88, v177, v185
	v_dot4c_i32_i8_e32 v87, v181, v185
	global_load_dwordx4 v[118:121], v218, s[60:61]
	global_load_dwordx4 v[122:125], v219, s[60:61]
	global_load_dwordx4 v[126:129], v220, s[60:61]
	global_load_dwordx4 v[130:133], v221, s[60:61]
	global_load_dwordx4 v[134:137], v222, s[60:61]
	global_load_dwordx4 v[138:141], v223, s[60:61]
	global_load_dwordx4 v[142:145], v224, s[60:61]
	global_load_dwordx4 v[146:149], v225, s[60:61]
	global_load_dwordx4 v[150:153], v226, s[60:61]
	global_load_dwordx4 v[154:157], v227, s[60:61]
	global_load_dwordx4 v[158:161], v229, s[60:61]
	global_load_dwordx4 v[162:165], v230, s[60:61]
	global_load_dwordx4 v[166:169], v231, s[60:61]
	global_load_dwordx4 v[170:173], v232, s[60:61]
	global_load_dwordx4 v[174:177], v233, s[60:61]
	global_load_dwordx4 v[178:181], v234, s[60:61]
	ds_read_b128 v[182:185], v117 offset:8192
	s_waitcnt lgkmcnt(0)
	s_waitcnt vmcnt(15)
	v_dot4c_i32_i8_e32 v86, v118, v182
	s_waitcnt vmcnt(14)
	v_dot4c_i32_i8_e32 v85, v122, v182
	s_waitcnt vmcnt(13)
	v_dot4c_i32_i8_e32 v84, v126, v182
	s_waitcnt vmcnt(12)
	v_dot4c_i32_i8_e32 v83, v130, v182
	s_waitcnt vmcnt(11)
	v_dot4c_i32_i8_e32 v82, v134, v182
	s_waitcnt vmcnt(10)
	v_dot4c_i32_i8_e32 v81, v138, v182
	s_waitcnt vmcnt(9)
	v_dot4c_i32_i8_e32 v80, v142, v182
	s_waitcnt vmcnt(8)
	v_dot4c_i32_i8_e32 v79, v146, v182
	s_waitcnt vmcnt(7)
	v_dot4c_i32_i8_e32 v78, v150, v182
	s_waitcnt vmcnt(6)
	v_dot4c_i32_i8_e32 v77, v154, v182
	s_waitcnt vmcnt(5)
	v_dot4c_i32_i8_e32 v76, v158, v182
	v_dot4c_i32_i8_e32 v86, v119, v183
	v_dot4c_i32_i8_e32 v85, v123, v183
	v_dot4c_i32_i8_e32 v84, v127, v183
	v_dot4c_i32_i8_e32 v83, v131, v183
	v_dot4c_i32_i8_e32 v82, v135, v183
	v_dot4c_i32_i8_e32 v81, v139, v183
	v_dot4c_i32_i8_e32 v80, v143, v183
	v_dot4c_i32_i8_e32 v79, v147, v183
	v_dot4c_i32_i8_e32 v78, v151, v183
	v_dot4c_i32_i8_e32 v77, v155, v183
	v_dot4c_i32_i8_e32 v76, v159, v183
	v_dot4c_i32_i8_e32 v86, v120, v184
	v_dot4c_i32_i8_e32 v85, v124, v184
	v_dot4c_i32_i8_e32 v84, v128, v184
	v_dot4c_i32_i8_e32 v83, v132, v184
	v_dot4c_i32_i8_e32 v82, v136, v184
	v_dot4c_i32_i8_e32 v81, v140, v184
	v_dot4c_i32_i8_e32 v80, v144, v184
	v_dot4c_i32_i8_e32 v79, v148, v184
	v_dot4c_i32_i8_e32 v78, v152, v184
	v_dot4c_i32_i8_e32 v77, v156, v184
	v_dot4c_i32_i8_e32 v76, v160, v184
	v_dot4c_i32_i8_e32 v86, v121, v185
	v_dot4c_i32_i8_e32 v85, v125, v185
	v_dot4c_i32_i8_e32 v84, v129, v185
	v_dot4c_i32_i8_e32 v83, v133, v185
	v_dot4c_i32_i8_e32 v82, v137, v185
	v_dot4c_i32_i8_e32 v81, v141, v185
	v_dot4c_i32_i8_e32 v80, v145, v185
	v_dot4c_i32_i8_e32 v79, v149, v185
	v_dot4c_i32_i8_e32 v78, v153, v185
	v_dot4c_i32_i8_e32 v77, v157, v185
	v_dot4c_i32_i8_e32 v76, v161, v185
	s_waitcnt vmcnt(4)
	v_dot4c_i32_i8_e32 v75, v162, v182
	v_dot4c_i32_i8_e32 v75, v163, v183
	s_waitcnt vmcnt(3)
	v_dot4c_i32_i8_e32 v74, v166, v182
	v_dot4c_i32_i8_e32 v74, v167, v183
	s_waitcnt vmcnt(2)
	v_dot4c_i32_i8_e32 v73, v170, v182
	v_dot4c_i32_i8_e32 v73, v171, v183
	s_waitcnt vmcnt(1)
	v_dot4c_i32_i8_e32 v72, v174, v182
	v_dot4c_i32_i8_e32 v72, v175, v183
	s_waitcnt vmcnt(0)
; #define LAS __attribute__((address_space(3)))
; __device__ __forceinline__ void peer_expert_phase(const Args& a, int layer, LAS unsigned char* lds, int G, int bid) {
;     ...
;             for (int i = 0; i < 4; ++i) {
;                 int tok = tb + i * NGW; tok = tok < NTOK ? tok : tb;
;                 const u32x4 xq = *(const LAS u32x4*)(X8 + i * 4096 + s * 128 + 16 * l7);
;                 u32x4 r[16];
; #pragma unroll
;                 for (int c = 0; c < 16; ++c) { const unsigned eo = (unsigned)__shfl((int)(c < 8 ? eoa[i] : eob[i]), (8 * c + g8) & 63); r[c] = *(const u32x4*)(pus + (eo + lo16)); }
; #pragma unroll
;                 for (int c = 0; c < 16; ++c) { int d = pacc[i][c];
; #pragma unroll
;                     for (int q = 0; q < 4; ++q) d = __builtin_amdgcn_sdot4((int)r[c][q], (int)xq[q], d, false);
;                     pacc[i][c] = d; }
;                 __builtin_amdgcn_sched_barrier(0);
;             }
;         }
;         float pa[4], pb[4];
; #pragma unroll
;         for (int i = 0; i < 4; ++i) { pa[i] = 0.f; pb[i] = 0.f;
; #pragma unroll
;             for (int c = 0; c < 16; ++c) { float v = (float)pacc[i][c]; v += __shfl_xor(v, 1); v += __shfl_xor(v, 2); v += __shfl_xor(v, 4);
;                 const float t = __shfl(v, 8 * (lane & 7));
;                 if (c < 8) pa[i] = (g8 == c) ? t : pa[i]; else pb[i] = (g8 == c - 8) ? t : pb[i]; } }
	v_dot4c_i32_i8_e32 v71, v178, v182
	v_dot4c_i32_i8_e32 v71, v179, v183
	v_dot4c_i32_i8_e32 v75, v164, v184
	v_dot4c_i32_i8_e32 v74, v168, v184
	v_dot4c_i32_i8_e32 v73, v172, v184
	v_dot4c_i32_i8_e32 v72, v176, v184
	v_dot4c_i32_i8_e32 v71, v180, v184
	v_dot4c_i32_i8_e32 v75, v165, v185
	v_dot4c_i32_i8_e32 v74, v169, v185
	v_dot4c_i32_i8_e32 v73, v173, v185
	v_dot4c_i32_i8_e32 v72, v177, v185
	v_dot4c_i32_i8_e32 v71, v181, v185
	global_load_dwordx4 v[118:121], v235, s[60:61]
	global_load_dwordx4 v[122:125], v236, s[60:61]
	global_load_dwordx4 v[126:129], v237, s[60:61]
	global_load_dwordx4 v[130:133], v238, s[60:61]
	global_load_dwordx4 v[134:137], v239, s[60:61]
	global_load_dwordx4 v[138:141], v240, s[60:61]
	global_load_dwordx4 v[142:145], v241, s[60:61]
	global_load_dwordx4 v[146:149], v242, s[60:61]
	global_load_dwordx4 v[150:153], v243, s[60:61]
	global_load_dwordx4 v[154:157], v244, s[60:61]
	global_load_dwordx4 v[158:161], v245, s[60:61]
	global_load_dwordx4 v[162:165], v246, s[60:61]
	global_load_dwordx4 v[166:169], v247, s[60:61]
	global_load_dwordx4 v[170:173], v248, s[60:61]
	global_load_dwordx4 v[174:177], v249, s[60:61]
	global_load_dwordx4 v[178:181], v250, s[60:61]
	ds_read_b128 v[182:185], v117 offset:12288
	s_waitcnt lgkmcnt(0)
	s_waitcnt vmcnt(15)
	v_dot4c_i32_i8_e32 v70, v118, v182
	s_waitcnt vmcnt(14)
	v_dot4c_i32_i8_e32 v69, v122, v182
	s_waitcnt vmcnt(13)
	v_dot4c_i32_i8_e32 v68, v126, v182
	s_waitcnt vmcnt(12)
	v_dot4c_i32_i8_e32 v67, v130, v182
	s_waitcnt vmcnt(11)
	v_dot4c_i32_i8_e32 v66, v134, v182
	s_waitcnt vmcnt(10)
	v_dot4c_i32_i8_e32 v65, v138, v182
	s_waitcnt vmcnt(9)
	v_dot4c_i32_i8_e32 v64, v142, v182
	s_waitcnt vmcnt(8)
	v_dot4c_i32_i8_e32 v63, v146, v182
	s_waitcnt vmcnt(7)
	v_dot4c_i32_i8_e32 v62, v150, v182
	s_waitcnt vmcnt(6)
	v_dot4c_i32_i8_e32 v61, v154, v182
	s_waitcnt vmcnt(5)
	v_dot4c_i32_i8_e32 v60, v158, v182
	v_dot4c_i32_i8_e32 v70, v119, v183
	v_dot4c_i32_i8_e32 v69, v123, v183
	v_dot4c_i32_i8_e32 v68, v127, v183
	v_dot4c_i32_i8_e32 v67, v131, v183
	v_dot4c_i32_i8_e32 v66, v135, v183
	v_dot4c_i32_i8_e32 v65, v139, v183
	v_dot4c_i32_i8_e32 v64, v143, v183
	v_dot4c_i32_i8_e32 v63, v147, v183
	v_dot4c_i32_i8_e32 v62, v151, v183
	v_dot4c_i32_i8_e32 v61, v155, v183
	v_dot4c_i32_i8_e32 v60, v159, v183
	v_dot4c_i32_i8_e32 v70, v120, v184
	v_dot4c_i32_i8_e32 v69, v124, v184
	v_dot4c_i32_i8_e32 v68, v128, v184
	v_dot4c_i32_i8_e32 v67, v132, v184
	v_dot4c_i32_i8_e32 v66, v136, v184
	v_dot4c_i32_i8_e32 v65, v140, v184
	v_dot4c_i32_i8_e32 v64, v144, v184
	v_dot4c_i32_i8_e32 v63, v148, v184
	v_dot4c_i32_i8_e32 v62, v152, v184
	v_dot4c_i32_i8_e32 v61, v156, v184
	v_dot4c_i32_i8_e32 v60, v160, v184
	v_dot4c_i32_i8_e32 v70, v121, v185
	v_dot4c_i32_i8_e32 v69, v125, v185
	v_dot4c_i32_i8_e32 v68, v129, v185
	v_dot4c_i32_i8_e32 v67, v133, v185
	v_dot4c_i32_i8_e32 v66, v137, v185
	v_dot4c_i32_i8_e32 v65, v141, v185
	v_dot4c_i32_i8_e32 v64, v145, v185
	v_dot4c_i32_i8_e32 v63, v149, v185
	v_dot4c_i32_i8_e32 v62, v153, v185
	v_dot4c_i32_i8_e32 v61, v157, v185
	v_dot4c_i32_i8_e32 v60, v161, v185
	s_waitcnt vmcnt(4)
	v_dot4c_i32_i8_e32 v59, v162, v182
	v_dot4c_i32_i8_e32 v59, v163, v183
	s_waitcnt vmcnt(3)
	v_dot4c_i32_i8_e32 v19, v166, v182
	v_dot4c_i32_i8_e32 v19, v167, v183
	s_waitcnt vmcnt(2)
	v_dot4c_i32_i8_e32 v23, v170, v182
	v_dot4c_i32_i8_e32 v23, v171, v183
	s_waitcnt vmcnt(1)
	v_dot4c_i32_i8_e32 v21, v174, v182
	v_dot4c_i32_i8_e32 v21, v175, v183
	s_waitcnt vmcnt(0)
	v_dot4c_i32_i8_e32 v7, v178, v182
	v_dot4c_i32_i8_e32 v7, v179, v183
	v_dot4c_i32_i8_e32 v59, v164, v184
	v_dot4c_i32_i8_e32 v19, v168, v184
	v_dot4c_i32_i8_e32 v23, v172, v184
	v_dot4c_i32_i8_e32 v21, v176, v184
	v_dot4c_i32_i8_e32 v7, v180, v184
	v_dot4c_i32_i8_e32 v59, v165, v185
	v_dot4c_i32_i8_e32 v19, v169, v185
	v_dot4c_i32_i8_e32 v23, v173, v185
	v_dot4c_i32_i8_e32 v21, v177, v185
	v_dot4c_i32_i8_e32 v7, v181, v185
	s_addk_i32 s40, 0x80
	s_cmpk_eq_i32 s40, 0x1000
	s_cbranch_scc0 .LBB0_2267
	v_cvt_f32_i32_e32 v116, v116
	v_cvt_f32_i32_e32 v115, v115
	v_cvt_f32_i32_e32 v119, v27
	v_mul_f32_e32 v27, 0x3c010204, v3
	ds_bpermute_b32 v117, v34, v116
	ds_bpermute_b32 v118, v34, v115
	v_cvt_f32_i32_e32 v3, v114
	ds_bpermute_b32 v114, v34, v119
	v_cvt_f32_i32_e32 v112, v112
	s_waitcnt lgkmcnt(2)
	v_add_f32_e32 v116, v116, v117
	s_waitcnt lgkmcnt(1)
	v_add_f32_e32 v115, v115, v118
	ds_bpermute_b32 v117, v33, v116
	ds_bpermute_b32 v118, v33, v115
	ds_bpermute_b32 v120, v34, v3
	s_waitcnt lgkmcnt(3)
	v_add_f32_e32 v114, v119, v114
	ds_bpermute_b32 v119, v33, v114
	s_waitcnt lgkmcnt(3)
	v_add_f32_e32 v116, v116, v117
	s_waitcnt lgkmcnt(2)
	v_add_f32_e32 v115, v115, v118
	ds_bpermute_b32 v117, v32, v116
	ds_bpermute_b32 v118, v32, v115
	s_waitcnt lgkmcnt(3)
	v_add_f32_e32 v3, v3, v120
	s_waitcnt lgkmcnt(2)
	v_add_f32_e32 v114, v114, v119
	v_cvt_f32_i32_e32 v113, v113
	s_waitcnt lgkmcnt(1)
	v_add_f32_e32 v116, v116, v117
	s_waitcnt lgkmcnt(0)
	v_add_f32_e32 v115, v115, v118
	ds_bpermute_b32 v116, v37, v116
	ds_bpermute_b32 v118, v33, v3
	ds_bpermute_b32 v115, v37, v115
	ds_bpermute_b32 v117, v32, v114
	ds_bpermute_b32 v119, v34, v113
	s_waitcnt lgkmcnt(4)
	v_cndmask_b32_e64 v116, 0, v116, s[6:7]
	s_waitcnt lgkmcnt(3)
	v_add_f32_e32 v3, v3, v118
	s_waitcnt lgkmcnt(2)
	v_cndmask_b32_e64 v115, v116, v115, s[8:9]
	ds_bpermute_b32 v116, v32, v3
	s_waitcnt lgkmcnt(2)
	v_add_f32_e32 v114, v114, v117
	ds_bpermute_b32 v114, v37, v114
	s_waitcnt lgkmcnt(2)
	v_add_f32_e32 v113, v113, v119
	ds_bpermute_b32 v117, v33, v113
	s_waitcnt lgkmcnt(2)
	v_add_f32_e32 v3, v3, v116
	ds_bpermute_b32 v116, v34, v112
	ds_bpermute_b32 v3, v37, v3
	s_waitcnt lgkmcnt(3)
; __device__ __forceinline__ void peer_expert_phase(const Args& a, int layer, LAS unsigned char* lds, int G, int bid) {
;     ...
;         float pa[4], pb[4];
; #pragma unroll
;         for (int i = 0; i < 4; ++i) { pa[i] = 0.f; pb[i] = 0.f;
; #pragma unroll
;             for (int c = 0; c < 16; ++c) { float v = (float)pacc[i][c]; v += __shfl_xor(v, 1); v += __shfl_xor(v, 2); v += __shfl_xor(v, 4);
;                 const float t = __shfl(v, 8 * (lane & 7));
;                 if (c < 8) pa[i] = (g8 == c) ? t : pa[i]; else pb[i] = (g8 == c - 8) ? t : pb[i]; } }
	v_cndmask_b32_e64 v114, v115, v114, s[10:11]
	v_cvt_f32_i32_e32 v110, v110
	s_waitcnt lgkmcnt(2)
	v_add_f32_e32 v113, v113, v117
	s_waitcnt lgkmcnt(1)
	v_add_f32_e32 v112, v112, v116
	ds_bpermute_b32 v116, v33, v112
	s_waitcnt lgkmcnt(1)
	v_cndmask_b32_e64 v3, v114, v3, s[12:13]
	v_cvt_f32_i32_e32 v111, v111
	ds_bpermute_b32 v117, v32, v113
	v_cvt_f32_i32_e32 v109, v109
	s_waitcnt lgkmcnt(1)
	v_add_f32_e32 v112, v112, v116
	ds_bpermute_b32 v114, v32, v112
	ds_bpermute_b32 v115, v34, v111
	s_waitcnt lgkmcnt(2)
	v_add_f32_e32 v113, v113, v117
	ds_bpermute_b32 v113, v37, v113
	v_cvt_f32_i32_e32 v108, v108
	s_waitcnt lgkmcnt(2)
	v_add_f32_e32 v112, v112, v114
	ds_bpermute_b32 v114, v34, v110
	ds_bpermute_b32 v112, v37, v112
	s_waitcnt lgkmcnt(3)
	v_add_f32_e32 v111, v111, v115
	ds_bpermute_b32 v115, v33, v111
	s_waitcnt lgkmcnt(3)
	v_cndmask_b32_e64 v3, v3, v113, s[14:15]
	s_waitcnt lgkmcnt(2)
	v_add_f32_e32 v110, v110, v114
	ds_bpermute_b32 v114, v33, v110
	ds_bpermute_b32 v113, v34, v109
	s_waitcnt lgkmcnt(3)
	v_cndmask_b32_e64 v3, v3, v112, s[16:17]
	s_waitcnt lgkmcnt(2)
	v_add_f32_e32 v111, v111, v115
	ds_bpermute_b32 v115, v32, v111
	s_waitcnt lgkmcnt(2)
	v_add_f32_e32 v110, v110, v114
	ds_bpermute_b32 v112, v32, v110
	s_waitcnt lgkmcnt(2)
	v_add_f32_e32 v109, v109, v113
	ds_bpermute_b32 v113, v33, v109
	s_waitcnt lgkmcnt(2)
	v_add_f32_e32 v111, v111, v115
	ds_bpermute_b32 v111, v37, v111
	s_waitcnt lgkmcnt(2)
	v_add_f32_e32 v110, v110, v112
	ds_bpermute_b32 v112, v34, v108
	v_cvt_f32_i32_e32 v114, v26
	s_waitcnt lgkmcnt(2)
	v_add_f32_e32 v109, v109, v113
	ds_bpermute_b32 v110, v37, v110
	ds_bpermute_b32 v113, v32, v109
	s_waitcnt lgkmcnt(2)
	v_add_f32_e32 v108, v108, v112
	ds_bpermute_b32 v112, v33, v108
	v_cndmask_b32_e64 v3, v3, v111, s[18:19]
	ds_bpermute_b32 v111, v34, v114
	s_waitcnt lgkmcnt(3)
	v_cndmask_b32_e64 v26, v3, v110, s[20:21]
	s_waitcnt lgkmcnt(2)
	v_add_f32_e32 v3, v109, v113
	s_waitcnt lgkmcnt(1)
	v_add_f32_e32 v108, v108, v112
	ds_bpermute_b32 v109, v32, v108
	s_waitcnt lgkmcnt(1)
	v_add_f32_e32 v110, v114, v111
	ds_bpermute_b32 v111, v33, v110
	v_cvt_f32_i32_e32 v112, v107
	ds_bpermute_b32 v107, v37, v3
	s_waitcnt lgkmcnt(2)
	v_add_f32_e32 v3, v108, v109
	v_cvt_f32_i32_e32 v108, v106
	ds_bpermute_b32 v109, v34, v112
	s_waitcnt lgkmcnt(2)
	v_add_f32_e32 v110, v110, v111
	ds_bpermute_b32 v111, v32, v110
	ds_bpermute_b32 v113, v34, v108
	ds_bpermute_b32 v106, v37, v3
	s_waitcnt lgkmcnt(3)
	v_add_f32_e32 v3, v112, v109
	ds_bpermute_b32 v109, v33, v3
	s_waitcnt lgkmcnt(3)
	v_add_f32_e32 v110, v110, v111
	s_waitcnt lgkmcnt(2)
	v_add_f32_e32 v111, v108, v113
	ds_bpermute_b32 v112, v33, v111
	v_cvt_f32_i32_e32 v105, v105
	s_waitcnt lgkmcnt(1)
	v_add_f32_e32 v3, v3, v109
	ds_bpermute_b32 v108, v37, v110
	ds_bpermute_b32 v109, v32, v3
	s_waitcnt lgkmcnt(2)
	v_add_f32_e32 v110, v111, v112
	ds_bpermute_b32 v113, v34, v105
	ds_bpermute_b32 v112, v32, v110
	v_cvt_f32_i32_e32 v104, v104
	s_waitcnt lgkmcnt(2)
	v_add_f32_e32 v3, v3, v109
	ds_bpermute_b32 v111, v37, v3
	s_waitcnt lgkmcnt(2)
	v_add_f32_e32 v105, v105, v113
	ds_bpermute_b32 v109, v34, v104
	s_waitcnt lgkmcnt(2)
	v_add_f32_e32 v3, v110, v112
	ds_bpermute_b32 v110, v33, v105
	v_cvt_f32_i32_e32 v103, v103
	ds_bpermute_b32 v115, v37, v3
	s_waitcnt lgkmcnt(2)
	v_add_f32_e32 v104, v104, v109
	ds_bpermute_b32 v109, v33, v104
	s_waitcnt lgkmcnt(2)
	v_add_f32_e32 v3, v105, v110
	ds_bpermute_b32 v105, v34, v103
	ds_bpermute_b32 v110, v32, v3
	v_cvt_f32_i32_e32 v102, v102
	s_waitcnt lgkmcnt(2)
	v_add_f32_e32 v104, v104, v109
	ds_bpermute_b32 v109, v32, v104
	s_waitcnt lgkmcnt(2)
	v_add_f32_e32 v103, v103, v105
	ds_bpermute_b32 v105, v33, v103
	s_waitcnt lgkmcnt(2)
	v_add_f32_e32 v3, v3, v110
	ds_bpermute_b32 v110, v34, v102
	ds_bpermute_b32 v116, v37, v3
	s_waitcnt lgkmcnt(3)
	v_add_f32_e32 v3, v104, v109
	s_waitcnt lgkmcnt(2)
	v_add_f32_e32 v103, v103, v105
	ds_bpermute_b32 v104, v32, v103
	s_waitcnt lgkmcnt(2)
	v_add_f32_e32 v102, v102, v110
	v_cvt_f32_i32_e32 v101, v101
	ds_bpermute_b32 v105, v33, v102
	v_cvt_f32_i32_e32 v100, v100
	ds_bpermute_b32 v117, v37, v3
	s_waitcnt lgkmcnt(2)
	v_add_f32_e32 v3, v103, v104
	ds_bpermute_b32 v103, v34, v101
	s_waitcnt lgkmcnt(2)
	v_add_f32_e32 v102, v102, v105
	ds_bpermute_b32 v105, v34, v100
	ds_bpermute_b32 v104, v32, v102
	ds_bpermute_b32 v118, v37, v3
	s_waitcnt lgkmcnt(3)
	v_add_f32_e32 v3, v101, v103
	ds_bpermute_b32 v101, v33, v3
	s_waitcnt lgkmcnt(3)
	v_add_f32_e32 v103, v100, v105
	s_waitcnt lgkmcnt(2)
	v_add_f32_e32 v102, v102, v104
	ds_bpermute_b32 v104, v33, v103
	v_cvt_f32_i32_e32 v99, v99
	s_waitcnt lgkmcnt(1)
	v_add_f32_e32 v3, v3, v101
	ds_bpermute_b32 v101, v32, v3
	ds_bpermute_b32 v100, v37, v102
	s_waitcnt lgkmcnt(2)
	v_add_f32_e32 v102, v103, v104
	v_cvt_f32_i32_e32 v103, v98
	ds_bpermute_b32 v105, v34, v99
	ds_bpermute_b32 v104, v32, v102
	s_waitcnt lgkmcnt(3)
	v_add_f32_e32 v3, v3, v101
	ds_bpermute_b32 v101, v34, v103
	ds_bpermute_b32 v98, v37, v3
	s_waitcnt lgkmcnt(3)
	v_add_f32_e32 v99, v99, v105
	s_waitcnt lgkmcnt(2)
	v_add_f32_e32 v3, v102, v104
	ds_bpermute_b32 v102, v33, v99
	s_waitcnt lgkmcnt(2)
	v_add_f32_e32 v101, v103, v101
	v_cvt_f32_i32_e32 v103, v97
	ds_bpermute_b32 v97, v37, v3
	ds_bpermute_b32 v104, v33, v101
	s_waitcnt lgkmcnt(2)
	v_add_f32_e32 v3, v99, v102
	ds_bpermute_b32 v99, v34, v103
	ds_bpermute_b32 v102, v32, v3
	v_cvt_f32_i32_e32 v105, v96
	s_waitcnt lgkmcnt(2)
	v_add_f32_e32 v101, v101, v104
	ds_bpermute_b32 v104, v32, v101
	s_waitcnt lgkmcnt(2)
	v_add_f32_e32 v99, v103, v99
	ds_bpermute_b32 v103, v33, v99
	s_waitcnt lgkmcnt(2)
	v_add_f32_e32 v3, v3, v102
	ds_bpermute_b32 v102, v34, v105
	ds_bpermute_b32 v96, v37, v3
	s_waitcnt lgkmcnt(3)
; __device__ __forceinline__ void peer_expert_phase(const Args& a, int layer, LAS unsigned char* lds, int G, int bid) {
;     ...
;         float pa[4], pb[4];
; #pragma unroll
;         for (int i = 0; i < 4; ++i) { pa[i] = 0.f; pb[i] = 0.f;
; #pragma unroll
;             for (int c = 0; c < 16; ++c) { float v = (float)pacc[i][c]; v += __shfl_xor(v, 1); v += __shfl_xor(v, 2); v += __shfl_xor(v, 4);
;                 const float t = __shfl(v, 8 * (lane & 7));
;                 if (c < 8) pa[i] = (g8 == c) ? t : pa[i]; else pb[i] = (g8 == c - 8) ? t : pb[i]; } }
	v_add_f32_e32 v3, v101, v104
	s_waitcnt lgkmcnt(2)
	v_add_f32_e32 v99, v99, v103
	ds_bpermute_b32 v101, v32, v99
	v_cvt_f32_i32_e32 v104, v95
	s_waitcnt lgkmcnt(2)
	v_add_f32_e32 v102, v105, v102
	ds_bpermute_b32 v103, v33, v102
	ds_bpermute_b32 v95, v37, v3
	s_waitcnt lgkmcnt(2)
	v_add_f32_e32 v3, v99, v101
	v_cvt_f32_i32_e32 v94, v94
	ds_bpermute_b32 v99, v34, v104
	s_waitcnt lgkmcnt(2)
	v_add_f32_e32 v101, v102, v103
	ds_bpermute_b32 v102, v32, v101
	ds_bpermute_b32 v105, v34, v94
	ds_bpermute_b32 v103, v37, v3
	s_waitcnt lgkmcnt(3)
	v_add_f32_e32 v3, v104, v99
	ds_bpermute_b32 v99, v33, v3
	s_waitcnt lgkmcnt(3)
	v_add_f32_e32 v101, v101, v102
	s_waitcnt lgkmcnt(2)
	v_add_f32_e32 v94, v94, v105
	ds_bpermute_b32 v102, v33, v94
	v_cvt_f32_i32_e32 v93, v93
	s_waitcnt lgkmcnt(1)
	v_add_f32_e32 v3, v3, v99
	ds_bpermute_b32 v99, v32, v3
	v_cvt_f32_i32_e32 v92, v92
	s_waitcnt lgkmcnt(1)
	v_add_f32_e32 v94, v94, v102
	ds_bpermute_b32 v102, v34, v93
	ds_bpermute_b32 v105, v37, v101
	ds_bpermute_b32 v101, v32, v94
	s_waitcnt lgkmcnt(3)
	v_add_f32_e32 v3, v3, v99
	ds_bpermute_b32 v99, v34, v92
	s_waitcnt lgkmcnt(3)
	v_add_f32_e32 v93, v93, v102
	ds_bpermute_b32 v109, v37, v3
	s_waitcnt lgkmcnt(2)
	v_add_f32_e32 v3, v94, v101
	ds_bpermute_b32 v94, v33, v93
	s_waitcnt lgkmcnt(2)
	v_add_f32_e32 v92, v92, v99
	v_cvt_f32_i32_e32 v99, v89
	ds_bpermute_b32 v101, v33, v92
	ds_bpermute_b32 v89, v37, v3
	s_waitcnt lgkmcnt(2)
	v_add_f32_e32 v3, v93, v94
	ds_bpermute_b32 v93, v34, v99
	ds_bpermute_b32 v94, v32, v3
	s_waitcnt lgkmcnt(3)
	v_add_f32_e32 v92, v92, v101
	v_cvt_f32_i32_e32 v102, v91
	ds_bpermute_b32 v101, v32, v92
	s_waitcnt lgkmcnt(2)
	v_add_f32_e32 v93, v99, v93
	ds_bpermute_b32 v99, v33, v93
	s_waitcnt lgkmcnt(2)
	v_add_f32_e32 v3, v3, v94
	ds_bpermute_b32 v94, v34, v102
	ds_bpermute_b32 v91, v37, v3
	s_waitcnt lgkmcnt(3)
	v_add_f32_e32 v3, v92, v101
	s_waitcnt lgkmcnt(2)
	v_add_f32_e32 v92, v93, v99
	ds_bpermute_b32 v93, v32, v92
	s_waitcnt lgkmcnt(2)
	v_add_f32_e32 v94, v102, v94
	ds_bpermute_b32 v99, v33, v94
	v_cvt_f32_i32_e32 v101, v90
	ds_bpermute_b32 v90, v37, v3
	s_waitcnt lgkmcnt(2)
	v_add_f32_e32 v3, v92, v93
	v_cvt_f32_i32_e32 v92, v88
	ds_bpermute_b32 v93, v34, v101
	s_waitcnt lgkmcnt(2)
	v_add_f32_e32 v94, v94, v99
	ds_bpermute_b32 v99, v32, v94
	ds_bpermute_b32 v102, v34, v92
	ds_bpermute_b32 v88, v37, v3
	s_waitcnt lgkmcnt(3)
	v_add_f32_e32 v3, v101, v93
	ds_bpermute_b32 v93, v33, v3
	s_waitcnt lgkmcnt(3)
	v_add_f32_e32 v94, v94, v99
	s_waitcnt lgkmcnt(2)
	v_add_f32_e32 v99, v92, v102
	ds_bpermute_b32 v101, v33, v99
	v_cvt_f32_i32_e32 v87, v87
	s_waitcnt lgkmcnt(1)
	v_add_f32_e32 v3, v3, v93
	ds_bpermute_b32 v92, v37, v94
	ds_bpermute_b32 v93, v32, v3
	s_waitcnt lgkmcnt(2)
	v_add_f32_e32 v94, v99, v101
	ds_bpermute_b32 v101, v34, v87
	ds_bpermute_b32 v99, v32, v94
	v_cvt_f32_i32_e32 v86, v86
	s_waitcnt lgkmcnt(2)
	v_add_f32_e32 v3, v3, v93
	ds_bpermute_b32 v104, v37, v3
	s_waitcnt lgkmcnt(2)
	v_add_f32_e32 v87, v87, v101
	ds_bpermute_b32 v93, v34, v86
	s_waitcnt lgkmcnt(2)
	v_add_f32_e32 v3, v94, v99
	ds_bpermute_b32 v94, v33, v87
	v_cvt_f32_i32_e32 v85, v85
	ds_bpermute_b32 v110, v37, v3
	s_waitcnt lgkmcnt(2)
	v_add_f32_e32 v86, v86, v93
	ds_bpermute_b32 v93, v33, v86
	s_waitcnt lgkmcnt(2)
	v_add_f32_e32 v3, v87, v94
	ds_bpermute_b32 v87, v34, v85
	ds_bpermute_b32 v94, v32, v3
	v_cvt_f32_i32_e32 v84, v84
	s_waitcnt lgkmcnt(2)
	v_add_f32_e32 v86, v86, v93
	ds_bpermute_b32 v93, v32, v86
	s_waitcnt lgkmcnt(2)
	v_add_f32_e32 v85, v85, v87
	ds_bpermute_b32 v87, v33, v85
	s_waitcnt lgkmcnt(2)
	v_add_f32_e32 v3, v3, v94
	ds_bpermute_b32 v94, v34, v84
	ds_bpermute_b32 v112, v37, v3
	s_waitcnt lgkmcnt(3)
	v_add_f32_e32 v3, v86, v93
	s_waitcnt lgkmcnt(2)
	v_add_f32_e32 v85, v85, v87
	ds_bpermute_b32 v86, v32, v85
	s_waitcnt lgkmcnt(2)
	v_add_f32_e32 v84, v84, v94
	v_cvt_f32_i32_e32 v93, v83
	ds_bpermute_b32 v87, v33, v84
	ds_bpermute_b32 v83, v37, v3
	s_waitcnt lgkmcnt(2)
	v_add_f32_e32 v3, v85, v86
	v_cvt_f32_i32_e32 v85, v82
	ds_bpermute_b32 v86, v34, v93
	s_waitcnt lgkmcnt(2)
	v_add_f32_e32 v84, v84, v87
	ds_bpermute_b32 v87, v32, v84
	ds_bpermute_b32 v94, v34, v85
	ds_bpermute_b32 v82, v37, v3
	s_waitcnt lgkmcnt(3)
	v_add_f32_e32 v3, v93, v86
	ds_bpermute_b32 v86, v33, v3
	s_waitcnt lgkmcnt(3)
	v_add_f32_e32 v84, v84, v87
	s_waitcnt lgkmcnt(2)
	v_add_f32_e32 v85, v85, v94
	ds_bpermute_b32 v87, v33, v85
	v_cvt_f32_i32_e32 v81, v81
	s_waitcnt lgkmcnt(1)
	v_add_f32_e32 v3, v3, v86
	ds_bpermute_b32 v86, v32, v3
	v_cvt_f32_i32_e32 v76, v76
	s_waitcnt lgkmcnt(1)
	v_add_f32_e32 v85, v85, v87
	v_cvt_f32_i32_e32 v87, v80
	ds_bpermute_b32 v94, v34, v81
	ds_bpermute_b32 v93, v32, v85
	s_waitcnt lgkmcnt(2)
	v_add_f32_e32 v3, v3, v86
	ds_bpermute_b32 v86, v34, v87
	ds_bpermute_b32 v80, v37, v3
	s_waitcnt lgkmcnt(3)
	v_add_f32_e32 v81, v81, v94
	s_waitcnt lgkmcnt(2)
	v_add_f32_e32 v3, v85, v93
	ds_bpermute_b32 v85, v33, v81
	s_waitcnt lgkmcnt(2)
	v_add_f32_e32 v86, v87, v86
	v_cvt_f32_i32_e32 v87, v79
	ds_bpermute_b32 v93, v33, v86
	ds_bpermute_b32 v79, v37, v3
	s_waitcnt lgkmcnt(2)
	v_add_f32_e32 v3, v81, v85
	ds_bpermute_b32 v81, v34, v87
	ds_bpermute_b32 v85, v32, v3
	v_cvt_f32_i32_e32 v94, v78
	s_waitcnt lgkmcnt(3)
	v_add_f32_e32 v86, v86, v93
	ds_bpermute_b32 v93, v32, v86
	s_waitcnt lgkmcnt(2)
	v_add_f32_e32 v81, v87, v81
	ds_bpermute_b32 v87, v33, v81
	s_waitcnt lgkmcnt(2)
	v_add_f32_e32 v3, v3, v85
	ds_bpermute_b32 v85, v34, v94
	ds_bpermute_b32 v78, v37, v3
	s_waitcnt lgkmcnt(3)
	v_add_f32_e32 v3, v86, v93
	s_waitcnt lgkmcnt(2)
	v_add_f32_e32 v86, v81, v87
	ds_bpermute_b32 v87, v32, v86
	s_waitcnt lgkmcnt(2)
; __device__ __forceinline__ void peer_expert_phase(const Args& a, int layer, LAS unsigned char* lds, int G, int bid) {
;     ...
;         float pa[4], pb[4];
; #pragma unroll
;         for (int i = 0; i < 4; ++i) { pa[i] = 0.f; pb[i] = 0.f;
; #pragma unroll
;             for (int c = 0; c < 16; ++c) { float v = (float)pacc[i][c]; v += __shfl_xor(v, 1); v += __shfl_xor(v, 2); v += __shfl_xor(v, 4);
;                 const float t = __shfl(v, 8 * (lane & 7));
;                 if (c < 8) pa[i] = (g8 == c) ? t : pa[i]; else pb[i] = (g8 == c - 8) ? t : pb[i]; } }
;         float wa[4], wb[4], ssq[4], hgm[4] = {0.f, 0.f, 0.f, 0.f};
; #pragma unroll
;         for (int i = 0; i < 4; ++i) { int tok = tb + i * NGW; tok = tok < NTOK ? tok : tb;
;             const float rstd_t = 1.0f / sqrtf(wave_sum(((const float*)(ws + WS_SSP))[((size_t)layer * NTOK + tok) * 64 + lane]) * (1.0f / DM) + EPS);
	v_add_f32_e32 v85, v94, v85
	ds_bpermute_b32 v93, v33, v85
	v_cvt_f32_i32_e32 v94, v77
	ds_bpermute_b32 v81, v37, v3
	s_waitcnt lgkmcnt(2)
	v_add_f32_e32 v3, v86, v87
	ds_bpermute_b32 v77, v37, v3
	ds_bpermute_b32 v86, v34, v94
	s_waitcnt lgkmcnt(3)
	v_add_f32_e32 v85, v85, v93
	ds_bpermute_b32 v87, v32, v85
	ds_bpermute_b32 v93, v34, v76
	v_cvt_f32_i32_e32 v75, v75
	s_waitcnt lgkmcnt(2)
	v_add_f32_e32 v3, v94, v86
	ds_bpermute_b32 v86, v33, v3
	s_waitcnt lgkmcnt(2)
	v_add_f32_e32 v85, v85, v87
	s_waitcnt lgkmcnt(1)
	v_add_f32_e32 v87, v76, v93
	ds_bpermute_b32 v93, v33, v87
	ds_bpermute_b32 v76, v37, v85
	s_waitcnt lgkmcnt(2)
	v_add_f32_e32 v3, v3, v86
	ds_bpermute_b32 v85, v32, v3
	ds_bpermute_b32 v94, v34, v75
	s_waitcnt lgkmcnt(3)
	v_add_f32_e32 v86, v87, v93
	v_cvt_f32_i32_e32 v87, v74
	ds_bpermute_b32 v93, v32, v86
	s_waitcnt lgkmcnt(2)
	v_add_f32_e32 v3, v3, v85
	s_waitcnt lgkmcnt(1)
	v_add_f32_e32 v75, v75, v94
	ds_bpermute_b32 v85, v34, v87
	ds_bpermute_b32 v74, v37, v3
	s_waitcnt lgkmcnt(2)
	v_add_f32_e32 v3, v86, v93
	ds_bpermute_b32 v86, v33, v75
	v_cvt_f32_i32_e32 v94, v72
	s_waitcnt lgkmcnt(2)
	v_add_f32_e32 v85, v87, v85
	v_cvt_f32_i32_e32 v87, v73
	ds_bpermute_b32 v73, v37, v3
	s_waitcnt lgkmcnt(1)
	v_add_f32_e32 v3, v75, v86
	ds_bpermute_b32 v93, v33, v85
	ds_bpermute_b32 v75, v34, v87
	ds_bpermute_b32 v86, v32, v3
	v_cvt_f32_i32_e32 v69, v69
	v_cvt_f32_i32_e32 v68, v68
	s_waitcnt lgkmcnt(2)
	v_add_f32_e32 v85, v85, v93
	s_waitcnt lgkmcnt(1)
	v_add_f32_e32 v75, v87, v75
	ds_bpermute_b32 v87, v33, v75
	ds_bpermute_b32 v93, v32, v85
	s_waitcnt lgkmcnt(2)
	v_add_f32_e32 v3, v3, v86
	ds_bpermute_b32 v86, v34, v94
	ds_bpermute_b32 v72, v37, v3
	s_waitcnt lgkmcnt(3)
	v_add_f32_e32 v75, v75, v87
	s_waitcnt lgkmcnt(2)
	v_add_f32_e32 v3, v85, v93
	ds_bpermute_b32 v85, v32, v75
	v_cvt_f32_i32_e32 v93, v71
	s_waitcnt lgkmcnt(2)
	v_add_f32_e32 v86, v94, v86
	ds_bpermute_b32 v71, v37, v3
	ds_bpermute_b32 v87, v33, v86
	s_waitcnt lgkmcnt(2)
	v_add_f32_e32 v3, v75, v85
	ds_bpermute_b32 v85, v34, v93
	v_cvt_f32_i32_e32 v75, v70
	ds_bpermute_b32 v70, v37, v3
	s_waitcnt lgkmcnt(2)
	v_add_f32_e32 v86, v86, v87
	ds_bpermute_b32 v87, v32, v86
	s_waitcnt lgkmcnt(2)
	v_add_f32_e32 v3, v93, v85
	ds_bpermute_b32 v85, v33, v3
	ds_bpermute_b32 v94, v34, v75
	s_lshl_b64 s[60:61], s[26:27], 8
	s_waitcnt lgkmcnt(2)
	v_add_f32_e32 v86, v86, v87
	v_cvt_f32_i32_e32 v101, v66
	s_waitcnt lgkmcnt(1)
	v_add_f32_e32 v3, v3, v85
	s_waitcnt lgkmcnt(0)
	v_add_f32_e32 v87, v75, v94
	ds_bpermute_b32 v85, v32, v3
	ds_bpermute_b32 v93, v33, v87
	ds_bpermute_b32 v75, v37, v86
	ds_bpermute_b32 v94, v34, v69
	v_cvt_f32_i32_e32 v64, v64
	s_waitcnt lgkmcnt(3)
	v_add_f32_e32 v3, v3, v85
	s_waitcnt lgkmcnt(2)
	v_add_f32_e32 v87, v87, v93
	ds_bpermute_b32 v86, v37, v3
	ds_bpermute_b32 v3, v34, v68
	ds_bpermute_b32 v93, v32, v87
	s_waitcnt lgkmcnt(3)
	v_add_f32_e32 v69, v69, v94
	v_cvt_f32_i32_e32 v63, v63
	v_cvt_f32_i32_e32 v62, v62
	s_waitcnt lgkmcnt(1)
	v_add_f32_e32 v3, v68, v3
	s_waitcnt lgkmcnt(0)
	v_add_f32_e32 v85, v87, v93
	ds_bpermute_b32 v87, v33, v69
	ds_bpermute_b32 v68, v33, v3
	v_cvt_f32_i32_e32 v93, v67
	ds_bpermute_b32 v67, v37, v85
	v_cvt_f32_i32_e32 v61, v61
	s_waitcnt lgkmcnt(2)
	v_add_f32_e32 v87, v69, v87
	s_waitcnt lgkmcnt(1)
	v_add_f32_e32 v3, v3, v68
	v_lshl_add_u64 v[68:69], v[12:13], 0, s[60:61]
	global_load_dword v102, v[68:69], off
	ds_bpermute_b32 v85, v34, v93
	ds_bpermute_b32 v68, v34, v101
	ds_bpermute_b32 v94, v32, v87
	ds_bpermute_b32 v99, v32, v3
	v_cvt_f32_i32_e32 v60, v60
	s_waitcnt lgkmcnt(3)
	v_add_f32_e32 v85, v93, v85
	ds_bpermute_b32 v93, v33, v85
	s_waitcnt lgkmcnt(3)
	v_add_f32_e32 v68, v101, v68
	s_waitcnt lgkmcnt(2)
	v_add_f32_e32 v66, v87, v94
	ds_bpermute_b32 v87, v33, v68
	s_waitcnt lgkmcnt(2)
	v_add_f32_e32 v3, v3, v99
	s_waitcnt lgkmcnt(1)
	v_add_f32_e32 v69, v85, v93
	ds_bpermute_b32 v85, v32, v69
	v_cvt_f32_i32_e32 v93, v65
	ds_bpermute_b32 v65, v37, v3
	s_waitcnt lgkmcnt(2)
	v_add_f32_e32 v68, v68, v87
	ds_bpermute_b32 v94, v34, v64
	s_waitcnt lgkmcnt(2)
	v_add_f32_e32 v3, v69, v85
	ds_bpermute_b32 v69, v34, v93
	ds_bpermute_b32 v87, v32, v68
	ds_bpermute_b32 v85, v37, v3
	s_waitcnt lgkmcnt(3)
	v_add_f32_e32 v64, v64, v94
	ds_bpermute_b32 v94, v34, v63
	s_waitcnt lgkmcnt(3)
	v_add_f32_e32 v3, v93, v69
	ds_bpermute_b32 v93, v33, v3
	s_waitcnt lgkmcnt(3)
	v_add_f32_e32 v68, v68, v87
	ds_bpermute_b32 v87, v33, v64
	ds_bpermute_b32 v69, v37, v68
	s_waitcnt lgkmcnt(3)
	v_add_f32_e32 v63, v63, v94
	s_waitcnt lgkmcnt(2)
	v_add_f32_e32 v3, v3, v93
	ds_bpermute_b32 v68, v32, v3
	s_waitcnt lgkmcnt(2)
	v_add_f32_e32 v64, v64, v87
	ds_bpermute_b32 v87, v32, v64
	v_cvt_f32_i32_e32 v59, v59
	v_lshl_add_u64 v[120:121], v[14:15], 0, s[22:23]
	s_waitcnt lgkmcnt(1)
	v_add_f32_e32 v3, v3, v68
	ds_bpermute_b32 v68, v34, v62
	ds_bpermute_b32 v93, v37, v3
	s_waitcnt lgkmcnt(2)
	v_add_f32_e32 v3, v64, v87
	ds_bpermute_b32 v64, v33, v63
	ds_bpermute_b32 v99, v37, v3
	s_waitcnt lgkmcnt(3)
; __device__ __forceinline__ float gelu_tanh(float x) { const float u = 0.7978845608028654f * (x + 0.044715f * x * x * x); return 0.5f * x * (1.0f + tanhf(u)); }
; __device__ __forceinline__ void peer_expert_phase(const Args& a, int layer, LAS unsigned char* lds, int G, int bid) {
;     ...
;         float pa[4], pb[4];
; #pragma unroll
;         for (int i = 0; i < 4; ++i) { pa[i] = 0.f; pb[i] = 0.f;
; #pragma unroll
;             for (int c = 0; c < 16; ++c) { float v = (float)pacc[i][c]; v += __shfl_xor(v, 1); v += __shfl_xor(v, 2); v += __shfl_xor(v, 4);
;                 const float t = __shfl(v, 8 * (lane & 7));
;                 if (c < 8) pa[i] = (g8 == c) ? t : pa[i]; else pb[i] = (g8 == c - 8) ? t : pb[i]; } }
;         float wa[4], wb[4], ssq[4], hgm[4] = {0.f, 0.f, 0.f, 0.f};
; #pragma unroll
;         for (int i = 0; i < 4; ++i) { int tok = tb + i * NGW; tok = tok < NTOK ? tok : tb;
;             const float rstd_t = 1.0f / sqrtf(wave_sum(((const float*)(ws + WS_SSP))[((size_t)layer * NTOK + tok) * 64 + lane]) * (1.0f / DM) + EPS);
;             const float ga = GATE[(size_t)tok * 128 + lane], gb = GATE[(size_t)tok * 128 + 64 + lane];
;             const float rx = rstd_t * xs[i];
;             wa[i] = ga * gelu_tanh(pa[i] * SCU[ea[i]] * rx) * SCV[ea[i]]; wb[i] = gb * gelu_tanh(pb[i] * SCU[eb[i]] * rx) * SCV[eb[i]]; ssq[i] = 0.f; }
	v_add_f32_e32 v62, v62, v68
	ds_bpermute_b32 v68, v33, v62
	v_cvt_f32_i32_e32 v23, v23
	s_waitcnt lgkmcnt(2)
	v_add_f32_e32 v3, v63, v64
	ds_bpermute_b32 v63, v34, v61
	ds_bpermute_b32 v64, v32, v3
	s_waitcnt lgkmcnt(2)
	v_add_f32_e32 v62, v62, v68
	ds_bpermute_b32 v68, v32, v62
	v_cvt_f32_i32_e32 v21, v21
	s_waitcnt lgkmcnt(2)
	v_add_f32_e32 v61, v61, v63
	ds_bpermute_b32 v63, v33, v61
	s_waitcnt lgkmcnt(2)
	v_add_f32_e32 v3, v3, v64
	ds_bpermute_b32 v64, v34, v60
	ds_bpermute_b32 v94, v37, v3
	s_waitcnt lgkmcnt(3)
	v_add_f32_e32 v3, v62, v68
	s_waitcnt lgkmcnt(2)
	v_add_f32_e32 v62, v61, v63
	ds_bpermute_b32 v63, v32, v62
	s_waitcnt lgkmcnt(2)
	v_add_f32_e32 v60, v60, v64
	ds_bpermute_b32 v64, v33, v60
	ds_bpermute_b32 v61, v37, v3
	v_cvt_f32_i32_e32 v7, v7
	s_waitcnt lgkmcnt(2)
	v_add_f32_e32 v3, v62, v63
	ds_bpermute_b32 v63, v34, v59
	ds_bpermute_b32 v62, v37, v3
	s_waitcnt lgkmcnt(3)
	v_add_f32_e32 v3, v60, v64
	v_cvt_f32_i32_e32 v64, v19
	v_ashrrev_i32_e32 v19, 31, v18
	s_waitcnt lgkmcnt(1)
	v_add_f32_e32 v63, v59, v63
	v_lshl_add_u64 v[122:123], v[18:19], 2, s[36:37]
	global_load_dword v59, v[120:121], off
	global_load_dword v60, v[120:121], off offset:256
	s_nop 0
	global_load_dword v120, v[122:123], off
	ds_bpermute_b32 v101, v34, v64
	ds_bpermute_b32 v87, v33, v63
	ds_bpermute_b32 v68, v32, v3
	ds_bpermute_b32 v84, v37, v84
	ds_bpermute_b32 v66, v37, v66
	s_waitcnt lgkmcnt(4)
	v_add_f32_e32 v64, v64, v101
	ds_bpermute_b32 v101, v33, v64
	s_waitcnt lgkmcnt(4)
	v_add_f32_e32 v63, v63, v87
	s_waitcnt vmcnt(3)
	ds_bpermute_b32 v113, v29, v102
	ds_bpermute_b32 v87, v32, v63
	s_waitcnt lgkmcnt(5)
	v_add_f32_e32 v3, v3, v68
	s_waitcnt lgkmcnt(2)
	v_add_f32_e32 v64, v64, v101
	ds_bpermute_b32 v68, v37, v3
	s_waitcnt lgkmcnt(2)
	v_add_f32_e32 v101, v102, v113
	ds_bpermute_b32 v102, v30, v101
	s_waitcnt lgkmcnt(2)
	v_add_f32_e32 v3, v63, v87
	ds_bpermute_b32 v63, v34, v23
	ds_bpermute_b32 v87, v37, v3
	ds_bpermute_b32 v113, v32, v64
	s_waitcnt lgkmcnt(3)
	v_add_f32_e32 v3, v101, v102
	ds_bpermute_b32 v101, v31, v3
	s_waitcnt lgkmcnt(3)
	v_add_f32_e32 v23, v23, v63
	ds_bpermute_b32 v63, v33, v23
	s_waitcnt lgkmcnt(2)
	v_add_f32_e32 v64, v64, v113
	s_waitcnt lgkmcnt(1)
	v_add_f32_e32 v3, v3, v101
	ds_bpermute_b32 v102, v32, v3
	s_waitcnt lgkmcnt(1)
	v_add_f32_e32 v23, v23, v63
	ds_bpermute_b32 v63, v32, v23
	ds_bpermute_b32 v101, v37, v64
	ds_bpermute_b32 v64, v34, v21
	s_waitcnt lgkmcnt(3)
	v_add_f32_e32 v3, v3, v102
	s_waitcnt lgkmcnt(2)
	v_add_f32_e32 v23, v23, v63
	ds_bpermute_b32 v63, v33, v3
	s_waitcnt lgkmcnt(1)
	v_add_f32_e32 v21, v21, v64
	ds_bpermute_b32 v64, v33, v21
	ds_bpermute_b32 v102, v37, v23
	ds_bpermute_b32 v23, v34, v7
	s_waitcnt lgkmcnt(3)
	v_add_f32_e32 v3, v3, v63
	ds_bpermute_b32 v63, v34, v3
	s_waitcnt lgkmcnt(3)
	v_add_f32_e32 v21, v21, v64
	ds_bpermute_b32 v64, v32, v21
	s_waitcnt lgkmcnt(2)
	v_add_f32_e32 v7, v7, v23
	ds_bpermute_b32 v23, v33, v7
	s_waitcnt lgkmcnt(2)
	v_add_f32_e32 v3, v3, v63
	v_fmamk_f32 v3, v3, 0x39800000, v47
	v_mul_f32_e32 v63, 0x4f800000, v3
	v_cmp_gt_f32_e32 vcc, s72, v3
	s_waitcnt lgkmcnt(1)
	v_add_f32_e32 v21, v21, v64
	s_waitcnt lgkmcnt(0)
	v_add_f32_e32 v7, v7, v23
	v_cndmask_b32_e32 v3, v3, v63, vcc
	v_sqrt_f32_e32 v63, v3
	ds_bpermute_b32 v23, v32, v7
	v_add_u32_e32 v64, -1, v63
	v_fma_f32 v113, -v64, v63, v3
	v_cmp_ge_f32_e64 s[22:23], 0, v113
	v_add_u32_e32 v113, 1, v63
	s_waitcnt lgkmcnt(0)
	v_add_f32_e32 v7, v7, v23
	v_cndmask_b32_e64 v64, v63, v64, s[22:23]
	v_fma_f32 v63, -v113, v63, v3
	v_cmp_lt_f32_e64 s[22:23], 0, v63
	ds_bpermute_b32 v114, v37, v7
	s_nop 0
	v_cndmask_b32_e64 v63, v64, v113, s[22:23]
	v_mul_f32_e32 v64, 0x37800000, v63
	v_cndmask_b32_e32 v63, v63, v64, vcc
	v_cmp_class_f32_e32 vcc, v3, v48
	ds_bpermute_b32 v113, v37, v21
	s_nop 0
	v_cndmask_b32_e32 v3, v63, v3, vcc
	v_div_scale_f32 v63, s[22:23], v3, v3, 1.0
	v_rcp_f32_e32 v64, v63
	s_nop 0
	v_fma_f32 v7, -v63, v64, 1.0
	v_fmac_f32_e32 v64, v7, v64
	v_div_scale_f32 v7, vcc, 1.0, v3, 1.0
	v_mul_f32_e32 v21, v7, v64
	v_fma_f32 v23, -v63, v21, v7
	v_fmac_f32_e32 v21, v23, v64
	v_fma_f32 v7, -v63, v21, v7
	v_div_fmas_f32 v7, v7, v64, v21
	v_div_fixup_f32 v121, v7, v3, 1.0
	s_waitcnt vmcnt(0)
	v_pk_mul_f32 v[26:27], v[26:27], v[120:121]
	s_nop 0
	v_mul_f32_e32 v26, v26, v27
	v_mul_f32_e32 v3, 0x3d372713, v26
	v_mul_f32_e32 v3, v26, v3
	v_fma_f32 v3, v26, v3, v26
	v_mul_f32_e32 v63, 0x3f4c422a, v3
	v_cmp_nlt_f32_e64 s[22:23], |v63|, s73
	s_and_saveexec_b64 s[60:61], s[22:23]
	s_xor_b64 s[22:23], exec, s[60:61]
	s_cbranch_execz .LBB0_2270
	v_add_f32_e64 v3, |v63|, |v63|
	v_mul_f32_e32 v7, 0x3fb8aa3b, v3
	v_rndne_f32_e32 v21, v7
	v_sub_f32_e32 v23, v7, v21
	v_fma_f32 v7, v3, s74, -v7
	v_fmac_f32_e32 v7, 0x32a5705f, v3
	v_add_f32_e32 v7, v23, v7
	v_cvt_i32_f32_e32 v21, v21
	v_exp_f32_e32 v7, v7
	v_cmp_ngt_f32_e32 vcc, s75, v3
	v_ldexp_f32 v7, v7, v21
	s_nop 0
	v_cndmask_b32_e32 v7, 0, v7, vcc
	v_cmp_nlt_f32_e32 vcc, s76, v3
	s_nop 1
	v_cndmask_b32_e32 v3, v50, v7, vcc
	v_add_f32_e32 v3, 1.0, v3
	v_rcp_f32_e32 v3, v3
	s_nop 0
	v_fma_f32 v64, v3, -2.0, 1.0
